# PEER routing: sub-key tiles prefetched 8 pairs ahead instead of load-wait per tile; the two dependent gathers per slot issued together
# speedup vs baseline: 1.0073x; 1.0073x over previous
.LBB0_3014:
	s_or_b64 exec, exec, s[6:7]
	s_movk_i32 s17, 0x7f
	s_waitcnt lgkmcnt(0)
	v_bitop3_b32 v11, v6, s17, v6 bitop3:0xc
	v_add_f32_e32 v6, v31, v66
	v_bitop3_b32 v10, v7, s17, v7 bitop3:0xc
	v_ashrrev_i32_e32 v7, 31, v6
	v_or_b32_e32 v7, 0x80000000, v7
	s_movk_i32 s6, 0xff00
	v_bitop3_b32 v6, v7, s6, v6 bitop3:0x48
	s_movk_i32 s16, 0xff
	v_bitop3_b32 v31, v6, s16, v1 bitop3:0x36
	v_add_f32_e32 v6, v19, v25
	v_ashrrev_i32_e32 v7, 31, v6
	v_bitop3_b32 v6, v7, v6, s95 bitop3:0x36
	v_and_or_b32 v19, v6, s6, v58
	v_add_f32_e32 v6, v13, v16
	v_ashrrev_i32_e32 v7, 31, v6
	v_bitop3_b32 v6, v7, v6, s95 bitop3:0x36
	v_and_or_b32 v16, v6, s6, v63
	v_add_f32_e32 v6, v70, v73
	v_ashrrev_i32_e32 v7, 31, v6
	v_or_b32_e32 v7, 0x80000000, v7
	v_bitop3_b32 v6, v7, s6, v6 bitop3:0x48
	v_bitop3_b32 v25, v6, s16, v1 bitop3:0x36
	v_add_f32_e32 v6, v64, v67
	v_ashrrev_i32_e32 v7, 31, v6
	v_bitop3_b32 v6, v7, v6, s95 bitop3:0x36
	v_and_or_b32 v64, v6, s6, v58
	v_add_f32_e32 v6, v20, v27
	v_ashrrev_i32_e32 v7, 31, v6
	v_bitop3_b32 v6, v7, v6, s95 bitop3:0x36
	v_and_or_b32 v20, v6, s6, v63
	v_add_f32_e32 v6, v71, v74
	v_ashrrev_i32_e32 v7, 31, v6
	v_or_b32_e32 v7, 0x80000000, v7
	v_bitop3_b32 v6, v7, s6, v6 bitop3:0x48
	v_bitop3_b32 v13, v12, s17, v12 bitop3:0xc
	v_bitop3_b32 v12, v14, s17, v14 bitop3:0xc
	v_bitop3_b32 v14, v18, s17, v18 bitop3:0xc
	v_bitop3_b32 v18, v6, s16, v1 bitop3:0x36
	v_add_f32_e32 v6, v65, v68
	v_ashrrev_i32_e32 v7, 31, v6
	v_bitop3_b32 v6, v7, v6, s95 bitop3:0x36
	v_and_or_b32 v27, v6, s6, v58
	v_add_f32_e32 v6, v21, v29
	v_add_f32_e32 v29, v130, v131
	v_ashrrev_i32_e32 v65, 31, v29
	v_or_b32_e32 v65, 0x80000000, v65
	v_bitop3_b32 v29, v65, s6, v29 bitop3:0x48
	v_add_f32_e32 v65, v128, v129
	v_ashrrev_i32_e32 v66, 31, v65
	v_bitop3_b32 v65, v66, v65, s95 bitop3:0x36
	v_add_f32_e32 v66, v126, v127
	v_ashrrev_i32_e32 v67, 31, v66
	v_bitop3_b32 v66, v67, v66, s95 bitop3:0x36
	v_ashrrev_i32_e32 v7, 31, v6
	v_bitop3_b32 v29, v29, s16, v1 bitop3:0x36
	v_and_or_b32 v65, v65, s6, v58
	v_and_or_b32 v66, v66, s6, v63
	v_bitop3_b32 v6, v7, v6, s95 bitop3:0x36
	v_max_u32_e32 v67, v29, v65
	v_min_u32_e32 v29, v29, v65
	v_max_u32_e32 v65, v66, v134
	v_min_u32_e32 v66, v66, v134
	v_and_or_b32 v21, v6, s6, v63
	v_max_u32_e32 v68, v67, v65
	v_min_u32_e32 v65, v67, v65
	v_max_u32_e32 v67, v29, v66
	v_min_u32_e32 v29, v29, v66
	v_max_u32_e32 v66, v67, v65
	v_min_u32_e32 v65, v67, v65
	v_max_u32_e32 v67, v18, v27
	v_min_u32_e32 v18, v18, v27
	v_max_u32_e32 v27, v21, v8
	v_min_u32_e32 v8, v21, v8
	v_max_u32_e32 v21, v67, v27
	v_min_u32_e32 v27, v67, v27
	v_max_u32_e32 v67, v18, v8
	v_min_u32_e32 v8, v18, v8
	v_max_u32_e32 v18, v67, v27
	v_min_u32_e32 v27, v67, v27
	v_max_u32_e32 v67, v25, v64
	v_min_u32_e32 v25, v25, v64
	v_max_u32_e32 v64, v20, v17
	v_min_u32_e32 v17, v20, v17
	v_max_u32_e32 v20, v67, v64
	v_min_u32_e32 v64, v67, v64
	v_max_u32_e32 v67, v25, v17
	v_min_u32_e32 v17, v25, v17
	v_max_u32_e32 v25, v67, v64
	v_min_u32_e32 v64, v67, v64
	v_max_u32_e32 v67, v31, v19
	v_min_u32_e32 v19, v31, v19
	v_max_u32_e32 v31, v16, v9
	v_min_u32_e32 v9, v16, v9
	v_max_u32_e32 v16, v67, v31
	v_min_u32_e32 v31, v67, v31
	v_max_u32_e32 v67, v19, v9
	v_min_u32_e32 v9, v19, v9
	v_max_u32_e32 v19, v67, v31
	v_min_u32_e32 v31, v67, v31
	v_max_u32_dpp v67, v68, v68 quad_perm:[1,0,3,2] row_mask:0xf bank_mask:0xf bound_ctrl:1
	v_bitop3_b32 v7, v118, s17, v118 bitop3:0xc
	v_bitop3_b32 v6, v121, s17, v121 bitop3:0xc
	v_max_u32_dpp v67, v67, v67 quad_perm:[2,3,0,1] row_mask:0xf bank_mask:0xf bound_ctrl:1
	v_readlane_b32 s12, v254, 4
	v_readlane_b32 s13, v254, 5
	v_max_u32_dpp v67, v67, v67 row_half_mirror row_mask:0xf bank_mask:0xf bound_ctrl:1
	v_readlane_b32 s14, v254, 6
	v_readlane_b32 s15, v254, 7
	v_max_u32_dpp v67, v67, v67 row_mirror row_mask:0xf bank_mask:0xf bound_ctrl:1
	v_cmp_eq_u32_e32 vcc, v68, v67
	v_cndmask_b32_e64 v69, 0, v67, s[72:73]
	v_readlane_b32 s14, v251, 14
	v_cndmask_b32_e32 v67, v68, v66, vcc
	v_max_u32_dpp v68, v21, v21 quad_perm:[1,0,3,2] row_mask:0xf bank_mask:0xf bound_ctrl:1
	v_cndmask_b32_e32 v66, v66, v65, vcc
	v_cndmask_b32_e32 v65, v65, v29, vcc
	v_max_u32_dpp v68, v68, v68 quad_perm:[2,3,0,1] row_mask:0xf bank_mask:0xf bound_ctrl:1
	v_cndmask_b32_e64 v29, v29, 0, vcc
	v_readlane_b32 s15, v251, 15
	v_max_u32_dpp v68, v68, v68 row_half_mirror row_mask:0xf bank_mask:0xf bound_ctrl:1
	s_mov_b32 s18, 0x1f000000
	v_readlane_b32 s10, v251, 10
	v_max_u32_dpp v68, v68, v68 row_mirror row_mask:0xf bank_mask:0xf bound_ctrl:1
	v_cndmask_b32_e64 v70, 0, v68, s[72:73]
	v_cmp_eq_u32_e32 vcc, v21, v68
	v_max_u32_dpp v68, v20, v20 quad_perm:[1,0,3,2] row_mask:0xf bank_mask:0xf bound_ctrl:1
	v_readlane_b32 s11, v251, 11
	v_cndmask_b32_e32 v21, v21, v18, vcc
	v_max_u32_dpp v68, v68, v68 quad_perm:[2,3,0,1] row_mask:0xf bank_mask:0xf bound_ctrl:1
	v_cndmask_b32_e32 v18, v18, v27, vcc
	v_cndmask_b32_e32 v27, v27, v8, vcc
	v_max_u32_dpp v68, v68, v68 row_half_mirror row_mask:0xf bank_mask:0xf bound_ctrl:1
	v_cndmask_b32_e64 v8, v8, 0, vcc
	s_brev_b32 s19, 4
	v_max_u32_dpp v68, v68, v68 row_mirror row_mask:0xf bank_mask:0xf bound_ctrl:1
	v_cndmask_b32_e64 v71, 0, v68, s[72:73]
	v_cmp_eq_u32_e32 vcc, v20, v68
	v_max_u32_dpp v68, v16, v16 quad_perm:[1,0,3,2] row_mask:0xf bank_mask:0xf bound_ctrl:1
	v_bitop3_b32 v15, v15, s17, v15 bitop3:0xc
	v_cndmask_b32_e32 v20, v20, v25, vcc
	v_max_u32_dpp v68, v68, v68 quad_perm:[2,3,0,1] row_mask:0xf bank_mask:0xf bound_ctrl:1
	v_cndmask_b32_e32 v25, v25, v64, vcc
	v_cndmask_b32_e32 v64, v64, v17, vcc
	v_max_u32_dpp v68, v68, v68 row_half_mirror row_mask:0xf bank_mask:0xf bound_ctrl:1
	v_cndmask_b32_e64 v17, v17, 0, vcc
	s_add_i32 s1, s1, -1
	v_max_u32_dpp v68, v68, v68 row_mirror row_mask:0xf bank_mask:0xf bound_ctrl:1
	v_cndmask_b32_e64 v72, 0, v68, s[72:73]
	v_cmp_eq_u32_e32 vcc, v16, v68
	v_max_u32_dpp v68, v67, v67 quad_perm:[1,0,3,2] row_mask:0xf bank_mask:0xf bound_ctrl:1
	s_cmp_lg_u32 s1, 0
	v_cndmask_b32_e32 v16, v16, v19, vcc
	v_max_u32_dpp v68, v68, v68 quad_perm:[2,3,0,1] row_mask:0xf bank_mask:0xf bound_ctrl:1
	v_cndmask_b32_e32 v19, v19, v31, vcc
	v_cndmask_b32_e32 v31, v31, v9, vcc
	v_max_u32_dpp v68, v68, v68 row_half_mirror row_mask:0xf bank_mask:0xf bound_ctrl:1
	v_cndmask_b32_e64 v9, v9, 0, vcc
	s_nop 0
	v_max_u32_dpp v68, v68, v68 row_mirror row_mask:0xf bank_mask:0xf bound_ctrl:1
	v_cndmask_b32_e64 v69, v69, v68, s[42:43]
	v_cmp_eq_u32_e32 vcc, v67, v68
	v_max_u32_dpp v68, v21, v21 quad_perm:[1,0,3,2] row_mask:0xf bank_mask:0xf bound_ctrl:1
	s_nop 0
	v_cndmask_b32_e32 v67, v67, v66, vcc
	v_max_u32_dpp v68, v68, v68 quad_perm:[2,3,0,1] row_mask:0xf bank_mask:0xf bound_ctrl:1
	v_cndmask_b32_e32 v66, v66, v65, vcc
	v_cndmask_b32_e32 v65, v65, v29, vcc
	v_max_u32_dpp v68, v68, v68 row_half_mirror row_mask:0xf bank_mask:0xf bound_ctrl:1
	v_cndmask_b32_e64 v29, v29, 0, vcc
	s_nop 0
	v_max_u32_dpp v68, v68, v68 row_mirror row_mask:0xf bank_mask:0xf bound_ctrl:1
	v_cndmask_b32_e64 v70, v70, v68, s[42:43]
	v_cmp_eq_u32_e32 vcc, v21, v68
	v_max_u32_dpp v68, v20, v20 quad_perm:[1,0,3,2] row_mask:0xf bank_mask:0xf bound_ctrl:1
	s_nop 0
	v_cndmask_b32_e32 v21, v21, v18, vcc
	v_max_u32_dpp v68, v68, v68 quad_perm:[2,3,0,1] row_mask:0xf bank_mask:0xf bound_ctrl:1
	v_cndmask_b32_e32 v18, v18, v27, vcc
	v_cndmask_b32_e32 v27, v27, v8, vcc
	v_max_u32_dpp v68, v68, v68 row_half_mirror row_mask:0xf bank_mask:0xf bound_ctrl:1
	v_cndmask_b32_e64 v8, v8, 0, vcc
	s_nop 0
	v_max_u32_dpp v68, v68, v68 row_mirror row_mask:0xf bank_mask:0xf bound_ctrl:1
	v_cndmask_b32_e64 v71, v71, v68, s[42:43]
	v_cmp_eq_u32_e32 vcc, v20, v68
	v_max_u32_dpp v68, v16, v16 quad_perm:[1,0,3,2] row_mask:0xf bank_mask:0xf bound_ctrl:1
	s_nop 0
	v_cndmask_b32_e32 v20, v20, v25, vcc
	v_max_u32_dpp v68, v68, v68 quad_perm:[2,3,0,1] row_mask:0xf bank_mask:0xf bound_ctrl:1
	v_cndmask_b32_e32 v25, v25, v64, vcc
	v_cndmask_b32_e32 v64, v64, v17, vcc
	v_max_u32_dpp v68, v68, v68 row_half_mirror row_mask:0xf bank_mask:0xf bound_ctrl:1
	v_cndmask_b32_e64 v17, v17, 0, vcc
	s_nop 0
	v_max_u32_dpp v68, v68, v68 row_mirror row_mask:0xf bank_mask:0xf bound_ctrl:1
	v_cndmask_b32_e64 v72, v72, v68, s[42:43]
	v_cmp_eq_u32_e32 vcc, v16, v68
	v_max_u32_dpp v68, v67, v67 quad_perm:[1,0,3,2] row_mask:0xf bank_mask:0xf bound_ctrl:1
	s_nop 0
	v_cndmask_b32_e32 v16, v16, v19, vcc
	v_max_u32_dpp v68, v68, v68 quad_perm:[2,3,0,1] row_mask:0xf bank_mask:0xf bound_ctrl:1
	v_cndmask_b32_e32 v19, v19, v31, vcc
	v_cndmask_b32_e32 v31, v31, v9, vcc
	v_max_u32_dpp v68, v68, v68 row_half_mirror row_mask:0xf bank_mask:0xf bound_ctrl:1
	v_cndmask_b32_e64 v9, v9, 0, vcc
	s_nop 0
	v_max_u32_dpp v68, v68, v68 row_mirror row_mask:0xf bank_mask:0xf bound_ctrl:1
	v_cndmask_b32_e64 v69, v69, v68, s[44:45]
	v_cmp_eq_u32_e32 vcc, v67, v68
	v_max_u32_dpp v68, v21, v21 quad_perm:[1,0,3,2] row_mask:0xf bank_mask:0xf bound_ctrl:1
	s_nop 0
	v_cndmask_b32_e32 v67, v67, v66, vcc
	v_max_u32_dpp v68, v68, v68 quad_perm:[2,3,0,1] row_mask:0xf bank_mask:0xf bound_ctrl:1
	v_cndmask_b32_e32 v66, v66, v65, vcc
	v_cndmask_b32_e32 v65, v65, v29, vcc
	v_max_u32_dpp v68, v68, v68 row_half_mirror row_mask:0xf bank_mask:0xf bound_ctrl:1
	v_cndmask_b32_e64 v29, v29, 0, vcc
	s_nop 0
	v_max_u32_dpp v68, v68, v68 row_mirror row_mask:0xf bank_mask:0xf bound_ctrl:1
	v_cndmask_b32_e64 v70, v70, v68, s[44:45]
	v_cmp_eq_u32_e32 vcc, v21, v68
	v_max_u32_dpp v68, v20, v20 quad_perm:[1,0,3,2] row_mask:0xf bank_mask:0xf bound_ctrl:1
	s_nop 0
	v_cndmask_b32_e32 v21, v21, v18, vcc
	v_max_u32_dpp v68, v68, v68 quad_perm:[2,3,0,1] row_mask:0xf bank_mask:0xf bound_ctrl:1
	v_cndmask_b32_e32 v18, v18, v27, vcc
	v_cndmask_b32_e32 v27, v27, v8, vcc
	v_max_u32_dpp v68, v68, v68 row_half_mirror row_mask:0xf bank_mask:0xf bound_ctrl:1
	v_cndmask_b32_e64 v8, v8, 0, vcc
	s_nop 0
	v_max_u32_dpp v68, v68, v68 row_mirror row_mask:0xf bank_mask:0xf bound_ctrl:1
	v_cndmask_b32_e64 v71, v71, v68, s[44:45]
	v_cmp_eq_u32_e32 vcc, v20, v68
	v_max_u32_dpp v68, v16, v16 quad_perm:[1,0,3,2] row_mask:0xf bank_mask:0xf bound_ctrl:1
	s_nop 0
	v_cndmask_b32_e32 v20, v20, v25, vcc
	v_max_u32_dpp v68, v68, v68 quad_perm:[2,3,0,1] row_mask:0xf bank_mask:0xf bound_ctrl:1
	v_cndmask_b32_e32 v25, v25, v64, vcc
	v_cndmask_b32_e32 v64, v64, v17, vcc
	v_max_u32_dpp v68, v68, v68 row_half_mirror row_mask:0xf bank_mask:0xf bound_ctrl:1
	v_cndmask_b32_e64 v17, v17, 0, vcc
	s_nop 0
	v_max_u32_dpp v68, v68, v68 row_mirror row_mask:0xf bank_mask:0xf bound_ctrl:1
	v_cndmask_b32_e64 v72, v72, v68, s[44:45]
	v_cmp_eq_u32_e32 vcc, v16, v68
	v_max_u32_dpp v68, v67, v67 quad_perm:[1,0,3,2] row_mask:0xf bank_mask:0xf bound_ctrl:1
	s_nop 0
	v_cndmask_b32_e32 v16, v16, v19, vcc
	v_max_u32_dpp v68, v68, v68 quad_perm:[2,3,0,1] row_mask:0xf bank_mask:0xf bound_ctrl:1
	v_cndmask_b32_e32 v19, v19, v31, vcc
	v_cndmask_b32_e32 v31, v31, v9, vcc
	v_max_u32_dpp v68, v68, v68 row_half_mirror row_mask:0xf bank_mask:0xf bound_ctrl:1
	v_cndmask_b32_e64 v9, v9, 0, vcc
	s_nop 0
	v_max_u32_dpp v68, v68, v68 row_mirror row_mask:0xf bank_mask:0xf bound_ctrl:1
	v_cndmask_b32_e64 v69, v69, v68, s[46:47]
	v_cmp_eq_u32_e32 vcc, v67, v68
	v_max_u32_dpp v68, v21, v21 quad_perm:[1,0,3,2] row_mask:0xf bank_mask:0xf bound_ctrl:1
	s_nop 0
	v_cndmask_b32_e32 v67, v67, v66, vcc
	v_max_u32_dpp v68, v68, v68 quad_perm:[2,3,0,1] row_mask:0xf bank_mask:0xf bound_ctrl:1
	v_cndmask_b32_e32 v66, v66, v65, vcc
	v_cndmask_b32_e32 v65, v65, v29, vcc
	v_max_u32_dpp v68, v68, v68 row_half_mirror row_mask:0xf bank_mask:0xf bound_ctrl:1
	v_cndmask_b32_e64 v29, v29, 0, vcc
	s_nop 0
	v_max_u32_dpp v68, v68, v68 row_mirror row_mask:0xf bank_mask:0xf bound_ctrl:1
	v_cndmask_b32_e64 v70, v70, v68, s[46:47]
	v_cmp_eq_u32_e32 vcc, v21, v68
	v_max_u32_dpp v68, v20, v20 quad_perm:[1,0,3,2] row_mask:0xf bank_mask:0xf bound_ctrl:1
	s_nop 0
	v_cndmask_b32_e32 v21, v21, v18, vcc
	v_max_u32_dpp v68, v68, v68 quad_perm:[2,3,0,1] row_mask:0xf bank_mask:0xf bound_ctrl:1
	v_cndmask_b32_e32 v18, v18, v27, vcc
	v_cndmask_b32_e32 v27, v27, v8, vcc
	v_max_u32_dpp v68, v68, v68 row_half_mirror row_mask:0xf bank_mask:0xf bound_ctrl:1
	v_cndmask_b32_e64 v8, v8, 0, vcc
	s_nop 0
	v_max_u32_dpp v68, v68, v68 row_mirror row_mask:0xf bank_mask:0xf bound_ctrl:1
	v_cndmask_b32_e64 v71, v71, v68, s[46:47]
	v_cmp_eq_u32_e32 vcc, v20, v68
	v_max_u32_dpp v68, v16, v16 quad_perm:[1,0,3,2] row_mask:0xf bank_mask:0xf bound_ctrl:1
	s_nop 0
	v_cndmask_b32_e32 v20, v20, v25, vcc
	v_max_u32_dpp v68, v68, v68 quad_perm:[2,3,0,1] row_mask:0xf bank_mask:0xf bound_ctrl:1
	v_cndmask_b32_e32 v25, v25, v64, vcc
	v_cndmask_b32_e32 v64, v64, v17, vcc
	v_max_u32_dpp v68, v68, v68 row_half_mirror row_mask:0xf bank_mask:0xf bound_ctrl:1
	v_cndmask_b32_e64 v17, v17, 0, vcc
	s_nop 0
	v_max_u32_dpp v68, v68, v68 row_mirror row_mask:0xf bank_mask:0xf bound_ctrl:1
	v_cndmask_b32_e64 v72, v72, v68, s[46:47]
	v_cmp_eq_u32_e32 vcc, v16, v68
	v_max_u32_dpp v68, v67, v67 quad_perm:[1,0,3,2] row_mask:0xf bank_mask:0xf bound_ctrl:1
	s_nop 0
	v_cndmask_b32_e32 v16, v16, v19, vcc
	v_max_u32_dpp v68, v68, v68 quad_perm:[2,3,0,1] row_mask:0xf bank_mask:0xf bound_ctrl:1
	v_cndmask_b32_e32 v19, v19, v31, vcc
	v_cndmask_b32_e32 v31, v31, v9, vcc
	v_max_u32_dpp v68, v68, v68 row_half_mirror row_mask:0xf bank_mask:0xf bound_ctrl:1
	v_cndmask_b32_e64 v9, v9, 0, vcc
	s_nop 0
	v_max_u32_dpp v68, v68, v68 row_mirror row_mask:0xf bank_mask:0xf bound_ctrl:1
	v_cndmask_b32_e64 v69, v69, v68, s[48:49]
	v_cmp_eq_u32_e32 vcc, v67, v68
	v_max_u32_dpp v68, v21, v21 quad_perm:[1,0,3,2] row_mask:0xf bank_mask:0xf bound_ctrl:1
	s_nop 0
	v_cndmask_b32_e32 v67, v67, v66, vcc
	v_max_u32_dpp v68, v68, v68 quad_perm:[2,3,0,1] row_mask:0xf bank_mask:0xf bound_ctrl:1
	v_cndmask_b32_e32 v66, v66, v65, vcc
	v_cndmask_b32_e32 v65, v65, v29, vcc
	v_max_u32_dpp v68, v68, v68 row_half_mirror row_mask:0xf bank_mask:0xf bound_ctrl:1
	v_cndmask_b32_e64 v29, v29, 0, vcc
	s_nop 0
	v_max_u32_dpp v68, v68, v68 row_mirror row_mask:0xf bank_mask:0xf bound_ctrl:1
	v_cndmask_b32_e64 v70, v70, v68, s[48:49]
	v_cmp_eq_u32_e32 vcc, v21, v68
	v_max_u32_dpp v68, v20, v20 quad_perm:[1,0,3,2] row_mask:0xf bank_mask:0xf bound_ctrl:1
	s_nop 0
	v_cndmask_b32_e32 v21, v21, v18, vcc
	v_max_u32_dpp v68, v68, v68 quad_perm:[2,3,0,1] row_mask:0xf bank_mask:0xf bound_ctrl:1
	v_cndmask_b32_e32 v18, v18, v27, vcc
	v_cndmask_b32_e32 v27, v27, v8, vcc
	v_max_u32_dpp v68, v68, v68 row_half_mirror row_mask:0xf bank_mask:0xf bound_ctrl:1
	v_cndmask_b32_e64 v8, v8, 0, vcc
	s_nop 0
	v_max_u32_dpp v68, v68, v68 row_mirror row_mask:0xf bank_mask:0xf bound_ctrl:1
	v_cndmask_b32_e64 v71, v71, v68, s[48:49]
	v_cmp_eq_u32_e32 vcc, v20, v68
	v_max_u32_dpp v68, v16, v16 quad_perm:[1,0,3,2] row_mask:0xf bank_mask:0xf bound_ctrl:1
	s_nop 0
	v_cndmask_b32_e32 v20, v20, v25, vcc
	v_max_u32_dpp v68, v68, v68 quad_perm:[2,3,0,1] row_mask:0xf bank_mask:0xf bound_ctrl:1
	v_cndmask_b32_e32 v25, v25, v64, vcc
	v_cndmask_b32_e32 v64, v64, v17, vcc
	v_max_u32_dpp v68, v68, v68 row_half_mirror row_mask:0xf bank_mask:0xf bound_ctrl:1
	v_cndmask_b32_e64 v17, v17, 0, vcc
	s_nop 0
	v_max_u32_dpp v68, v68, v68 row_mirror row_mask:0xf bank_mask:0xf bound_ctrl:1
	v_cndmask_b32_e64 v72, v72, v68, s[48:49]
	v_cmp_eq_u32_e32 vcc, v16, v68
	v_max_u32_dpp v68, v67, v67 quad_perm:[1,0,3,2] row_mask:0xf bank_mask:0xf bound_ctrl:1
	s_nop 0
	v_cndmask_b32_e32 v16, v16, v19, vcc
	v_max_u32_dpp v68, v68, v68 quad_perm:[2,3,0,1] row_mask:0xf bank_mask:0xf bound_ctrl:1
	v_cndmask_b32_e32 v19, v19, v31, vcc
	v_cndmask_b32_e32 v31, v31, v9, vcc
	v_max_u32_dpp v68, v68, v68 row_half_mirror row_mask:0xf bank_mask:0xf bound_ctrl:1
	v_cndmask_b32_e64 v9, v9, 0, vcc
	s_nop 0
	v_max_u32_dpp v68, v68, v68 row_mirror row_mask:0xf bank_mask:0xf bound_ctrl:1
	v_cndmask_b32_e64 v69, v69, v68, s[50:51]
	v_cmp_eq_u32_e32 vcc, v67, v68
	v_max_u32_dpp v68, v21, v21 quad_perm:[1,0,3,2] row_mask:0xf bank_mask:0xf bound_ctrl:1
	s_nop 0
	v_cndmask_b32_e32 v67, v67, v66, vcc
	v_max_u32_dpp v68, v68, v68 quad_perm:[2,3,0,1] row_mask:0xf bank_mask:0xf bound_ctrl:1
	v_cndmask_b32_e32 v66, v66, v65, vcc
	v_cndmask_b32_e32 v65, v65, v29, vcc
	v_max_u32_dpp v68, v68, v68 row_half_mirror row_mask:0xf bank_mask:0xf bound_ctrl:1
	v_cndmask_b32_e64 v29, v29, 0, vcc
	s_nop 0
	v_max_u32_dpp v68, v68, v68 row_mirror row_mask:0xf bank_mask:0xf bound_ctrl:1
	v_cndmask_b32_e64 v70, v70, v68, s[50:51]
	v_cmp_eq_u32_e32 vcc, v21, v68
	v_max_u32_dpp v68, v20, v20 quad_perm:[1,0,3,2] row_mask:0xf bank_mask:0xf bound_ctrl:1
	s_nop 0
	v_cndmask_b32_e32 v21, v21, v18, vcc
	v_max_u32_dpp v68, v68, v68 quad_perm:[2,3,0,1] row_mask:0xf bank_mask:0xf bound_ctrl:1
	v_cndmask_b32_e32 v18, v18, v27, vcc
	v_cndmask_b32_e32 v27, v27, v8, vcc
	v_max_u32_dpp v68, v68, v68 row_half_mirror row_mask:0xf bank_mask:0xf bound_ctrl:1
	v_cndmask_b32_e64 v8, v8, 0, vcc
	s_nop 0
	v_max_u32_dpp v68, v68, v68 row_mirror row_mask:0xf bank_mask:0xf bound_ctrl:1
	v_cndmask_b32_e64 v71, v71, v68, s[50:51]
	v_cmp_eq_u32_e32 vcc, v20, v68
	v_max_u32_dpp v68, v16, v16 quad_perm:[1,0,3,2] row_mask:0xf bank_mask:0xf bound_ctrl:1
	s_nop 0
	v_cndmask_b32_e32 v20, v20, v25, vcc
	v_max_u32_dpp v68, v68, v68 quad_perm:[2,3,0,1] row_mask:0xf bank_mask:0xf bound_ctrl:1
	v_cndmask_b32_e32 v25, v25, v64, vcc
	v_cndmask_b32_e32 v64, v64, v17, vcc
	v_max_u32_dpp v68, v68, v68 row_half_mirror row_mask:0xf bank_mask:0xf bound_ctrl:1
	v_cndmask_b32_e64 v17, v17, 0, vcc
	s_nop 0
	v_max_u32_dpp v68, v68, v68 row_mirror row_mask:0xf bank_mask:0xf bound_ctrl:1
	v_cndmask_b32_e64 v72, v72, v68, s[50:51]
	v_cmp_eq_u32_e32 vcc, v16, v68
	v_max_u32_dpp v68, v67, v67 quad_perm:[1,0,3,2] row_mask:0xf bank_mask:0xf bound_ctrl:1
	s_nop 0
	v_cndmask_b32_e32 v16, v16, v19, vcc
	v_max_u32_dpp v68, v68, v68 quad_perm:[2,3,0,1] row_mask:0xf bank_mask:0xf bound_ctrl:1
	v_cndmask_b32_e32 v19, v19, v31, vcc
	v_cndmask_b32_e32 v31, v31, v9, vcc
	v_max_u32_dpp v68, v68, v68 row_half_mirror row_mask:0xf bank_mask:0xf bound_ctrl:1
	v_cndmask_b32_e64 v9, v9, 0, vcc
	s_nop 0
	v_max_u32_dpp v68, v68, v68 row_mirror row_mask:0xf bank_mask:0xf bound_ctrl:1
	v_cndmask_b32_e64 v69, v69, v68, s[52:53]
	v_cmp_eq_u32_e32 vcc, v67, v68
	v_max_u32_dpp v68, v21, v21 quad_perm:[1,0,3,2] row_mask:0xf bank_mask:0xf bound_ctrl:1
	s_nop 0
	v_cndmask_b32_e32 v67, v67, v66, vcc
	v_max_u32_dpp v68, v68, v68 quad_perm:[2,3,0,1] row_mask:0xf bank_mask:0xf bound_ctrl:1
	v_cndmask_b32_e32 v66, v66, v65, vcc
	v_cndmask_b32_e32 v65, v65, v29, vcc
	v_max_u32_dpp v68, v68, v68 row_half_mirror row_mask:0xf bank_mask:0xf bound_ctrl:1
	v_cndmask_b32_e64 v29, v29, 0, vcc
	s_nop 0
	v_max_u32_dpp v68, v68, v68 row_mirror row_mask:0xf bank_mask:0xf bound_ctrl:1
	v_cndmask_b32_e64 v70, v70, v68, s[52:53]
	v_cmp_eq_u32_e32 vcc, v21, v68
	v_max_u32_dpp v68, v20, v20 quad_perm:[1,0,3,2] row_mask:0xf bank_mask:0xf bound_ctrl:1
	s_nop 0
	v_cndmask_b32_e32 v21, v21, v18, vcc
	v_max_u32_dpp v68, v68, v68 quad_perm:[2,3,0,1] row_mask:0xf bank_mask:0xf bound_ctrl:1
	v_cndmask_b32_e32 v18, v18, v27, vcc
	v_cndmask_b32_e32 v27, v27, v8, vcc
	v_max_u32_dpp v68, v68, v68 row_half_mirror row_mask:0xf bank_mask:0xf bound_ctrl:1
	v_cndmask_b32_e64 v8, v8, 0, vcc
	s_nop 0
	v_max_u32_dpp v68, v68, v68 row_mirror row_mask:0xf bank_mask:0xf bound_ctrl:1
	v_cndmask_b32_e64 v71, v71, v68, s[52:53]
	v_cmp_eq_u32_e32 vcc, v20, v68
	v_max_u32_dpp v68, v16, v16 quad_perm:[1,0,3,2] row_mask:0xf bank_mask:0xf bound_ctrl:1
	s_nop 0
	v_cndmask_b32_e32 v20, v20, v25, vcc
	v_max_u32_dpp v68, v68, v68 quad_perm:[2,3,0,1] row_mask:0xf bank_mask:0xf bound_ctrl:1
	v_cndmask_b32_e32 v25, v25, v64, vcc
	v_cndmask_b32_e32 v64, v64, v17, vcc
	v_max_u32_dpp v68, v68, v68 row_half_mirror row_mask:0xf bank_mask:0xf bound_ctrl:1
	v_cndmask_b32_e64 v17, v17, 0, vcc
	s_nop 0
	v_max_u32_dpp v68, v68, v68 row_mirror row_mask:0xf bank_mask:0xf bound_ctrl:1
	v_cndmask_b32_e64 v72, v72, v68, s[52:53]
	v_cmp_eq_u32_e32 vcc, v16, v68
	v_max_u32_dpp v68, v67, v67 quad_perm:[1,0,3,2] row_mask:0xf bank_mask:0xf bound_ctrl:1
	s_nop 0
	v_cndmask_b32_e32 v16, v16, v19, vcc
	v_max_u32_dpp v68, v68, v68 quad_perm:[2,3,0,1] row_mask:0xf bank_mask:0xf bound_ctrl:1
	v_cndmask_b32_e32 v19, v19, v31, vcc
	v_cndmask_b32_e32 v31, v31, v9, vcc
	v_max_u32_dpp v68, v68, v68 row_half_mirror row_mask:0xf bank_mask:0xf bound_ctrl:1
	v_cndmask_b32_e64 v9, v9, 0, vcc
	s_nop 0
	v_max_u32_dpp v68, v68, v68 row_mirror row_mask:0xf bank_mask:0xf bound_ctrl:1
	v_cndmask_b32_e64 v69, v69, v68, s[54:55]
	v_cmp_eq_u32_e32 vcc, v67, v68
	v_max_u32_dpp v68, v21, v21 quad_perm:[1,0,3,2] row_mask:0xf bank_mask:0xf bound_ctrl:1
	s_nop 0
	v_cndmask_b32_e32 v67, v67, v66, vcc
	v_max_u32_dpp v68, v68, v68 quad_perm:[2,3,0,1] row_mask:0xf bank_mask:0xf bound_ctrl:1
	v_cndmask_b32_e32 v66, v66, v65, vcc
	v_cndmask_b32_e32 v65, v65, v29, vcc
	v_max_u32_dpp v68, v68, v68 row_half_mirror row_mask:0xf bank_mask:0xf bound_ctrl:1
	v_cndmask_b32_e64 v29, v29, 0, vcc
	s_nop 0
	v_max_u32_dpp v68, v68, v68 row_mirror row_mask:0xf bank_mask:0xf bound_ctrl:1
	v_cndmask_b32_e64 v70, v70, v68, s[54:55]
	v_cmp_eq_u32_e32 vcc, v21, v68
	v_max_u32_dpp v68, v20, v20 quad_perm:[1,0,3,2] row_mask:0xf bank_mask:0xf bound_ctrl:1
	s_nop 0
	v_cndmask_b32_e32 v21, v21, v18, vcc
	v_max_u32_dpp v68, v68, v68 quad_perm:[2,3,0,1] row_mask:0xf bank_mask:0xf bound_ctrl:1
	v_cndmask_b32_e32 v18, v18, v27, vcc
	v_cndmask_b32_e32 v27, v27, v8, vcc
	v_max_u32_dpp v68, v68, v68 row_half_mirror row_mask:0xf bank_mask:0xf bound_ctrl:1
	v_cndmask_b32_e64 v8, v8, 0, vcc
	s_nop 0
	v_max_u32_dpp v68, v68, v68 row_mirror row_mask:0xf bank_mask:0xf bound_ctrl:1
	v_cndmask_b32_e64 v71, v71, v68, s[54:55]
	v_cmp_eq_u32_e32 vcc, v20, v68
	v_max_u32_dpp v68, v16, v16 quad_perm:[1,0,3,2] row_mask:0xf bank_mask:0xf bound_ctrl:1
	s_nop 0
	v_cndmask_b32_e32 v20, v20, v25, vcc
	v_max_u32_dpp v68, v68, v68 quad_perm:[2,3,0,1] row_mask:0xf bank_mask:0xf bound_ctrl:1
	v_cndmask_b32_e32 v25, v25, v64, vcc
	v_cndmask_b32_e32 v64, v64, v17, vcc
	v_max_u32_dpp v68, v68, v68 row_half_mirror row_mask:0xf bank_mask:0xf bound_ctrl:1
	v_cndmask_b32_e64 v17, v17, 0, vcc
	s_nop 0
	v_max_u32_dpp v68, v68, v68 row_mirror row_mask:0xf bank_mask:0xf bound_ctrl:1
	v_cndmask_b32_e64 v72, v72, v68, s[54:55]
	v_cmp_eq_u32_e32 vcc, v16, v68
	v_max_u32_dpp v68, v67, v67 quad_perm:[1,0,3,2] row_mask:0xf bank_mask:0xf bound_ctrl:1
	s_nop 0
	v_cndmask_b32_e32 v16, v16, v19, vcc
	v_max_u32_dpp v68, v68, v68 quad_perm:[2,3,0,1] row_mask:0xf bank_mask:0xf bound_ctrl:1
	v_cndmask_b32_e32 v19, v19, v31, vcc
	v_cndmask_b32_e32 v31, v31, v9, vcc
	v_max_u32_dpp v68, v68, v68 row_half_mirror row_mask:0xf bank_mask:0xf bound_ctrl:1
	v_cndmask_b32_e64 v9, v9, 0, vcc
	s_nop 0
	v_max_u32_dpp v68, v68, v68 row_mirror row_mask:0xf bank_mask:0xf bound_ctrl:1
	v_cndmask_b32_e64 v69, v69, v68, s[56:57]
	v_cmp_eq_u32_e32 vcc, v67, v68
	v_max_u32_dpp v68, v21, v21 quad_perm:[1,0,3,2] row_mask:0xf bank_mask:0xf bound_ctrl:1
	s_nop 0
	v_cndmask_b32_e32 v67, v67, v66, vcc
	v_max_u32_dpp v68, v68, v68 quad_perm:[2,3,0,1] row_mask:0xf bank_mask:0xf bound_ctrl:1
	v_cndmask_b32_e32 v66, v66, v65, vcc
	v_cndmask_b32_e32 v65, v65, v29, vcc
	v_max_u32_dpp v68, v68, v68 row_half_mirror row_mask:0xf bank_mask:0xf bound_ctrl:1
	v_cndmask_b32_e64 v29, v29, 0, vcc
	s_nop 0
	v_max_u32_dpp v68, v68, v68 row_mirror row_mask:0xf bank_mask:0xf bound_ctrl:1
	v_cndmask_b32_e64 v70, v70, v68, s[56:57]
	v_cmp_eq_u32_e32 vcc, v21, v68
	v_max_u32_dpp v68, v20, v20 quad_perm:[1,0,3,2] row_mask:0xf bank_mask:0xf bound_ctrl:1
	s_nop 0
	v_cndmask_b32_e32 v21, v21, v18, vcc
	v_max_u32_dpp v68, v68, v68 quad_perm:[2,3,0,1] row_mask:0xf bank_mask:0xf bound_ctrl:1
	v_cndmask_b32_e32 v18, v18, v27, vcc
	v_cndmask_b32_e32 v27, v27, v8, vcc
	v_max_u32_dpp v68, v68, v68 row_half_mirror row_mask:0xf bank_mask:0xf bound_ctrl:1
	v_cndmask_b32_e64 v8, v8, 0, vcc
	s_nop 0
	v_max_u32_dpp v68, v68, v68 row_mirror row_mask:0xf bank_mask:0xf bound_ctrl:1
	v_cndmask_b32_e64 v71, v71, v68, s[56:57]
	v_cmp_eq_u32_e32 vcc, v20, v68
	v_max_u32_dpp v68, v16, v16 quad_perm:[1,0,3,2] row_mask:0xf bank_mask:0xf bound_ctrl:1
	s_nop 0
	v_cndmask_b32_e32 v20, v20, v25, vcc
	v_max_u32_dpp v68, v68, v68 quad_perm:[2,3,0,1] row_mask:0xf bank_mask:0xf bound_ctrl:1
	v_cndmask_b32_e32 v25, v25, v64, vcc
	v_cndmask_b32_e32 v64, v64, v17, vcc
	v_max_u32_dpp v68, v68, v68 row_half_mirror row_mask:0xf bank_mask:0xf bound_ctrl:1
	v_cndmask_b32_e64 v17, v17, 0, vcc
	s_nop 0
	v_max_u32_dpp v68, v68, v68 row_mirror row_mask:0xf bank_mask:0xf bound_ctrl:1
	v_cndmask_b32_e64 v72, v72, v68, s[56:57]
	v_cmp_eq_u32_e32 vcc, v16, v68
	v_max_u32_dpp v68, v67, v67 quad_perm:[1,0,3,2] row_mask:0xf bank_mask:0xf bound_ctrl:1
	s_nop 0
	v_cndmask_b32_e32 v16, v16, v19, vcc
	v_max_u32_dpp v68, v68, v68 quad_perm:[2,3,0,1] row_mask:0xf bank_mask:0xf bound_ctrl:1
	v_cndmask_b32_e32 v19, v19, v31, vcc
	v_cndmask_b32_e32 v31, v31, v9, vcc
	v_max_u32_dpp v68, v68, v68 row_half_mirror row_mask:0xf bank_mask:0xf bound_ctrl:1
	v_cndmask_b32_e64 v9, v9, 0, vcc
	s_nop 0
	v_max_u32_dpp v68, v68, v68 row_mirror row_mask:0xf bank_mask:0xf bound_ctrl:1
	v_cndmask_b32_e64 v69, v69, v68, s[58:59]
	v_cmp_eq_u32_e32 vcc, v67, v68
	v_max_u32_dpp v68, v21, v21 quad_perm:[1,0,3,2] row_mask:0xf bank_mask:0xf bound_ctrl:1
	s_nop 0
	v_cndmask_b32_e32 v67, v67, v66, vcc
	v_max_u32_dpp v68, v68, v68 quad_perm:[2,3,0,1] row_mask:0xf bank_mask:0xf bound_ctrl:1
	v_cndmask_b32_e32 v66, v66, v65, vcc
	v_cndmask_b32_e32 v65, v65, v29, vcc
	v_max_u32_dpp v68, v68, v68 row_half_mirror row_mask:0xf bank_mask:0xf bound_ctrl:1
	v_cndmask_b32_e64 v29, v29, 0, vcc
	s_nop 0
	v_max_u32_dpp v68, v68, v68 row_mirror row_mask:0xf bank_mask:0xf bound_ctrl:1
	v_cndmask_b32_e64 v70, v70, v68, s[58:59]
	v_cmp_eq_u32_e32 vcc, v21, v68
	v_max_u32_dpp v68, v20, v20 quad_perm:[1,0,3,2] row_mask:0xf bank_mask:0xf bound_ctrl:1
	s_nop 0
	v_cndmask_b32_e32 v21, v21, v18, vcc
	v_max_u32_dpp v68, v68, v68 quad_perm:[2,3,0,1] row_mask:0xf bank_mask:0xf bound_ctrl:1
	v_cndmask_b32_e32 v18, v18, v27, vcc
	v_cndmask_b32_e32 v27, v27, v8, vcc
	v_max_u32_dpp v68, v68, v68 row_half_mirror row_mask:0xf bank_mask:0xf bound_ctrl:1
	v_cndmask_b32_e64 v8, v8, 0, vcc
	s_nop 0
	v_max_u32_dpp v68, v68, v68 row_mirror row_mask:0xf bank_mask:0xf bound_ctrl:1
	v_cndmask_b32_e64 v71, v71, v68, s[58:59]
	v_cmp_eq_u32_e32 vcc, v20, v68
	v_max_u32_dpp v68, v16, v16 quad_perm:[1,0,3,2] row_mask:0xf bank_mask:0xf bound_ctrl:1
	s_nop 0
	v_cndmask_b32_e32 v20, v20, v25, vcc
	v_max_u32_dpp v68, v68, v68 quad_perm:[2,3,0,1] row_mask:0xf bank_mask:0xf bound_ctrl:1
	v_cndmask_b32_e32 v25, v25, v64, vcc
	v_cndmask_b32_e32 v64, v64, v17, vcc
	v_max_u32_dpp v68, v68, v68 row_half_mirror row_mask:0xf bank_mask:0xf bound_ctrl:1
	v_cndmask_b32_e64 v17, v17, 0, vcc
	s_nop 0
	v_max_u32_dpp v68, v68, v68 row_mirror row_mask:0xf bank_mask:0xf bound_ctrl:1
	v_cndmask_b32_e64 v72, v72, v68, s[58:59]
	v_cmp_eq_u32_e32 vcc, v16, v68
	v_max_u32_dpp v68, v67, v67 quad_perm:[1,0,3,2] row_mask:0xf bank_mask:0xf bound_ctrl:1
	s_nop 0
	v_cndmask_b32_e32 v16, v16, v19, vcc
	v_max_u32_dpp v68, v68, v68 quad_perm:[2,3,0,1] row_mask:0xf bank_mask:0xf bound_ctrl:1
	v_cndmask_b32_e32 v19, v19, v31, vcc
	v_cndmask_b32_e32 v31, v31, v9, vcc
	v_max_u32_dpp v68, v68, v68 row_half_mirror row_mask:0xf bank_mask:0xf bound_ctrl:1
	v_cndmask_b32_e64 v9, v9, 0, vcc
	s_nop 0
	v_max_u32_dpp v68, v68, v68 row_mirror row_mask:0xf bank_mask:0xf bound_ctrl:1
	v_cndmask_b32_e64 v69, v69, v68, s[60:61]
	v_cmp_eq_u32_e32 vcc, v67, v68
	v_max_u32_dpp v68, v21, v21 quad_perm:[1,0,3,2] row_mask:0xf bank_mask:0xf bound_ctrl:1
	s_nop 0
	v_cndmask_b32_e32 v67, v67, v66, vcc
	v_max_u32_dpp v68, v68, v68 quad_perm:[2,3,0,1] row_mask:0xf bank_mask:0xf bound_ctrl:1
	v_cndmask_b32_e32 v66, v66, v65, vcc
	v_cndmask_b32_e32 v65, v65, v29, vcc
	v_max_u32_dpp v68, v68, v68 row_half_mirror row_mask:0xf bank_mask:0xf bound_ctrl:1
	v_cndmask_b32_e64 v29, v29, 0, vcc
	s_nop 0
	v_max_u32_dpp v68, v68, v68 row_mirror row_mask:0xf bank_mask:0xf bound_ctrl:1
	v_cndmask_b32_e64 v70, v70, v68, s[60:61]
	v_cmp_eq_u32_e32 vcc, v21, v68
	v_max_u32_dpp v68, v20, v20 quad_perm:[1,0,3,2] row_mask:0xf bank_mask:0xf bound_ctrl:1
	s_nop 0
	v_cndmask_b32_e32 v21, v21, v18, vcc
	v_max_u32_dpp v68, v68, v68 quad_perm:[2,3,0,1] row_mask:0xf bank_mask:0xf bound_ctrl:1
	v_cndmask_b32_e32 v18, v18, v27, vcc
	v_cndmask_b32_e32 v27, v27, v8, vcc
	v_max_u32_dpp v68, v68, v68 row_half_mirror row_mask:0xf bank_mask:0xf bound_ctrl:1
	v_cndmask_b32_e64 v8, v8, 0, vcc
	s_nop 0
	v_max_u32_dpp v68, v68, v68 row_mirror row_mask:0xf bank_mask:0xf bound_ctrl:1
	v_cndmask_b32_e64 v71, v71, v68, s[60:61]
	v_cmp_eq_u32_e32 vcc, v20, v68
	v_max_u32_dpp v68, v16, v16 quad_perm:[1,0,3,2] row_mask:0xf bank_mask:0xf bound_ctrl:1
	s_nop 0
	v_cndmask_b32_e32 v20, v20, v25, vcc
	v_max_u32_dpp v68, v68, v68 quad_perm:[2,3,0,1] row_mask:0xf bank_mask:0xf bound_ctrl:1
	v_cndmask_b32_e32 v25, v25, v64, vcc
	v_cndmask_b32_e32 v64, v64, v17, vcc
	v_max_u32_dpp v68, v68, v68 row_half_mirror row_mask:0xf bank_mask:0xf bound_ctrl:1
	v_cndmask_b32_e64 v17, v17, 0, vcc
	s_nop 0
	v_max_u32_dpp v68, v68, v68 row_mirror row_mask:0xf bank_mask:0xf bound_ctrl:1
	v_cndmask_b32_e64 v72, v72, v68, s[60:61]
	v_cmp_eq_u32_e32 vcc, v16, v68
	v_max_u32_dpp v68, v67, v67 quad_perm:[1,0,3,2] row_mask:0xf bank_mask:0xf bound_ctrl:1
	s_nop 0
	v_cndmask_b32_e32 v16, v16, v19, vcc
	v_max_u32_dpp v68, v68, v68 quad_perm:[2,3,0,1] row_mask:0xf bank_mask:0xf bound_ctrl:1
	v_cndmask_b32_e32 v19, v19, v31, vcc
	v_cndmask_b32_e32 v31, v31, v9, vcc
	v_max_u32_dpp v68, v68, v68 row_half_mirror row_mask:0xf bank_mask:0xf bound_ctrl:1
	v_cndmask_b32_e64 v9, v9, 0, vcc
	s_nop 0
	v_max_u32_dpp v68, v68, v68 row_mirror row_mask:0xf bank_mask:0xf bound_ctrl:1
	v_cndmask_b32_e64 v69, v69, v68, s[62:63]
	v_cmp_eq_u32_e32 vcc, v67, v68
	v_max_u32_dpp v68, v21, v21 quad_perm:[1,0,3,2] row_mask:0xf bank_mask:0xf bound_ctrl:1
	s_nop 0
	v_cndmask_b32_e32 v67, v67, v66, vcc
	v_max_u32_dpp v68, v68, v68 quad_perm:[2,3,0,1] row_mask:0xf bank_mask:0xf bound_ctrl:1
	v_cndmask_b32_e32 v66, v66, v65, vcc
	v_cndmask_b32_e32 v65, v65, v29, vcc
	v_max_u32_dpp v68, v68, v68 row_half_mirror row_mask:0xf bank_mask:0xf bound_ctrl:1
	v_cndmask_b32_e64 v29, v29, 0, vcc
	s_nop 0
	v_max_u32_dpp v68, v68, v68 row_mirror row_mask:0xf bank_mask:0xf bound_ctrl:1
	v_cndmask_b32_e64 v70, v70, v68, s[62:63]
	v_cmp_eq_u32_e32 vcc, v21, v68
	v_max_u32_dpp v68, v20, v20 quad_perm:[1,0,3,2] row_mask:0xf bank_mask:0xf bound_ctrl:1
	s_nop 0
	v_cndmask_b32_e32 v21, v21, v18, vcc
	v_max_u32_dpp v68, v68, v68 quad_perm:[2,3,0,1] row_mask:0xf bank_mask:0xf bound_ctrl:1
	v_cndmask_b32_e32 v18, v18, v27, vcc
	v_cndmask_b32_e32 v27, v27, v8, vcc
	v_max_u32_dpp v68, v68, v68 row_half_mirror row_mask:0xf bank_mask:0xf bound_ctrl:1
	v_cndmask_b32_e64 v8, v8, 0, vcc
	s_nop 0
	v_max_u32_dpp v68, v68, v68 row_mirror row_mask:0xf bank_mask:0xf bound_ctrl:1
	v_cndmask_b32_e64 v71, v71, v68, s[62:63]
	v_cmp_eq_u32_e32 vcc, v20, v68
	v_max_u32_dpp v68, v16, v16 quad_perm:[1,0,3,2] row_mask:0xf bank_mask:0xf bound_ctrl:1
	s_nop 0
	v_cndmask_b32_e32 v20, v20, v25, vcc
	v_max_u32_dpp v68, v68, v68 quad_perm:[2,3,0,1] row_mask:0xf bank_mask:0xf bound_ctrl:1
	v_cndmask_b32_e32 v25, v25, v64, vcc
	v_cndmask_b32_e32 v64, v64, v17, vcc
	v_max_u32_dpp v68, v68, v68 row_half_mirror row_mask:0xf bank_mask:0xf bound_ctrl:1
	v_cndmask_b32_e64 v17, v17, 0, vcc
	s_nop 0
	v_max_u32_dpp v68, v68, v68 row_mirror row_mask:0xf bank_mask:0xf bound_ctrl:1
	v_cndmask_b32_e64 v72, v72, v68, s[62:63]
	v_cmp_eq_u32_e32 vcc, v16, v68
	v_max_u32_dpp v68, v67, v67 quad_perm:[1,0,3,2] row_mask:0xf bank_mask:0xf bound_ctrl:1
	s_nop 0
	v_cndmask_b32_e32 v16, v16, v19, vcc
	v_max_u32_dpp v68, v68, v68 quad_perm:[2,3,0,1] row_mask:0xf bank_mask:0xf bound_ctrl:1
	v_cndmask_b32_e32 v19, v19, v31, vcc
	v_cndmask_b32_e32 v31, v31, v9, vcc
	v_max_u32_dpp v68, v68, v68 row_half_mirror row_mask:0xf bank_mask:0xf bound_ctrl:1
	v_cndmask_b32_e64 v9, v9, 0, vcc
	s_nop 0
	v_max_u32_dpp v68, v68, v68 row_mirror row_mask:0xf bank_mask:0xf bound_ctrl:1
	v_cmp_eq_u32_e32 vcc, v67, v68
	v_cndmask_b32_e64 v69, v69, v68, s[64:65]
	s_nop 0
	v_cndmask_b32_e32 v67, v67, v66, vcc
	v_cndmask_b32_e32 v66, v66, v65, vcc
	v_cndmask_b32_e32 v29, v65, v29, vcc
	v_max_u32_dpp v65, v21, v21 quad_perm:[1,0,3,2] row_mask:0xf bank_mask:0xf bound_ctrl:1
	s_nop 1
	v_max_u32_dpp v65, v65, v65 quad_perm:[2,3,0,1] row_mask:0xf bank_mask:0xf bound_ctrl:1
	s_nop 1
	v_max_u32_dpp v65, v65, v65 row_half_mirror row_mask:0xf bank_mask:0xf bound_ctrl:1
	s_nop 1
	v_max_u32_dpp v65, v65, v65 row_mirror row_mask:0xf bank_mask:0xf bound_ctrl:1
	v_cmp_eq_u32_e32 vcc, v21, v65
	v_cndmask_b32_e64 v68, v70, v65, s[64:65]
	s_nop 0
	v_cndmask_b32_e32 v21, v21, v18, vcc
	v_cndmask_b32_e32 v18, v18, v27, vcc
	v_cndmask_b32_e32 v8, v27, v8, vcc
	v_max_u32_dpp v27, v20, v20 quad_perm:[1,0,3,2] row_mask:0xf bank_mask:0xf bound_ctrl:1
	s_nop 1
	v_max_u32_dpp v27, v27, v27 quad_perm:[2,3,0,1] row_mask:0xf bank_mask:0xf bound_ctrl:1
	s_nop 1
	v_max_u32_dpp v27, v27, v27 row_half_mirror row_mask:0xf bank_mask:0xf bound_ctrl:1
	s_nop 1
	v_max_u32_dpp v27, v27, v27 row_mirror row_mask:0xf bank_mask:0xf bound_ctrl:1
	v_cndmask_b32_e64 v65, v71, v27, s[64:65]
	v_cmp_eq_u32_e32 vcc, v20, v27
	v_max_u32_dpp v27, v16, v16 quad_perm:[1,0,3,2] row_mask:0xf bank_mask:0xf bound_ctrl:1
	s_nop 0
	v_cndmask_b32_e32 v20, v20, v25, vcc
	v_max_u32_dpp v27, v27, v27 quad_perm:[2,3,0,1] row_mask:0xf bank_mask:0xf bound_ctrl:1
	v_cndmask_b32_e32 v25, v25, v64, vcc
	v_cndmask_b32_e32 v17, v64, v17, vcc
	v_max_u32_dpp v27, v27, v27 row_half_mirror row_mask:0xf bank_mask:0xf bound_ctrl:1
	s_nop 1
	v_max_u32_dpp v27, v27, v27 row_mirror row_mask:0xf bank_mask:0xf bound_ctrl:1
	v_cndmask_b32_e64 v64, v72, v27, s[64:65]
	v_cmp_eq_u32_e32 vcc, v16, v27
	v_max_u32_dpp v27, v67, v67 quad_perm:[1,0,3,2] row_mask:0xf bank_mask:0xf bound_ctrl:1
	s_nop 0
	v_cndmask_b32_e32 v16, v16, v19, vcc
	v_max_u32_dpp v27, v27, v27 quad_perm:[2,3,0,1] row_mask:0xf bank_mask:0xf bound_ctrl:1
	v_cndmask_b32_e32 v19, v19, v31, vcc
	v_cndmask_b32_e32 v9, v31, v9, vcc
	v_max_u32_dpp v27, v27, v27 row_half_mirror row_mask:0xf bank_mask:0xf bound_ctrl:1
	s_nop 1
	v_max_u32_dpp v27, v27, v27 row_mirror row_mask:0xf bank_mask:0xf bound_ctrl:1
	v_cmp_eq_u32_e32 vcc, v67, v27
	v_cndmask_b32_e64 v31, v69, v27, s[66:67]
	s_nop 0
	v_cndmask_b32_e32 v27, v67, v66, vcc
	v_cndmask_b32_e32 v29, v66, v29, vcc
	v_max_u32_dpp v66, v21, v21 quad_perm:[1,0,3,2] row_mask:0xf bank_mask:0xf bound_ctrl:1
	s_nop 1
	v_max_u32_dpp v66, v66, v66 quad_perm:[2,3,0,1] row_mask:0xf bank_mask:0xf bound_ctrl:1
	s_nop 1
	v_max_u32_dpp v66, v66, v66 row_half_mirror row_mask:0xf bank_mask:0xf bound_ctrl:1
	s_nop 1
	v_max_u32_dpp v66, v66, v66 row_mirror row_mask:0xf bank_mask:0xf bound_ctrl:1
	v_cmp_eq_u32_e32 vcc, v21, v66
	v_cndmask_b32_e64 v67, v68, v66, s[66:67]
	s_nop 0
	v_cndmask_b32_e32 v21, v21, v18, vcc
	v_cndmask_b32_e32 v8, v18, v8, vcc
	v_max_u32_dpp v18, v20, v20 quad_perm:[1,0,3,2] row_mask:0xf bank_mask:0xf bound_ctrl:1
	s_nop 1
	v_max_u32_dpp v18, v18, v18 quad_perm:[2,3,0,1] row_mask:0xf bank_mask:0xf bound_ctrl:1
	s_nop 1
	v_max_u32_dpp v18, v18, v18 row_half_mirror row_mask:0xf bank_mask:0xf bound_ctrl:1
	s_nop 1
	v_max_u32_dpp v18, v18, v18 row_mirror row_mask:0xf bank_mask:0xf bound_ctrl:1
	v_cmp_eq_u32_e32 vcc, v20, v18
	v_cndmask_b32_e64 v65, v65, v18, s[66:67]
	s_nop 0
	v_cndmask_b32_e32 v18, v20, v25, vcc
	v_max_u32_dpp v20, v16, v16 quad_perm:[1,0,3,2] row_mask:0xf bank_mask:0xf bound_ctrl:1
	v_cndmask_b32_e32 v17, v25, v17, vcc
	s_nop 0
	v_max_u32_dpp v20, v20, v20 quad_perm:[2,3,0,1] row_mask:0xf bank_mask:0xf bound_ctrl:1
	s_nop 1
	v_max_u32_dpp v20, v20, v20 row_half_mirror row_mask:0xf bank_mask:0xf bound_ctrl:1
	s_nop 1
	v_max_u32_dpp v20, v20, v20 row_mirror row_mask:0xf bank_mask:0xf bound_ctrl:1
	v_cmp_eq_u32_e32 vcc, v16, v20
	v_cndmask_b32_e64 v25, v64, v20, s[66:67]
	s_nop 0
	v_cndmask_b32_e32 v16, v16, v19, vcc
	v_cndmask_b32_e32 v9, v19, v9, vcc
	v_max_u32_dpp v19, v27, v27 quad_perm:[1,0,3,2] row_mask:0xf bank_mask:0xf bound_ctrl:1
	s_nop 1
	v_max_u32_dpp v19, v19, v19 quad_perm:[2,3,0,1] row_mask:0xf bank_mask:0xf bound_ctrl:1
	s_nop 1
	v_max_u32_dpp v19, v19, v19 row_half_mirror row_mask:0xf bank_mask:0xf bound_ctrl:1
	s_nop 1
	v_max_u32_dpp v19, v19, v19 row_mirror row_mask:0xf bank_mask:0xf bound_ctrl:1
	v_cmp_eq_u32_e32 vcc, v27, v19
	v_cndmask_b32_e64 v20, v31, v19, s[68:69]
	s_nop 0
	v_cndmask_b32_e32 v19, v27, v29, vcc
	v_max_u32_dpp v27, v21, v21 quad_perm:[1,0,3,2] row_mask:0xf bank_mask:0xf bound_ctrl:1
	s_nop 1
	v_max_u32_dpp v27, v27, v27 quad_perm:[2,3,0,1] row_mask:0xf bank_mask:0xf bound_ctrl:1
	s_nop 1
	v_max_u32_dpp v27, v27, v27 row_half_mirror row_mask:0xf bank_mask:0xf bound_ctrl:1
	s_nop 1
	v_max_u32_dpp v27, v27, v27 row_mirror row_mask:0xf bank_mask:0xf bound_ctrl:1
	v_cmp_eq_u32_e32 vcc, v21, v27
	v_cndmask_b32_e64 v29, v67, v27, s[68:69]
	s_nop 0
	v_cndmask_b32_e32 v8, v21, v8, vcc
	v_max_u32_dpp v21, v18, v18 quad_perm:[1,0,3,2] row_mask:0xf bank_mask:0xf bound_ctrl:1
	s_nop 0
	v_max_u32_dpp v8, v8, v8 quad_perm:[1,0,3,2] row_mask:0xf bank_mask:0xf bound_ctrl:1
	v_max_u32_dpp v21, v21, v21 quad_perm:[2,3,0,1] row_mask:0xf bank_mask:0xf bound_ctrl:1
	s_nop 0
	v_max_u32_dpp v8, v8, v8 quad_perm:[2,3,0,1] row_mask:0xf bank_mask:0xf bound_ctrl:1
	v_max_u32_dpp v21, v21, v21 row_half_mirror row_mask:0xf bank_mask:0xf bound_ctrl:1
	s_nop 0
	v_max_u32_dpp v8, v8, v8 row_half_mirror row_mask:0xf bank_mask:0xf bound_ctrl:1
	v_max_u32_dpp v21, v21, v21 row_mirror row_mask:0xf bank_mask:0xf bound_ctrl:1
	v_cmp_eq_u32_e32 vcc, v18, v21
	v_max_u32_dpp v8, v8, v8 row_mirror row_mask:0xf bank_mask:0xf bound_ctrl:1
	v_cndmask_b32_e64 v27, v65, v21, s[68:69]
	v_cndmask_b32_e32 v17, v18, v17, vcc
	v_max_u32_dpp v18, v16, v16 quad_perm:[1,0,3,2] row_mask:0xf bank_mask:0xf bound_ctrl:1
	s_nop 1
	v_max_u32_dpp v18, v18, v18 quad_perm:[2,3,0,1] row_mask:0xf bank_mask:0xf bound_ctrl:1
	s_nop 1
	v_max_u32_dpp v18, v18, v18 row_half_mirror row_mask:0xf bank_mask:0xf bound_ctrl:1
	s_nop 1
	v_max_u32_dpp v18, v18, v18 row_mirror row_mask:0xf bank_mask:0xf bound_ctrl:1
	v_cmp_eq_u32_e32 vcc, v16, v18
	v_cndmask_b32_e64 v25, v25, v18, s[68:69]
	s_nop 0
	v_cndmask_b32_e32 v9, v16, v9, vcc
	v_max_u32_dpp v16, v19, v19 quad_perm:[1,0,3,2] row_mask:0xf bank_mask:0xf bound_ctrl:1
	s_nop 1
	v_max_u32_dpp v16, v16, v16 quad_perm:[2,3,0,1] row_mask:0xf bank_mask:0xf bound_ctrl:1
	s_nop 1
	v_max_u32_dpp v16, v16, v16 row_half_mirror row_mask:0xf bank_mask:0xf bound_ctrl:1
	s_nop 1
	v_max_u32_dpp v16, v16, v16 row_mirror row_mask:0xf bank_mask:0xf bound_ctrl:1
	v_cndmask_b32_e64 v31, v20, v16, s[70:71]
	v_cndmask_b32_e64 v20, v29, v8, s[70:71]
	v_max_u32_dpp v8, v17, v17 quad_perm:[1,0,3,2] row_mask:0xf bank_mask:0xf bound_ctrl:1
	v_not_b32_e32 v64, v31
	v_cmp_gt_i32_e32 vcc, 0, v31
	v_max_u32_dpp v8, v8, v8 quad_perm:[2,3,0,1] row_mask:0xf bank_mask:0xf bound_ctrl:1
	v_not_b32_e32 v21, v20
	s_nop 0
	v_max_u32_dpp v8, v8, v8 row_half_mirror row_mask:0xf bank_mask:0xf bound_ctrl:1
	s_nop 1
	v_max_u32_dpp v8, v8, v8 row_mirror row_mask:0xf bank_mask:0xf bound_ctrl:1
	v_cndmask_b32_e64 v18, v27, v8, s[70:71]
	v_not_b32_e32 v19, v18
	v_max_u32_dpp v8, v9, v9 quad_perm:[1,0,3,2] row_mask:0xf bank_mask:0xf bound_ctrl:1
	v_bitop3_b32 v9, v31, s16, v31 bitop3:0xcf
	s_nop 0
	v_max_u32_dpp v8, v8, v8 quad_perm:[2,3,0,1] row_mask:0xf bank_mask:0xf bound_ctrl:1
	s_nop 1
	v_max_u32_dpp v8, v8, v8 row_half_mirror row_mask:0xf bank_mask:0xf bound_ctrl:1
	s_nop 1
	v_max_u32_dpp v8, v8, v8 row_mirror row_mask:0xf bank_mask:0xf bound_ctrl:1
	v_cndmask_b32_e64 v16, v25, v8, s[70:71]
	v_lshrrev_b32_e32 v8, 4, v64
	v_and_or_b32 v8, v8, 15, v53
	v_lshlrev_b32_e32 v8, 2, v8
	ds_bpermute_b32 v7, v8, v7
	v_bitop3_b32 v8, v31, v53, 15 bitop3:0xce
	v_lshlrev_b32_e32 v8, 2, v8
	ds_bpermute_b32 v6, v8, v6
	v_and_b32_e32 v8, 0x7fffff00, v31
	v_cndmask_b32_e32 v8, v9, v8, vcc
	v_mov_b32_e32 v9, v199
	v_max_f32_e32 v25, v8, v8
	v_not_b32_e32 v17, v16
	v_mov_b32_dpp v9, v8 quad_perm:[1,0,3,2] row_mask:0xf bank_mask:0xf
	v_max_f32_e32 v9, v9, v9
	v_max_f32_e32 v9, v25, v9
	v_mov_b32_e32 v25, v199
	s_nop 1
	v_mov_b32_dpp v25, v9 quad_perm:[2,3,0,1] row_mask:0xf bank_mask:0xf
	v_max_f32_e32 v25, v25, v25
	v_max_f32_e32 v9, v9, v25
	v_mov_b32_e32 v25, v199
	s_nop 1
	v_mov_b32_dpp v25, v9 row_half_mirror row_mask:0xf bank_mask:0xf
	v_max_f32_e32 v25, v25, v25
	v_max_f32_e32 v9, v9, v25
	v_mov_b32_e32 v25, v199
	s_nop 1
	v_mov_b32_dpp v25, v9 row_mirror row_mask:0xf bank_mask:0xf
	v_max_f32_e32 v25, v25, v25
	v_max_f32_e32 v9, v9, v25
	v_sub_f32_e32 v8, v8, v9
	v_mul_f32_e32 v8, 0x3fb8aa3b, v8
	v_exp_f32_e32 v9, v8
	s_nop 1
	v_add_f32_dpp v8, v9, v9 quad_perm:[1,0,3,2] row_mask:0xf bank_mask:0xf bound_ctrl:1
	s_nop 1
	v_add_f32_dpp v8, v8, v8 quad_perm:[2,3,0,1] row_mask:0xf bank_mask:0xf bound_ctrl:1
	s_nop 1
	v_add_f32_dpp v8, v8, v8 row_half_mirror row_mask:0xf bank_mask:0xf bound_ctrl:1
	s_nop 1
	v_add_f32_dpp v25, v8, v8 row_mirror row_mask:0xf bank_mask:0xf bound_ctrl:1
	v_div_scale_f32 v27, s[6:7], v25, v25, v9
	v_rcp_f32_e32 v29, v27
	s_waitcnt lgkmcnt(0)
	v_lshl_add_u32 v8, v7, 7, v6
	v_lshl_add_u64 v[6:7], s[12:13], 0, v[40:41]
	v_add_co_u32_e32 v64, vcc, 0x1e000000, v6
	v_fma_f32 v31, -v27, v29, 1.0
	s_nop 0
	v_addc_co_u32_e32 v65, vcc, 0, v7, vcc
	v_fmac_f32_e32 v29, v31, v29
	v_div_scale_f32 v31, vcc, v9, v25, v9
	global_store_dword v[64:65], v8, off
	v_mul_f32_e32 v64, v31, v29
	v_fma_f32 v65, -v27, v64, v31
	v_fmac_f32_e32 v64, v65, v29
	v_fma_f32 v27, -v27, v64, v31
	v_div_fmas_f32 v27, v27, v29, v64
	v_div_fixup_f32 v25, v27, v25, v9
	v_ashrrev_i32_e32 v9, 31, v8
	v_lshlrev_b64 v[8:9], 2, v[8:9]
	v_lshl_add_u64 v[64:65], s[14:15], 0, v[8:9]
	global_load_dword v27, v[64:65], off
	v_add_co_u32_e32 v64, vcc, s18, v6
	v_lshl_add_u64 v[8:9], s[10:11], 0, v[8:9]
	s_nop 0
	v_addc_co_u32_e32 v65, vcc, 0, v7, vcc
	v_add_co_u32_e32 v6, vcc, s19, v6
	v_lshl_add_u64 v[40:41], v[40:41], 0, 64
	s_nop 0
	v_addc_co_u32_e32 v7, vcc, 0, v7, vcc
	v_cmp_gt_i32_e32 vcc, 0, v20
	global_load_dword v8, v[8:9], off
	s_waitcnt vmcnt(0)
	v_mul_f32_e32 v25, v27, v25
	global_store_dword v[64:65], v25, off
	v_bitop3_b32 v9, v20, s16, v20 bitop3:0xcf
	global_store_dword v[6:7], v8, off
	v_and_b32_e32 v8, 0x7fffff00, v20
	v_bitop3_b32 v7, v20, v53, 15 bitop3:0xce
	v_cndmask_b32_e32 v8, v9, v8, vcc
	v_mov_b32_e32 v9, v199
	v_lshlrev_b32_e32 v7, 2, v7
	ds_bpermute_b32 v7, v7, v14
	v_mov_b32_dpp v9, v8 quad_perm:[1,0,3,2] row_mask:0xf bank_mask:0xf
	v_max_f32_e32 v14, v8, v8
	v_max_f32_e32 v9, v9, v9
	v_max_f32_e32 v9, v14, v9
	v_mov_b32_e32 v14, v199
	v_lshrrev_b32_e32 v6, 4, v21
	v_and_or_b32 v6, v6, 15, v53
	v_mov_b32_dpp v14, v9 quad_perm:[2,3,0,1] row_mask:0xf bank_mask:0xf
	v_max_f32_e32 v14, v14, v14
	v_max_f32_e32 v9, v9, v14
	v_mov_b32_e32 v14, v199
	v_lshlrev_b32_e32 v6, 2, v6
	ds_bpermute_b32 v6, v6, v15
	v_mov_b32_dpp v14, v9 row_half_mirror row_mask:0xf bank_mask:0xf
	v_max_f32_e32 v14, v14, v14
	v_max_f32_e32 v9, v9, v14
	v_mov_b32_e32 v14, v199
	s_nop 1
	v_mov_b32_dpp v14, v9 row_mirror row_mask:0xf bank_mask:0xf
	v_max_f32_e32 v14, v14, v14
	v_max_f32_e32 v9, v9, v14
	v_sub_f32_e32 v8, v8, v9
	v_mul_f32_e32 v8, 0x3fb8aa3b, v8
	v_exp_f32_e32 v9, v8
	s_nop 1
	v_add_f32_dpp v8, v9, v9 quad_perm:[1,0,3,2] row_mask:0xf bank_mask:0xf bound_ctrl:1
	s_nop 1
	v_add_f32_dpp v8, v8, v8 quad_perm:[2,3,0,1] row_mask:0xf bank_mask:0xf bound_ctrl:1
	s_nop 1
	v_add_f32_dpp v8, v8, v8 row_half_mirror row_mask:0xf bank_mask:0xf bound_ctrl:1
	s_nop 1
	v_add_f32_dpp v20, v8, v8 row_mirror row_mask:0xf bank_mask:0xf bound_ctrl:1
	s_waitcnt lgkmcnt(0)
	v_lshl_add_u32 v8, v6, 7, v7
	v_lshl_add_u64 v[6:7], s[12:13], 0, v[38:39]
	v_add_co_u32_e32 v14, vcc, 0x1e000000, v6
	v_lshl_add_u64 v[38:39], v[38:39], 0, 64
	s_nop 0
	v_addc_co_u32_e32 v15, vcc, 0, v7, vcc
	global_store_dword v[14:15], v8, off
	v_div_scale_f32 v14, s[6:7], v20, v20, v9
	v_rcp_f32_e32 v15, v14
	s_nop 0
	v_fma_f32 v21, -v14, v15, 1.0
	v_fmac_f32_e32 v15, v21, v15
	v_div_scale_f32 v21, vcc, v9, v20, v9
	v_mul_f32_e32 v25, v21, v15
	v_fma_f32 v27, -v14, v25, v21
	v_fmac_f32_e32 v25, v27, v15
	v_fma_f32 v14, -v14, v25, v21
	v_div_fmas_f32 v14, v14, v15, v25
	v_div_fixup_f32 v20, v14, v20, v9
	v_ashrrev_i32_e32 v9, 31, v8
	v_lshlrev_b64 v[8:9], 2, v[8:9]
	v_lshl_add_u64 v[14:15], s[14:15], 0, v[8:9]
	global_load_dword v14, v[14:15], off
	v_lshl_add_u64 v[8:9], s[10:11], 0, v[8:9]
	global_load_dword v8, v[8:9], off
	s_waitcnt vmcnt(0)
	v_mul_f32_e32 v20, v14, v20
	v_add_co_u32_e32 v14, vcc, s18, v6
	s_nop 1
	v_addc_co_u32_e32 v15, vcc, 0, v7, vcc
	global_store_dword v[14:15], v20, off
	v_add_co_u32_e32 v6, vcc, s19, v6
	v_bitop3_b32 v9, v18, s16, v18 bitop3:0xcf
	s_nop 0
	v_addc_co_u32_e32 v7, vcc, 0, v7, vcc
	v_cmp_gt_i32_e32 vcc, 0, v18
	global_store_dword v[6:7], v8, off
	v_and_b32_e32 v8, 0x7fffff00, v18
	v_bitop3_b32 v7, v18, v53, 15 bitop3:0xce
	v_cndmask_b32_e32 v8, v9, v8, vcc
	v_mov_b32_e32 v9, v199
	v_lshlrev_b32_e32 v7, 2, v7
	ds_bpermute_b32 v7, v7, v12
	v_mov_b32_dpp v9, v8 quad_perm:[1,0,3,2] row_mask:0xf bank_mask:0xf
	v_max_f32_e32 v12, v8, v8
	v_max_f32_e32 v9, v9, v9
	v_max_f32_e32 v9, v12, v9
	v_mov_b32_e32 v12, v199
	v_lshrrev_b32_e32 v6, 4, v19
	v_and_or_b32 v6, v6, 15, v53
	v_mov_b32_dpp v12, v9 quad_perm:[2,3,0,1] row_mask:0xf bank_mask:0xf
	v_max_f32_e32 v12, v12, v12
	v_max_f32_e32 v9, v9, v12
	v_mov_b32_e32 v12, v199
	v_lshlrev_b32_e32 v6, 2, v6
	ds_bpermute_b32 v6, v6, v13
	v_mov_b32_dpp v12, v9 row_half_mirror row_mask:0xf bank_mask:0xf
	v_max_f32_e32 v12, v12, v12
	v_max_f32_e32 v9, v9, v12
	v_mov_b32_e32 v12, v199
	s_nop 1
	v_mov_b32_dpp v12, v9 row_mirror row_mask:0xf bank_mask:0xf
	v_max_f32_e32 v12, v12, v12
	v_max_f32_e32 v9, v9, v12
	v_sub_f32_e32 v8, v8, v9
	v_mul_f32_e32 v8, 0x3fb8aa3b, v8
	v_exp_f32_e32 v9, v8
	s_nop 1
	v_add_f32_dpp v8, v9, v9 quad_perm:[1,0,3,2] row_mask:0xf bank_mask:0xf bound_ctrl:1
	s_nop 1
	v_add_f32_dpp v8, v8, v8 quad_perm:[2,3,0,1] row_mask:0xf bank_mask:0xf bound_ctrl:1
	s_nop 1
	v_add_f32_dpp v8, v8, v8 row_half_mirror row_mask:0xf bank_mask:0xf bound_ctrl:1
	s_nop 1
	v_add_f32_dpp v14, v8, v8 row_mirror row_mask:0xf bank_mask:0xf bound_ctrl:1
	s_waitcnt lgkmcnt(0)
	v_lshl_add_u32 v8, v6, 7, v7
	v_lshl_add_u64 v[6:7], s[12:13], 0, v[36:37]
	v_add_co_u32_e32 v12, vcc, 0x1e000000, v6
	v_lshl_add_u64 v[36:37], v[36:37], 0, 64
	s_nop 0
	v_addc_co_u32_e32 v13, vcc, 0, v7, vcc
	global_store_dword v[12:13], v8, off
	v_div_scale_f32 v12, s[6:7], v14, v14, v9
	v_rcp_f32_e32 v13, v12
	s_nop 0
	v_fma_f32 v15, -v12, v13, 1.0
	v_fmac_f32_e32 v13, v15, v13
	v_div_scale_f32 v15, vcc, v9, v14, v9
	v_mul_f32_e32 v18, v15, v13
	v_fma_f32 v19, -v12, v18, v15
	v_fmac_f32_e32 v18, v19, v13
	v_fma_f32 v12, -v12, v18, v15
	v_div_fmas_f32 v12, v12, v13, v18
	v_div_fixup_f32 v14, v12, v14, v9
	v_ashrrev_i32_e32 v9, 31, v8
	v_lshlrev_b64 v[8:9], 2, v[8:9]
	v_lshl_add_u64 v[12:13], s[14:15], 0, v[8:9]
	global_load_dword v12, v[12:13], off
	v_lshl_add_u64 v[8:9], s[10:11], 0, v[8:9]
	global_load_dword v8, v[8:9], off
	s_waitcnt vmcnt(0)
	v_mul_f32_e32 v14, v12, v14
	v_add_co_u32_e32 v12, vcc, s18, v6
	s_nop 1
	v_addc_co_u32_e32 v13, vcc, 0, v7, vcc
	global_store_dword v[12:13], v14, off
	v_add_co_u32_e32 v6, vcc, s19, v6
	v_bitop3_b32 v9, v16, s16, v16 bitop3:0xcf
	s_nop 0
	v_addc_co_u32_e32 v7, vcc, 0, v7, vcc
	v_cmp_gt_i32_e32 vcc, 0, v16
	global_store_dword v[6:7], v8, off
	v_and_b32_e32 v8, 0x7fffff00, v16
	v_bitop3_b32 v7, v16, v53, 15 bitop3:0xce
	v_cndmask_b32_e32 v8, v9, v8, vcc
	v_mov_b32_e32 v9, v199
	v_lshlrev_b32_e32 v7, 2, v7
	ds_bpermute_b32 v7, v7, v10
	v_mov_b32_dpp v9, v8 quad_perm:[1,0,3,2] row_mask:0xf bank_mask:0xf
	v_max_f32_e32 v10, v8, v8
	v_max_f32_e32 v9, v9, v9
	v_max_f32_e32 v9, v10, v9
	v_mov_b32_e32 v10, v199
	v_lshrrev_b32_e32 v6, 4, v17
	v_and_or_b32 v6, v6, 15, v53
	v_mov_b32_dpp v10, v9 quad_perm:[2,3,0,1] row_mask:0xf bank_mask:0xf
	v_max_f32_e32 v10, v10, v10
	v_max_f32_e32 v9, v9, v10
	v_mov_b32_e32 v10, v199
	v_lshlrev_b32_e32 v6, 2, v6
	ds_bpermute_b32 v6, v6, v11
	v_mov_b32_dpp v10, v9 row_half_mirror row_mask:0xf bank_mask:0xf
	v_max_f32_e32 v10, v10, v10
	v_max_f32_e32 v9, v9, v10
	v_mov_b32_e32 v10, v199
	s_nop 1
	v_mov_b32_dpp v10, v9 row_mirror row_mask:0xf bank_mask:0xf
	v_max_f32_e32 v10, v10, v10
	v_max_f32_e32 v9, v9, v10
	v_sub_f32_e32 v8, v8, v9
	v_mul_f32_e32 v8, 0x3fb8aa3b, v8
	v_exp_f32_e32 v9, v8
	s_nop 1
	v_add_f32_dpp v8, v9, v9 quad_perm:[1,0,3,2] row_mask:0xf bank_mask:0xf bound_ctrl:1
	s_nop 1
	v_add_f32_dpp v8, v8, v8 quad_perm:[2,3,0,1] row_mask:0xf bank_mask:0xf bound_ctrl:1
	s_nop 1
	v_add_f32_dpp v8, v8, v8 row_half_mirror row_mask:0xf bank_mask:0xf bound_ctrl:1
	s_nop 1
	v_add_f32_dpp v12, v8, v8 row_mirror row_mask:0xf bank_mask:0xf bound_ctrl:1
	s_waitcnt lgkmcnt(0)
	v_lshl_add_u32 v8, v6, 7, v7
	v_lshl_add_u64 v[6:7], s[12:13], 0, v[34:35]
	v_add_co_u32_e32 v10, vcc, 0x1e000000, v6
	v_lshl_add_u64 v[34:35], v[34:35], 0, 64
	s_nop 0
	v_addc_co_u32_e32 v11, vcc, 0, v7, vcc
	global_store_dword v[10:11], v8, off
	v_div_scale_f32 v10, s[6:7], v12, v12, v9
	v_rcp_f32_e32 v11, v10
	s_mov_b64 s[6:7], 0x8000
	v_lshl_add_u64 v[44:45], v[44:45], 0, s[6:7]
	s_mov_b64 s[6:7], 0x1000
	v_fma_f32 v13, -v10, v11, 1.0
	v_fmac_f32_e32 v11, v13, v11
	v_div_scale_f32 v13, vcc, v9, v12, v9
	v_mul_f32_e32 v14, v13, v11
	v_fma_f32 v15, -v10, v14, v13
	v_fmac_f32_e32 v14, v15, v11
	v_fma_f32 v10, -v10, v14, v13
	v_div_fmas_f32 v10, v10, v11, v14
	v_div_fixup_f32 v12, v10, v12, v9
	v_ashrrev_i32_e32 v9, 31, v8
	v_lshlrev_b64 v[8:9], 2, v[8:9]
	v_lshl_add_u64 v[10:11], s[14:15], 0, v[8:9]
	global_load_dword v10, v[10:11], off
	v_lshl_add_u64 v[8:9], s[10:11], 0, v[8:9]
	v_lshl_add_u64 v[42:43], v[42:43], 0, s[6:7]
	global_load_dword v8, v[8:9], off
	s_waitcnt vmcnt(0)
	v_mul_f32_e32 v12, v10, v12
	v_add_co_u32_e32 v10, vcc, s18, v6
	s_nop 1
	v_addc_co_u32_e32 v11, vcc, 0, v7, vcc
	global_store_dword v[10:11], v12, off
	v_add_co_u32_e32 v6, vcc, 0x20000000, v6
	s_nop 1
	v_addc_co_u32_e32 v7, vcc, 0, v7, vcc
	global_store_dword v[6:7], v8, off
	s_cbranch_scc0 .LBB0_3012
.LBB0_3015:
	v_lshl_add_u64 v[14:15], s[12:13], 0, v[44:45]
	v_add_co_u32_e32 v68, vcc, 0x400000, v14
	v_lshl_add_u64 v[16:17], s[12:13], 0, v[42:43]
	s_nop 0
	v_addc_co_u32_e32 v69, vcc, 0, v15, vcc
	global_load_dwordx4 v[6:9], v[16:17], off offset:-2048
	global_load_dwordx4 v[10:13], v[16:17], off offset:-1024
	s_mov_b32 s74, 0x401000
	s_mov_b32 s75, 0
	s_mov_b32 s76, 0x403000
	s_mov_b32 s77, 0
	s_mov_b32 s78, 0x405000
	s_mov_b32 s79, 0
	s_mov_b32 s80, 0x407000
	s_mov_b32 s81, 0
	v_lshl_add_u64 v[196:197], v[14:15], 0, s[74:75]
	v_lshl_add_u64 v[244:245], v[14:15], 0, s[76:77]
	v_lshl_add_u64 v[246:247], v[14:15], 0, s[78:79]
	global_load_dwordx4 v[164:167], v[196:197], off offset:-4096
	global_load_dwordx4 v[168:171], v[196:197], off offset:-3072
	global_load_dwordx4 v[172:175], v[196:197], off offset:-2048
	global_load_dwordx4 v[176:179], v[196:197], off offset:-1024
	global_load_dwordx4 v[180:183], v[196:197], off
	global_load_dwordx4 v[184:187], v[196:197], off offset:1024
	global_load_dwordx4 v[188:191], v[196:197], off offset:2048
	global_load_dwordx4 v[192:195], v[196:197], off offset:3072
	global_load_dwordx4 v[200:203], v[244:245], off offset:-4096
	global_load_dwordx4 v[204:207], v[244:245], off offset:-3072
	global_load_dwordx4 v[208:211], v[244:245], off offset:-2048
	global_load_dwordx4 v[212:215], v[244:245], off offset:-1024
	global_load_dwordx4 v[216:219], v[244:245], off
	global_load_dwordx4 v[220:223], v[244:245], off offset:1024
	global_load_dwordx4 v[224:227], v[244:245], off offset:2048
	global_load_dwordx4 v[228:231], v[244:245], off offset:3072
	v_lshl_add_u64 v[196:197], v[14:15], 0, s[80:81]
	s_mov_b32 s6, 0x401000
	v_add_co_u32_e32 v74, vcc, s6, v14
	s_mov_b32 s6, 0x402000
	s_nop 0
	v_addc_co_u32_e32 v75, vcc, 0, v15, vcc
	v_add_co_u32_e32 v84, vcc, s6, v14
	s_mov_b32 s6, 0x403000
	s_nop 0
	v_addc_co_u32_e32 v85, vcc, 0, v15, vcc
	s_waitcnt vmcnt(14)
	v_mfma_f32_16x16x32_bf16 v[18:21], v[6:9], v[164:167], 0
	v_mfma_f32_16x16x32_bf16 v[18:21], v[10:13], v[168:171], v[18:21]
	global_load_dwordx4 v[164:167], v[246:247], off offset:-4096
	global_load_dwordx4 v[168:171], v[246:247], off offset:-3072
	s_nop 7
	v_ashrrev_i32_e32 v25, 31, v18
	v_bitop3_b32 v18, v25, v18, s95 bitop3:0x36
	v_and_or_b32 v64, v18, s33, v23
	v_ashrrev_i32_e32 v18, 31, v19
	v_bitop3_b32 v18, v18, v19, s95 bitop3:0x36
	v_and_or_b32 v29, v18, s33, v23
	v_ashrrev_i32_e32 v18, 31, v20
	v_bitop3_b32 v18, v18, v20, s95 bitop3:0x36
	v_and_or_b32 v27, v18, s33, v23
	v_ashrrev_i32_e32 v18, 31, v21
	v_bitop3_b32 v18, v18, v21, s95 bitop3:0x36
	v_and_or_b32 v25, v18, s33, v23
	s_nop 0
	s_waitcnt vmcnt(14)
	v_mfma_f32_16x16x32_bf16 v[18:21], v[6:9], v[172:175], 0
	v_mfma_f32_16x16x32_bf16 v[18:21], v[10:13], v[176:179], v[18:21]
	global_load_dwordx4 v[172:175], v[246:247], off offset:-2048
	global_load_dwordx4 v[176:179], v[246:247], off offset:-1024
	s_nop 7
	v_ashrrev_i32_e32 v31, 31, v18
	v_bitop3_b32 v18, v31, v18, s95 bitop3:0x36
	v_and_or_b32 v68, v18, s33, v46
	v_ashrrev_i32_e32 v18, 31, v19
	v_bitop3_b32 v18, v18, v19, s95 bitop3:0x36
	v_and_or_b32 v66, v18, s33, v46
	v_ashrrev_i32_e32 v18, 31, v20
	v_bitop3_b32 v18, v18, v20, s95 bitop3:0x36
	v_and_or_b32 v65, v18, s33, v46
	v_ashrrev_i32_e32 v18, 31, v21
	v_bitop3_b32 v18, v18, v21, s95 bitop3:0x36
	v_and_or_b32 v31, v18, s33, v46
	s_waitcnt vmcnt(14)
	v_mfma_f32_16x16x32_bf16 v[18:21], v[6:9], v[180:183], 0
	v_mfma_f32_16x16x32_bf16 v[18:21], v[10:13], v[184:187], v[18:21]
	global_load_dwordx4 v[180:183], v[246:247], off
	global_load_dwordx4 v[184:187], v[246:247], off offset:1024
	s_nop 7
	v_ashrrev_i32_e32 v67, 31, v18
	v_bitop3_b32 v18, v67, v18, s95 bitop3:0x36
	v_and_or_b32 v77, v18, s33, v47
	v_ashrrev_i32_e32 v18, 31, v19
	v_bitop3_b32 v18, v18, v19, s95 bitop3:0x36
	v_and_or_b32 v72, v18, s33, v47
	v_ashrrev_i32_e32 v18, 31, v20
	v_bitop3_b32 v18, v18, v20, s95 bitop3:0x36
	v_and_or_b32 v69, v18, s33, v47
	v_ashrrev_i32_e32 v18, 31, v21
	v_bitop3_b32 v18, v18, v21, s95 bitop3:0x36
	v_and_or_b32 v67, v18, s33, v47
	s_waitcnt vmcnt(14)
	v_mfma_f32_16x16x32_bf16 v[18:21], v[6:9], v[188:191], 0
	v_mfma_f32_16x16x32_bf16 v[18:21], v[10:13], v[192:195], v[18:21]
	global_load_dwordx4 v[188:191], v[246:247], off offset:2048
	global_load_dwordx4 v[192:195], v[246:247], off offset:3072
	s_nop 7
	v_ashrrev_i32_e32 v70, 31, v18
	v_bitop3_b32 v18, v70, v18, s95 bitop3:0x36
	v_and_or_b32 v107, v18, s33, v48
	v_ashrrev_i32_e32 v18, 31, v19
	v_bitop3_b32 v18, v18, v19, s95 bitop3:0x36
	v_and_or_b32 v98, v18, s33, v48
	v_ashrrev_i32_e32 v18, 31, v20
	v_bitop3_b32 v18, v18, v20, s95 bitop3:0x36
	v_and_or_b32 v87, v18, s33, v48
	v_ashrrev_i32_e32 v18, 31, v21
	v_bitop3_b32 v18, v18, v21, s95 bitop3:0x36
	v_and_or_b32 v78, v18, s33, v48
	s_waitcnt vmcnt(14)
	v_mfma_f32_16x16x32_bf16 v[18:21], v[6:9], v[200:203], 0
	v_mfma_f32_16x16x32_bf16 v[18:21], v[10:13], v[204:207], v[18:21]
	global_load_dwordx4 v[200:203], v[196:197], off offset:-4096
	global_load_dwordx4 v[204:207], v[196:197], off offset:-3072
	s_nop 7
	v_ashrrev_i32_e32 v70, 31, v18
	v_bitop3_b32 v18, v70, v18, s95 bitop3:0x36
	v_and_or_b32 v109, v18, s33, v49
	v_ashrrev_i32_e32 v18, 31, v19
	v_bitop3_b32 v18, v18, v19, s95 bitop3:0x36
	v_and_or_b32 v101, v18, s33, v49
	v_ashrrev_i32_e32 v18, 31, v20
	v_bitop3_b32 v18, v18, v20, s95 bitop3:0x36
	v_and_or_b32 v91, v18, s33, v49
	v_ashrrev_i32_e32 v18, 31, v21
	v_bitop3_b32 v18, v18, v21, s95 bitop3:0x36
	v_and_or_b32 v82, v18, s33, v49
	s_waitcnt vmcnt(14)
	v_mfma_f32_16x16x32_bf16 v[18:21], v[6:9], v[208:211], 0
	v_mfma_f32_16x16x32_bf16 v[18:21], v[10:13], v[212:215], v[18:21]
	global_load_dwordx4 v[208:211], v[196:197], off offset:-2048
	global_load_dwordx4 v[212:215], v[196:197], off offset:-1024
	s_nop 7
	v_ashrrev_i32_e32 v70, 31, v18
	v_bitop3_b32 v18, v70, v18, s95 bitop3:0x36
	v_and_or_b32 v112, v18, s33, v50
	v_ashrrev_i32_e32 v18, 31, v19
	v_bitop3_b32 v18, v18, v19, s95 bitop3:0x36
	v_and_or_b32 v105, v18, s33, v50
	v_ashrrev_i32_e32 v18, 31, v20
	v_add_co_u32_e32 v70, vcc, s6, v14
	v_bitop3_b32 v18, v18, v20, s95 bitop3:0x36
	s_nop 0
	v_addc_co_u32_e32 v71, vcc, 0, v15, vcc
	s_mov_b32 s6, 0x404000
	v_and_or_b32 v96, v18, s33, v50
	v_ashrrev_i32_e32 v18, 31, v21
	v_add_co_u32_e32 v74, vcc, s6, v14
	v_bitop3_b32 v18, v18, v21, s95 bitop3:0x36
	s_nop 0
	v_addc_co_u32_e32 v75, vcc, 0, v15, vcc
	v_and_or_b32 v86, v18, s33, v50
	s_mov_b32 s6, 0x405000
	s_waitcnt vmcnt(14)
	v_mfma_f32_16x16x32_bf16 v[18:21], v[6:9], v[216:219], 0
	v_mfma_f32_16x16x32_bf16 v[18:21], v[10:13], v[220:223], v[18:21]
	global_load_dwordx4 v[216:219], v[196:197], off
	global_load_dwordx4 v[220:223], v[196:197], off offset:1024
	s_nop 7
	v_ashrrev_i32_e32 v73, 31, v18
	v_bitop3_b32 v18, v73, v18, s95 bitop3:0x36
	v_and_or_b32 v114, v18, s33, v51
	v_ashrrev_i32_e32 v18, 31, v19
	v_bitop3_b32 v18, v18, v19, s95 bitop3:0x36
	v_and_or_b32 v110, v18, s33, v51
	v_ashrrev_i32_e32 v18, 31, v20
	v_bitop3_b32 v18, v18, v20, s95 bitop3:0x36
	v_and_or_b32 v102, v18, s33, v51
	v_ashrrev_i32_e32 v18, 31, v21
	v_bitop3_b32 v18, v18, v21, s95 bitop3:0x36
	v_and_or_b32 v92, v18, s33, v51
	s_waitcnt vmcnt(14)
	v_mfma_f32_16x16x32_bf16 v[6:9], v[6:9], v[224:227], 0
	v_mfma_f32_16x16x32_bf16 v[6:9], v[10:13], v[228:231], v[6:9]
	global_load_dwordx4 v[224:227], v[196:197], off offset:2048
	global_load_dwordx4 v[228:231], v[196:197], off offset:3072
	s_nop 7
	v_ashrrev_i32_e32 v10, 31, v6
	v_bitop3_b32 v6, v10, v6, s95 bitop3:0x36
	v_and_or_b32 v115, v6, s33, v52
	v_ashrrev_i32_e32 v6, 31, v7
	v_bitop3_b32 v6, v6, v7, s95 bitop3:0x36
	v_and_or_b32 v113, v6, s33, v52
	v_ashrrev_i32_e32 v6, 31, v8
	v_bitop3_b32 v6, v6, v8, s95 bitop3:0x36
	v_and_or_b32 v106, v6, s33, v52
	v_ashrrev_i32_e32 v6, 31, v9
	v_bitop3_b32 v6, v6, v9, s95 bitop3:0x36
	v_and_or_b32 v97, v6, s33, v52
	global_load_dwordx4 v[10:13], v[16:17], off
	global_load_dwordx4 v[6:9], v[16:17], off offset:1024
	s_nop 0
	s_waitcnt vmcnt(0)
	v_mfma_f32_16x16x32_bf16 v[16:19], v[10:13], v[164:167], 0
	v_mfma_f32_16x16x32_bf16 v[16:19], v[6:9], v[168:171], v[16:19]
	s_nop 7
	v_ashrrev_i32_e32 v20, 31, v16
	v_bitop3_b32 v16, v20, v16, s95 bitop3:0x36
	v_and_or_b32 v89, v16, s33, v23
	v_ashrrev_i32_e32 v16, 31, v17
	v_bitop3_b32 v16, v16, v17, s95 bitop3:0x36
	v_and_or_b32 v80, v16, s33, v23
	v_ashrrev_i32_e32 v16, 31, v18
	v_bitop3_b32 v16, v16, v18, s95 bitop3:0x36
	v_and_or_b32 v73, v16, s33, v23
	v_ashrrev_i32_e32 v16, 31, v19
	v_bitop3_b32 v16, v16, v19, s95 bitop3:0x36
	v_and_or_b32 v70, v16, s33, v23
	s_waitcnt vmcnt(12)
	v_mfma_f32_16x16x32_bf16 v[16:19], v[10:13], v[172:175], 0
	v_mfma_f32_16x16x32_bf16 v[16:19], v[6:9], v[176:179], v[16:19]
	s_nop 7
	v_ashrrev_i32_e32 v20, 31, v16
	v_bitop3_b32 v16, v20, v16, s95 bitop3:0x36
	v_and_or_b32 v94, v16, s33, v46
	v_ashrrev_i32_e32 v16, 31, v17
	v_bitop3_b32 v16, v16, v17, s95 bitop3:0x36
	v_and_or_b32 v84, v16, s33, v46
	v_ashrrev_i32_e32 v16, 31, v18
	v_add_co_u32_e32 v20, vcc, s6, v14
	v_bitop3_b32 v16, v16, v18, s95 bitop3:0x36
	s_nop 0
	v_addc_co_u32_e32 v21, vcc, 0, v15, vcc
	s_mov_b32 s6, 0x406000
	v_and_or_b32 v75, v16, s33, v46
	v_ashrrev_i32_e32 v16, 31, v19
	v_add_co_u32_e32 v120, vcc, s6, v14
	v_bitop3_b32 v16, v16, v19, s95 bitop3:0x36
	s_nop 0
	v_addc_co_u32_e32 v121, vcc, 0, v15, vcc
	v_and_or_b32 v71, v16, s33, v46
	s_waitcnt vmcnt(10)
	v_mfma_f32_16x16x32_bf16 v[16:19], v[10:13], v[180:183], 0
	s_mov_b32 s6, 0x407000
	v_mfma_f32_16x16x32_bf16 v[16:19], v[6:9], v[184:187], v[16:19]
	s_nop 7
	v_ashrrev_i32_e32 v74, 31, v16
	v_bitop3_b32 v16, v74, v16, s95 bitop3:0x36
	v_and_or_b32 v100, v16, s33, v47
	v_ashrrev_i32_e32 v16, 31, v17
	v_bitop3_b32 v16, v16, v17, s95 bitop3:0x36
	v_and_or_b32 v90, v16, s33, v47
	v_ashrrev_i32_e32 v16, 31, v18
	v_bitop3_b32 v16, v16, v18, s95 bitop3:0x36
	v_and_or_b32 v81, v16, s33, v47
	v_ashrrev_i32_e32 v16, 31, v19
	v_bitop3_b32 v16, v16, v19, s95 bitop3:0x36
	v_and_or_b32 v74, v16, s33, v47
	s_waitcnt vmcnt(8)
	v_mfma_f32_16x16x32_bf16 v[16:19], v[10:13], v[188:191], 0
	v_mfma_f32_16x16x32_bf16 v[16:19], v[6:9], v[192:195], v[16:19]
	s_nop 7
	v_ashrrev_i32_e32 v20, 31, v16
	v_bitop3_b32 v16, v20, v16, s95 bitop3:0x36
	v_and_or_b32 v104, v16, s33, v48
	v_ashrrev_i32_e32 v16, 31, v17
	v_bitop3_b32 v16, v16, v17, s95 bitop3:0x36
	v_and_or_b32 v95, v16, s33, v48
	v_ashrrev_i32_e32 v16, 31, v18
	v_bitop3_b32 v16, v16, v18, s95 bitop3:0x36
	v_and_or_b32 v85, v16, s33, v48
	v_ashrrev_i32_e32 v16, 31, v19
	v_bitop3_b32 v16, v16, v19, s95 bitop3:0x36
	v_and_or_b32 v76, v16, s33, v48
	s_waitcnt vmcnt(6)
	v_mfma_f32_16x16x32_bf16 v[16:19], v[10:13], v[200:203], 0
	v_mfma_f32_16x16x32_bf16 v[16:19], v[6:9], v[204:207], v[16:19]
	s_nop 7
	v_ashrrev_i32_e32 v20, 31, v16
	v_bitop3_b32 v16, v20, v16, s95 bitop3:0x36
	v_and_or_b32 v108, v16, s33, v49
	v_ashrrev_i32_e32 v16, 31, v17
	v_bitop3_b32 v16, v16, v17, s95 bitop3:0x36
	v_and_or_b32 v99, v16, s33, v49
	v_ashrrev_i32_e32 v16, 31, v18
	v_bitop3_b32 v16, v16, v18, s95 bitop3:0x36
	v_and_or_b32 v88, v16, s33, v49
	v_ashrrev_i32_e32 v16, 31, v19
	v_bitop3_b32 v16, v16, v19, s95 bitop3:0x36
	v_and_or_b32 v79, v16, s33, v49
	s_waitcnt vmcnt(4)
	v_mfma_f32_16x16x32_bf16 v[16:19], v[10:13], v[208:211], 0
	v_add_co_u32_e32 v120, vcc, s6, v14
	v_mfma_f32_16x16x32_bf16 v[16:19], v[6:9], v[212:215], v[16:19]
	v_addc_co_u32_e32 v121, vcc, 0, v15, vcc
	s_nop 6
	v_ashrrev_i32_e32 v20, 31, v16
	v_bitop3_b32 v16, v20, v16, s95 bitop3:0x36
	v_and_or_b32 v111, v16, s33, v50
	v_ashrrev_i32_e32 v16, 31, v17
	v_bitop3_b32 v16, v16, v17, s95 bitop3:0x36
	v_and_or_b32 v103, v16, s33, v50
	v_ashrrev_i32_e32 v16, 31, v18
	v_bitop3_b32 v16, v16, v18, s95 bitop3:0x36
	v_and_or_b32 v93, v16, s33, v50
	v_ashrrev_i32_e32 v16, 31, v19
	v_bitop3_b32 v16, v16, v19, s95 bitop3:0x36
	v_and_or_b32 v83, v16, s33, v50
	s_waitcnt vmcnt(2)
	v_mfma_f32_16x16x32_bf16 v[14:17], v[10:13], v[216:219], 0
	v_mfma_f32_16x16x32_bf16 v[14:17], v[6:9], v[220:223], v[14:17]
	s_nop 7
	v_ashrrev_i32_e32 v18, 31, v14
	v_bitop3_b32 v14, v18, v14, s95 bitop3:0x36
	v_and_or_b32 v119, v14, s33, v51
	v_ashrrev_i32_e32 v14, 31, v15
	v_bitop3_b32 v14, v14, v15, s95 bitop3:0x36
	v_and_or_b32 v118, v14, s33, v51
	v_ashrrev_i32_e32 v14, 31, v16
	v_bitop3_b32 v14, v14, v16, s95 bitop3:0x36
	v_and_or_b32 v117, v14, s33, v51
	v_ashrrev_i32_e32 v14, 31, v17
	v_bitop3_b32 v14, v14, v17, s95 bitop3:0x36
	v_and_or_b32 v116, v14, s33, v51
	s_waitcnt vmcnt(0)
	v_mfma_f32_16x16x32_bf16 v[10:13], v[10:13], v[224:227], 0
	v_max_u32_e32 v14, v109, v112
	v_min_u32_e32 v15, v109, v112
	v_max_u32_e32 v16, v114, v115
	v_mfma_f32_16x16x32_bf16 v[6:9], v[6:9], v[228:231], v[10:13]
	v_min_u32_e32 v17, v114, v115
	v_min_u32_e32 v19, v29, v66
	v_max_u32_e32 v20, v72, v98
	v_min_u32_e32 v11, v64, v68
	v_max_u32_e32 v12, v77, v107
	s_nop 2
	v_ashrrev_i32_e32 v10, 31, v6
	v_bitop3_b32 v6, v10, v6, s95 bitop3:0x36
	v_ashrrev_i32_e32 v10, 31, v7
	v_bitop3_b32 v7, v10, v7, s95 bitop3:0x36
	v_ashrrev_i32_e32 v10, 31, v8
	v_bitop3_b32 v8, v10, v8, s95 bitop3:0x36
	v_ashrrev_i32_e32 v10, 31, v9
	v_bitop3_b32 v9, v10, v9, s95 bitop3:0x36
	v_max_u32_e32 v10, v64, v68
	v_min_u32_e32 v13, v77, v107
	v_max_u32_e32 v18, v10, v12
	v_min_u32_e32 v10, v10, v12
	v_max_u32_e32 v12, v11, v13
	v_min_u32_e32 v11, v11, v13
	v_max_u32_e32 v13, v14, v16
	v_min_u32_e32 v14, v14, v16
	v_max_u32_e32 v16, v15, v17
	v_min_u32_e32 v15, v15, v17
	v_max_u32_e32 v17, v12, v10
	v_min_u32_e32 v10, v12, v10
	v_max_u32_e32 v12, v16, v14
	v_min_u32_e32 v14, v16, v14
	v_max_u32_e32 v16, v18, v13
	v_min_u32_e32 v13, v18, v13
	v_max_u32_e32 v18, v11, v15
	v_min_u32_e32 v11, v11, v15
	v_max_u32_e32 v15, v17, v12
	v_min_u32_e32 v12, v17, v12
	v_max_u32_e32 v17, v10, v14
	v_min_u32_e32 v10, v10, v14
	v_max_u32_e32 v14, v15, v13
	v_min_u32_e32 v13, v15, v13
	v_max_u32_e32 v15, v18, v10
	v_min_u32_e32 v10, v18, v10
	v_max_u32_e32 v18, v17, v13
	v_min_u32_e32 v13, v17, v13
	v_max_u32_e32 v17, v15, v12
	v_min_u32_e32 v12, v15, v12
	v_max_u32_e32 v15, v17, v13
	v_min_u32_e32 v13, v17, v13
	v_max_u32_e32 v17, v29, v66
	v_min_u32_e32 v21, v72, v98
	v_max_u32_e32 v29, v101, v105
	v_min_u32_e32 v64, v101, v105
	v_max_u32_e32 v66, v110, v113
	v_min_u32_e32 v68, v110, v113
	v_max_u32_e32 v72, v17, v20
	v_min_u32_e32 v17, v17, v20
	v_max_u32_e32 v20, v19, v21
	v_min_u32_e32 v19, v19, v21
	v_max_u32_e32 v21, v29, v66
	v_min_u32_e32 v29, v29, v66
	v_max_u32_e32 v66, v64, v68
	v_min_u32_e32 v64, v64, v68
	v_max_u32_e32 v68, v20, v17
	v_min_u32_e32 v17, v20, v17
	v_max_u32_e32 v20, v66, v29
	v_min_u32_e32 v29, v66, v29
	v_max_u32_e32 v66, v72, v21
	v_min_u32_e32 v21, v72, v21
	v_max_u32_e32 v72, v19, v64
	v_min_u32_e32 v19, v19, v64
	v_max_u32_e32 v64, v68, v20
	v_min_u32_e32 v20, v68, v20
	v_max_u32_e32 v68, v17, v29
	v_min_u32_e32 v17, v17, v29
	v_max_u32_e32 v29, v64, v21
	v_min_u32_e32 v21, v64, v21
	v_max_u32_e32 v64, v72, v17
	v_min_u32_e32 v17, v72, v17
	v_max_u32_e32 v72, v68, v21
	v_min_u32_e32 v21, v68, v21
	v_max_u32_e32 v68, v64, v20
	v_min_u32_e32 v20, v64, v20
	v_max_u32_e32 v64, v68, v21
	v_min_u32_e32 v21, v68, v21
	v_max_u32_e32 v68, v27, v65
	v_min_u32_e32 v27, v27, v65
	v_max_u32_e32 v65, v69, v87
	v_min_u32_e32 v69, v69, v87
	v_max_u32_e32 v77, v91, v96
	v_min_u32_e32 v87, v91, v96
	v_max_u32_e32 v91, v102, v106
	v_min_u32_e32 v96, v102, v106
	v_max_u32_e32 v98, v68, v65
	v_min_u32_e32 v65, v68, v65
	v_max_u32_e32 v68, v27, v69
	v_min_u32_e32 v27, v27, v69
	v_max_u32_e32 v69, v77, v91
	v_min_u32_e32 v77, v77, v91
	v_max_u32_e32 v91, v87, v96
	v_min_u32_e32 v87, v87, v96
	v_max_u32_e32 v96, v68, v65
	v_min_u32_e32 v65, v68, v65
	v_max_u32_e32 v68, v91, v77
	v_min_u32_e32 v77, v91, v77
	v_max_u32_e32 v91, v98, v69
	v_min_u32_e32 v69, v98, v69
	v_max_u32_e32 v98, v27, v87
	v_min_u32_e32 v27, v27, v87
	v_max_u32_e32 v87, v96, v68
	v_min_u32_e32 v68, v96, v68
	v_max_u32_e32 v96, v65, v77
	v_min_u32_e32 v65, v65, v77
	v_max_u32_e32 v77, v87, v69
	v_min_u32_e32 v69, v87, v69
	v_max_u32_e32 v87, v98, v65
	v_min_u32_e32 v65, v98, v65
	v_max_u32_e32 v98, v96, v69
	v_min_u32_e32 v69, v96, v69
	v_max_u32_e32 v96, v87, v68
	v_min_u32_e32 v68, v87, v68
	v_max_u32_e32 v87, v96, v69
	v_min_u32_e32 v69, v96, v69
	v_max_u32_e32 v96, v25, v31
	v_min_u32_e32 v25, v25, v31
	v_max_u32_e32 v31, v67, v78
	v_min_u32_e32 v67, v67, v78
	v_max_u32_e32 v78, v82, v86
	v_min_u32_e32 v82, v82, v86
	v_max_u32_e32 v86, v92, v97
	v_min_u32_e32 v92, v92, v97
	v_max_u32_e32 v97, v96, v31
	v_min_u32_e32 v31, v96, v31
	v_max_u32_e32 v96, v25, v67
	v_min_u32_e32 v25, v25, v67
	v_max_u32_e32 v67, v78, v86
	v_min_u32_e32 v78, v78, v86
	v_max_u32_e32 v86, v82, v92
	v_min_u32_e32 v82, v82, v92
	v_max_u32_e32 v92, v96, v31
	v_min_u32_e32 v31, v96, v31
	v_max_u32_e32 v96, v86, v78
	v_min_u32_e32 v78, v86, v78
	v_max_u32_e32 v86, v97, v67
	v_min_u32_e32 v67, v97, v67
	v_max_u32_e32 v97, v25, v82
	v_min_u32_e32 v25, v25, v82
	v_max_u32_e32 v82, v92, v96
	v_min_u32_e32 v92, v92, v96
	v_max_u32_e32 v96, v31, v78
	v_min_u32_e32 v31, v31, v78
	v_max_u32_e32 v78, v82, v67
	v_min_u32_e32 v67, v82, v67
	v_max_u32_e32 v82, v97, v31
	v_and_or_b32 v6, v6, s33, v52
	v_min_u32_e32 v31, v97, v31
	v_max_u32_e32 v97, v96, v67
	v_min_u32_e32 v67, v96, v67
	v_max_u32_e32 v96, v82, v92
	v_min_u32_e32 v82, v82, v92
	v_max_u32_e32 v92, v96, v67
	v_min_u32_e32 v67, v96, v67
	v_max_u32_e32 v96, v89, v94
	v_min_u32_e32 v89, v89, v94
	v_max_u32_e32 v94, v100, v104
	v_min_u32_e32 v100, v100, v104
	v_max_u32_e32 v101, v108, v111
	v_min_u32_e32 v102, v108, v111
	v_max_u32_e32 v104, v119, v6
	v_min_u32_e32 v6, v119, v6
	v_max_u32_e32 v105, v96, v94
	v_min_u32_e32 v94, v96, v94
	v_max_u32_e32 v96, v89, v100
	v_min_u32_e32 v89, v89, v100
	v_max_u32_e32 v100, v101, v104
	v_min_u32_e32 v101, v101, v104
	v_max_u32_e32 v104, v102, v6
	v_min_u32_e32 v6, v102, v6
	v_max_u32_e32 v102, v96, v94
	v_min_u32_e32 v94, v96, v94
	v_max_u32_e32 v96, v104, v101
	v_min_u32_e32 v101, v104, v101
	v_max_u32_e32 v104, v105, v100
	v_min_u32_e32 v100, v105, v100
	v_max_u32_e32 v105, v89, v6
	v_min_u32_e32 v89, v89, v6
	v_max_u32_e32 v6, v102, v96
	v_min_u32_e32 v96, v102, v96
	v_max_u32_e32 v102, v94, v101
	v_min_u32_e32 v94, v94, v101
	v_max_u32_e32 v101, v6, v100
	v_min_u32_e32 v6, v6, v100
	v_max_u32_e32 v100, v105, v94
	v_and_or_b32 v7, v7, s33, v52
	v_min_u32_e32 v94, v105, v94
	v_max_u32_e32 v105, v102, v6
	v_min_u32_e32 v6, v102, v6
	v_max_u32_e32 v102, v100, v96
	v_min_u32_e32 v96, v100, v96
	v_max_u32_e32 v100, v102, v6
	v_min_u32_e32 v102, v102, v6
	v_max_u32_e32 v6, v80, v84
	v_min_u32_e32 v80, v80, v84
	v_max_u32_e32 v84, v90, v95
	v_min_u32_e32 v90, v90, v95
	v_max_u32_e32 v95, v99, v103
	v_min_u32_e32 v99, v99, v103
	v_max_u32_e32 v103, v118, v7
	v_min_u32_e32 v7, v118, v7
	v_max_u32_e32 v106, v6, v84
	v_min_u32_e32 v6, v6, v84
	v_max_u32_e32 v84, v80, v90
	v_min_u32_e32 v80, v80, v90
	v_max_u32_e32 v90, v95, v103
	v_min_u32_e32 v95, v95, v103
	v_max_u32_e32 v103, v99, v7
	v_min_u32_e32 v7, v99, v7
	v_max_u32_e32 v99, v84, v6
	v_min_u32_e32 v6, v84, v6
	v_max_u32_e32 v84, v103, v95
	v_min_u32_e32 v95, v103, v95
	v_max_u32_e32 v103, v106, v90
	v_min_u32_e32 v90, v106, v90
	v_max_u32_e32 v106, v80, v7
	v_min_u32_e32 v7, v80, v7
	v_max_u32_e32 v80, v99, v84
	v_min_u32_e32 v84, v99, v84
	v_max_u32_e32 v99, v6, v95
	v_min_u32_e32 v6, v6, v95
	v_max_u32_e32 v95, v80, v90
	v_min_u32_e32 v80, v80, v90
	v_max_u32_e32 v90, v106, v6
	v_and_or_b32 v8, v8, s33, v52
	v_min_u32_e32 v106, v106, v6
	v_max_u32_e32 v107, v99, v80
	v_min_u32_e32 v6, v99, v80
	v_max_u32_e32 v80, v90, v84
	v_min_u32_e32 v84, v90, v84
	v_max_u32_e32 v90, v80, v6
	v_min_u32_e32 v80, v80, v6
	v_max_u32_e32 v6, v73, v75
	v_min_u32_e32 v73, v73, v75
	v_max_u32_e32 v75, v81, v85
	v_min_u32_e32 v81, v81, v85
	v_max_u32_e32 v85, v88, v93
	v_min_u32_e32 v88, v88, v93
	v_max_u32_e32 v93, v117, v8
	v_min_u32_e32 v8, v117, v8
	v_max_u32_e32 v99, v6, v75
	v_min_u32_e32 v6, v6, v75
	v_max_u32_e32 v75, v73, v81
	v_min_u32_e32 v73, v73, v81
	v_max_u32_e32 v81, v85, v93
	v_min_u32_e32 v85, v85, v93
	v_max_u32_e32 v93, v88, v8
	v_min_u32_e32 v8, v88, v8
	v_max_u32_e32 v88, v75, v6
	v_min_u32_e32 v6, v75, v6
	v_max_u32_e32 v75, v93, v85
	v_min_u32_e32 v85, v93, v85
	v_max_u32_e32 v93, v99, v81
	v_min_u32_e32 v81, v99, v81
	v_max_u32_e32 v99, v73, v8
	v_min_u32_e32 v73, v73, v8
	v_max_u32_e32 v8, v88, v75
	v_min_u32_e32 v75, v88, v75
	v_max_u32_e32 v88, v6, v85
	v_min_u32_e32 v6, v6, v85
	v_max_u32_e32 v85, v8, v81
	v_min_u32_e32 v8, v8, v81
	v_max_u32_e32 v81, v99, v6
	v_and_or_b32 v9, v9, s33, v52
	v_min_u32_e32 v99, v99, v6
	v_max_u32_e32 v108, v88, v8
	v_min_u32_e32 v6, v88, v8
	v_max_u32_e32 v8, v81, v75
	v_min_u32_e32 v75, v81, v75
	v_max_u32_e32 v81, v8, v6
	v_min_u32_e32 v88, v8, v6
	v_max_u32_e32 v6, v70, v71
	v_min_u32_e32 v8, v70, v71
	v_max_u32_e32 v70, v74, v76
	v_min_u32_e32 v71, v74, v76
	v_max_u32_e32 v74, v79, v83
	v_min_u32_e32 v76, v79, v83
	v_max_u32_e32 v79, v116, v9
	v_min_u32_e32 v9, v116, v9
	v_max_u32_e32 v83, v6, v70
	v_min_u32_e32 v6, v6, v70
	v_max_u32_e32 v70, v8, v71
	v_min_u32_e32 v8, v8, v71
	v_max_u32_e32 v71, v74, v79
	v_min_u32_e32 v74, v74, v79
	v_max_u32_e32 v79, v76, v9
	v_min_u32_e32 v9, v76, v9
	v_max_u32_e32 v76, v70, v6
	v_min_u32_e32 v6, v70, v6
	v_max_u32_e32 v70, v79, v74
	v_min_u32_e32 v74, v79, v74
	v_max_u32_e32 v79, v83, v71
	v_min_u32_e32 v71, v83, v71
	v_max_u32_e32 v83, v8, v9
	v_min_u32_e32 v109, v8, v9
	v_max_u32_e32 v8, v76, v70
	v_min_u32_e32 v9, v76, v70
	v_max_u32_e32 v70, v6, v74
	v_min_u32_e32 v6, v6, v74
	v_max_u32_e32 v74, v8, v71
	v_min_u32_e32 v8, v8, v71
	v_max_u32_e32 v71, v83, v6
	v_min_u32_e32 v76, v83, v6
	v_max_u32_e32 v83, v70, v8
	v_min_u32_e32 v6, v70, v8
	v_max_u32_e32 v8, v71, v9
	v_min_u32_e32 v70, v71, v9
	v_max_u32_e32 v71, v8, v6
	v_min_u32_e32 v110, v8, v6
	v_max_u32_dpp v6, v16, v16 quad_perm:[1,0,3,2] row_mask:0xf bank_mask:0xf bound_ctrl:1
	v_mov_b32_e32 v8, 0
	s_nop 0
	v_max_u32_dpp v6, v6, v6 quad_perm:[2,3,0,1] row_mask:0xf bank_mask:0xf bound_ctrl:1
	s_nop 1
	v_max_u32_dpp v6, v6, v6 row_half_mirror row_mask:0xf bank_mask:0xf bound_ctrl:1
	s_nop 1
	v_max_u32_dpp v6, v6, v6 row_mirror row_mask:0xf bank_mask:0xf bound_ctrl:1
	v_cndmask_b32_e64 v111, 0, v6, s[72:73]
	v_cmp_eq_u32_e32 vcc, v16, v6
	v_max_u32_dpp v6, v66, v66 quad_perm:[1,0,3,2] row_mask:0xf bank_mask:0xf bound_ctrl:1
	s_nop 0
	v_cndmask_b32_e32 v112, v15, v13, vcc
	v_max_u32_dpp v6, v6, v6 quad_perm:[2,3,0,1] row_mask:0xf bank_mask:0xf bound_ctrl:1
	v_cndmask_b32_e32 v13, v13, v12, vcc
	v_cndmask_b32_e32 v113, v12, v10, vcc
	v_max_u32_dpp v6, v6, v6 row_half_mirror row_mask:0xf bank_mask:0xf bound_ctrl:1
	v_cndmask_b32_e32 v10, v10, v11, vcc
	v_cndmask_b32_e64 v114, v11, 0, vcc
	v_max_u32_dpp v12, v6, v6 row_mirror row_mask:0xf bank_mask:0xf bound_ctrl:1
	v_max_u32_dpp v6, v91, v91 quad_perm:[1,0,3,2] row_mask:0xf bank_mask:0xf bound_ctrl:1
	v_max_u32_dpp v11, v104, v104 quad_perm:[1,0,3,2] row_mask:0xf bank_mask:0xf bound_ctrl:1
	v_cndmask_b32_e32 v16, v16, v14, vcc
	v_max_u32_dpp v6, v6, v6 quad_perm:[2,3,0,1] row_mask:0xf bank_mask:0xf bound_ctrl:1
	v_cndmask_b32_e32 v14, v14, v18, vcc
	v_cndmask_b32_e32 v18, v18, v15, vcc
	v_max_u32_dpp v6, v6, v6 row_half_mirror row_mask:0xf bank_mask:0xf bound_ctrl:1
	v_cmp_eq_u32_e32 vcc, v66, v12
	v_max_u32_dpp v11, v11, v11 quad_perm:[2,3,0,1] row_mask:0xf bank_mask:0xf bound_ctrl:1
	v_max_u32_dpp v9, v6, v6 row_mirror row_mask:0xf bank_mask:0xf bound_ctrl:1
	v_max_u32_dpp v6, v86, v86 quad_perm:[1,0,3,2] row_mask:0xf bank_mask:0xf bound_ctrl:1
	v_cndmask_b32_e32 v66, v66, v29, vcc
	v_cndmask_b32_e32 v29, v29, v72, vcc
	v_max_u32_dpp v6, v6, v6 quad_perm:[2,3,0,1] row_mask:0xf bank_mask:0xf bound_ctrl:1
	v_cndmask_b32_e32 v72, v72, v64, vcc
	v_cndmask_b32_e32 v64, v64, v21, vcc
	v_max_u32_dpp v6, v6, v6 row_half_mirror row_mask:0xf bank_mask:0xf bound_ctrl:1
	v_cndmask_b32_e32 v21, v21, v20, vcc
	v_cndmask_b32_e32 v20, v20, v17, vcc
	v_cndmask_b32_e32 v17, v17, v19, vcc
	v_cndmask_b32_e64 v19, v19, 0, vcc
	v_cmp_eq_u32_e32 vcc, v91, v9
	v_max_u32_dpp v6, v6, v6 row_mirror row_mask:0xf bank_mask:0xf bound_ctrl:1
	v_max_u32_dpp v11, v11, v11 row_half_mirror row_mask:0xf bank_mask:0xf bound_ctrl:1
	v_cndmask_b32_e32 v91, v91, v77, vcc
	v_cndmask_b32_e32 v77, v77, v98, vcc
	v_cndmask_b32_e32 v98, v98, v87, vcc
	v_cndmask_b32_e32 v87, v87, v69, vcc
	v_cndmask_b32_e32 v69, v69, v68, vcc
	v_cndmask_b32_e32 v68, v68, v65, vcc
	v_cndmask_b32_e32 v65, v65, v27, vcc
	v_cndmask_b32_e64 v27, v27, 0, vcc
	v_cmp_eq_u32_e32 vcc, v86, v6
	v_max_u32_dpp v11, v11, v11 row_mirror row_mask:0xf bank_mask:0xf bound_ctrl:1
	v_cndmask_b32_e64 v115, 0, v11, s[72:73]
	v_cndmask_b32_e32 v86, v86, v78, vcc
	v_cndmask_b32_e32 v78, v78, v97, vcc
	v_cndmask_b32_e32 v97, v97, v92, vcc
	v_cndmask_b32_e32 v92, v92, v67, vcc
	v_cndmask_b32_e32 v67, v67, v82, vcc
	v_cndmask_b32_e32 v82, v82, v31, vcc
	v_cndmask_b32_e32 v31, v31, v25, vcc
	v_cndmask_b32_e64 v25, v25, 0, vcc
	v_cmp_eq_u32_e32 vcc, v104, v11
	v_max_u32_dpp v11, v103, v103 quad_perm:[1,0,3,2] row_mask:0xf bank_mask:0xf bound_ctrl:1
	v_max_u32_dpp v117, v16, v16 quad_perm:[1,0,3,2] row_mask:0xf bank_mask:0xf bound_ctrl:1
	v_cndmask_b32_e32 v104, v104, v101, vcc
	v_max_u32_dpp v11, v11, v11 quad_perm:[2,3,0,1] row_mask:0xf bank_mask:0xf bound_ctrl:1
	v_cndmask_b32_e32 v101, v101, v105, vcc
	v_cndmask_b32_e32 v105, v105, v100, vcc
	v_max_u32_dpp v11, v11, v11 row_half_mirror row_mask:0xf bank_mask:0xf bound_ctrl:1
	v_cndmask_b32_e32 v100, v100, v102, vcc
	v_cndmask_b32_e32 v102, v102, v96, vcc
	v_max_u32_dpp v15, v11, v11 row_mirror row_mask:0xf bank_mask:0xf bound_ctrl:1
	v_cndmask_b32_e32 v96, v96, v94, vcc
	v_cndmask_b32_e32 v94, v94, v89, vcc
	v_cndmask_b32_e64 v89, v89, 0, vcc
	v_cmp_eq_u32_e32 vcc, v103, v15
	v_max_u32_dpp v117, v117, v117 quad_perm:[2,3,0,1] row_mask:0xf bank_mask:0xf bound_ctrl:1
	s_nop 0
	v_cndmask_b32_e32 v103, v103, v95, vcc
	v_cndmask_b32_e32 v95, v95, v107, vcc
	v_cndmask_b32_e32 v107, v107, v90, vcc
	v_cndmask_b32_e32 v90, v90, v80, vcc
	v_cndmask_b32_e32 v80, v80, v84, vcc
	v_cndmask_b32_e32 v84, v84, v106, vcc
	v_cndmask_b32_e32 v106, v106, v7, vcc
	v_cndmask_b32_e64 v116, v7, 0, vcc
	v_max_u32_dpp v7, v93, v93 quad_perm:[1,0,3,2] row_mask:0xf bank_mask:0xf bound_ctrl:1
	v_max_u32_dpp v117, v117, v117 row_half_mirror row_mask:0xf bank_mask:0xf bound_ctrl:1
	s_nop 0
	v_max_u32_dpp v7, v7, v7 quad_perm:[2,3,0,1] row_mask:0xf bank_mask:0xf bound_ctrl:1
	v_max_u32_dpp v117, v117, v117 row_mirror row_mask:0xf bank_mask:0xf bound_ctrl:1
	v_cndmask_b32_e64 v111, v111, v117, s[42:43]
	v_max_u32_dpp v7, v7, v7 row_half_mirror row_mask:0xf bank_mask:0xf bound_ctrl:1
	s_nop 1
	v_max_u32_dpp v11, v7, v7 row_mirror row_mask:0xf bank_mask:0xf bound_ctrl:1
	v_max_u32_dpp v7, v79, v79 quad_perm:[1,0,3,2] row_mask:0xf bank_mask:0xf bound_ctrl:1
	v_cmp_eq_u32_e32 vcc, v93, v11
	s_nop 0
	v_max_u32_dpp v7, v7, v7 quad_perm:[2,3,0,1] row_mask:0xf bank_mask:0xf bound_ctrl:1
	v_cndmask_b32_e32 v93, v93, v85, vcc
	v_cndmask_b32_e32 v85, v85, v108, vcc
	v_max_u32_dpp v7, v7, v7 row_half_mirror row_mask:0xf bank_mask:0xf bound_ctrl:1
	v_cndmask_b32_e32 v108, v108, v81, vcc
	v_cndmask_b32_e32 v81, v81, v88, vcc
	v_max_u32_dpp v7, v7, v7 row_mirror row_mask:0xf bank_mask:0xf bound_ctrl:1
	v_cndmask_b32_e32 v88, v88, v75, vcc
	v_cndmask_b32_e32 v75, v75, v99, vcc
	v_cndmask_b32_e32 v99, v99, v73, vcc
	v_cndmask_b32_e64 v73, v73, 0, vcc
	v_cmp_eq_u32_e32 vcc, v79, v7
	s_nop 1
	v_cndmask_b32_e32 v79, v79, v74, vcc
	v_cndmask_b32_e32 v74, v74, v83, vcc
	v_cndmask_b32_e32 v83, v83, v71, vcc
	v_cndmask_b32_e32 v71, v71, v110, vcc
	v_cndmask_b32_e32 v110, v110, v70, vcc
	v_cndmask_b32_e32 v70, v70, v76, vcc
	v_cndmask_b32_e32 v76, v76, v109, vcc
	v_cndmask_b32_e64 v109, v109, 0, vcc
	v_cmp_eq_u32_e32 vcc, v16, v117
	s_nop 1
	v_cndmask_b32_e32 v119, v13, v113, vcc
	v_cndmask_b32_e32 v113, v113, v10, vcc
	v_cndmask_b32_e32 v120, v10, v114, vcc
	v_max_u32_dpp v10, v66, v66 quad_perm:[1,0,3,2] row_mask:0xf bank_mask:0xf bound_ctrl:1
	v_cndmask_b32_e32 v117, v14, v18, vcc
	v_cndmask_b32_e32 v118, v18, v112, vcc
	v_max_u32_dpp v10, v10, v10 quad_perm:[2,3,0,1] row_mask:0xf bank_mask:0xf bound_ctrl:1
	v_cndmask_b32_e32 v16, v16, v14, vcc
	v_cndmask_b32_e32 v112, v112, v13, vcc
	v_max_u32_dpp v10, v10, v10 row_half_mirror row_mask:0xf bank_mask:0xf bound_ctrl:1
	v_max_u32_dpp v13, v104, v104 quad_perm:[1,0,3,2] row_mask:0xf bank_mask:0xf bound_ctrl:1
	v_cndmask_b32_e64 v114, v114, 0, vcc
	v_max_u32_dpp v18, v10, v10 row_mirror row_mask:0xf bank_mask:0xf bound_ctrl:1
	v_max_u32_dpp v10, v91, v91 quad_perm:[1,0,3,2] row_mask:0xf bank_mask:0xf bound_ctrl:1
	v_cmp_eq_u32_e32 vcc, v66, v18
	v_max_u32_dpp v13, v13, v13 quad_perm:[2,3,0,1] row_mask:0xf bank_mask:0xf bound_ctrl:1
	v_max_u32_dpp v10, v10, v10 quad_perm:[2,3,0,1] row_mask:0xf bank_mask:0xf bound_ctrl:1
	v_cndmask_b32_e32 v66, v66, v29, vcc
	v_cndmask_b32_e32 v121, v29, v72, vcc
	v_max_u32_dpp v10, v10, v10 row_half_mirror row_mask:0xf bank_mask:0xf bound_ctrl:1
	v_cndmask_b32_e32 v72, v72, v64, vcc
	v_cndmask_b32_e32 v64, v64, v21, vcc
	v_max_u32_dpp v14, v10, v10 row_mirror row_mask:0xf bank_mask:0xf bound_ctrl:1
	v_max_u32_dpp v10, v86, v86 quad_perm:[1,0,3,2] row_mask:0xf bank_mask:0xf bound_ctrl:1
	v_cndmask_b32_e32 v122, v21, v20, vcc
	v_cndmask_b32_e32 v20, v20, v17, vcc
	v_max_u32_dpp v10, v10, v10 quad_perm:[2,3,0,1] row_mask:0xf bank_mask:0xf bound_ctrl:1
	v_cndmask_b32_e32 v123, v17, v19, vcc
	v_cndmask_b32_e64 v19, v19, 0, vcc
	v_max_u32_dpp v10, v10, v10 row_half_mirror row_mask:0xf bank_mask:0xf bound_ctrl:1
	v_cmp_eq_u32_e32 vcc, v91, v14
	v_max_u32_dpp v13, v13, v13 row_half_mirror row_mask:0xf bank_mask:0xf bound_ctrl:1
	v_max_u32_dpp v10, v10, v10 row_mirror row_mask:0xf bank_mask:0xf bound_ctrl:1
	v_cndmask_b32_e32 v91, v91, v77, vcc
	v_cndmask_b32_e32 v77, v77, v98, vcc
	v_cndmask_b32_e32 v98, v98, v87, vcc
	v_cndmask_b32_e32 v87, v87, v69, vcc
	v_cndmask_b32_e32 v69, v69, v68, vcc
	v_cndmask_b32_e32 v68, v68, v65, vcc
	v_cndmask_b32_e32 v65, v65, v27, vcc
	v_cndmask_b32_e64 v27, v27, 0, vcc
	v_cmp_eq_u32_e32 vcc, v86, v10
	v_max_u32_dpp v13, v13, v13 row_mirror row_mask:0xf bank_mask:0xf bound_ctrl:1
	v_cndmask_b32_e64 v115, v115, v13, s[42:43]
	v_cndmask_b32_e32 v86, v86, v78, vcc
	v_cndmask_b32_e32 v78, v78, v97, vcc
	v_cndmask_b32_e32 v97, v97, v92, vcc
	v_cndmask_b32_e32 v92, v92, v67, vcc
	v_cndmask_b32_e32 v67, v67, v82, vcc
	v_cndmask_b32_e32 v82, v82, v31, vcc
	v_cndmask_b32_e32 v31, v31, v25, vcc
	v_cndmask_b32_e64 v25, v25, 0, vcc
	v_cmp_eq_u32_e32 vcc, v104, v13
	v_max_u32_dpp v13, v103, v103 quad_perm:[1,0,3,2] row_mask:0xf bank_mask:0xf bound_ctrl:1
	v_max_u32_dpp v29, v16, v16 quad_perm:[1,0,3,2] row_mask:0xf bank_mask:0xf bound_ctrl:1
	v_cndmask_b32_e32 v104, v104, v101, vcc
	v_max_u32_dpp v13, v13, v13 quad_perm:[2,3,0,1] row_mask:0xf bank_mask:0xf bound_ctrl:1
	v_cndmask_b32_e32 v101, v101, v105, vcc
	v_cndmask_b32_e32 v105, v105, v100, vcc
	v_max_u32_dpp v13, v13, v13 row_half_mirror row_mask:0xf bank_mask:0xf bound_ctrl:1
	v_cndmask_b32_e32 v100, v100, v102, vcc
	v_cndmask_b32_e32 v102, v102, v96, vcc
	v_max_u32_dpp v21, v13, v13 row_mirror row_mask:0xf bank_mask:0xf bound_ctrl:1
	v_max_u32_dpp v13, v93, v93 quad_perm:[1,0,3,2] row_mask:0xf bank_mask:0xf bound_ctrl:1
	v_cndmask_b32_e32 v96, v96, v94, vcc
	v_cndmask_b32_e32 v94, v94, v89, vcc
	v_max_u32_dpp v13, v13, v13 quad_perm:[2,3,0,1] row_mask:0xf bank_mask:0xf bound_ctrl:1
	v_cndmask_b32_e64 v89, v89, 0, vcc
	v_cmp_eq_u32_e32 vcc, v103, v21
	v_max_u32_dpp v13, v13, v13 row_half_mirror row_mask:0xf bank_mask:0xf bound_ctrl:1
	v_max_u32_dpp v29, v29, v29 quad_perm:[2,3,0,1] row_mask:0xf bank_mask:0xf bound_ctrl:1
	v_cndmask_b32_e32 v103, v103, v95, vcc
	v_max_u32_dpp v17, v13, v13 row_mirror row_mask:0xf bank_mask:0xf bound_ctrl:1
	v_max_u32_dpp v13, v79, v79 quad_perm:[1,0,3,2] row_mask:0xf bank_mask:0xf bound_ctrl:1
	v_cndmask_b32_e32 v95, v95, v107, vcc
	v_cndmask_b32_e32 v107, v107, v90, vcc
	v_max_u32_dpp v13, v13, v13 quad_perm:[2,3,0,1] row_mask:0xf bank_mask:0xf bound_ctrl:1
	v_cndmask_b32_e32 v90, v90, v80, vcc
	v_cndmask_b32_e32 v80, v80, v84, vcc
	v_max_u32_dpp v13, v13, v13 row_half_mirror row_mask:0xf bank_mask:0xf bound_ctrl:1
	v_cndmask_b32_e32 v84, v84, v106, vcc
	v_cndmask_b32_e32 v106, v106, v116, vcc
	v_cndmask_b32_e64 v116, v116, 0, vcc
	v_cmp_eq_u32_e32 vcc, v93, v17
	v_max_u32_dpp v13, v13, v13 row_mirror row_mask:0xf bank_mask:0xf bound_ctrl:1
	v_max_u32_dpp v29, v29, v29 row_half_mirror row_mask:0xf bank_mask:0xf bound_ctrl:1
	v_cndmask_b32_e32 v93, v93, v85, vcc
	v_cndmask_b32_e32 v85, v85, v108, vcc
	v_cndmask_b32_e32 v108, v108, v81, vcc
	v_cndmask_b32_e32 v81, v81, v88, vcc
	v_cndmask_b32_e32 v88, v88, v75, vcc
	v_cndmask_b32_e32 v75, v75, v99, vcc
	v_cndmask_b32_e32 v99, v99, v73, vcc
	v_cndmask_b32_e64 v73, v73, 0, vcc
	v_cmp_eq_u32_e32 vcc, v79, v13
	v_max_u32_dpp v29, v29, v29 row_mirror row_mask:0xf bank_mask:0xf bound_ctrl:1
	v_cndmask_b32_e64 v111, v111, v29, s[44:45]
	v_cndmask_b32_e32 v79, v79, v74, vcc
	v_cndmask_b32_e32 v74, v74, v83, vcc
	v_cndmask_b32_e32 v83, v83, v71, vcc
	v_cndmask_b32_e32 v71, v71, v110, vcc
	v_cndmask_b32_e32 v110, v110, v70, vcc
	v_cndmask_b32_e32 v70, v70, v76, vcc
	v_cndmask_b32_e32 v76, v76, v109, vcc
	v_cndmask_b32_e64 v109, v109, 0, vcc
	v_cmp_eq_u32_e32 vcc, v16, v29
	s_nop 1
	v_cndmask_b32_e32 v124, v16, v117, vcc
	v_max_u32_dpp v16, v66, v66 quad_perm:[1,0,3,2] row_mask:0xf bank_mask:0xf bound_ctrl:1
	v_cndmask_b32_e32 v117, v117, v118, vcc
	v_cndmask_b32_e32 v118, v118, v112, vcc
	v_max_u32_dpp v16, v16, v16 quad_perm:[2,3,0,1] row_mask:0xf bank_mask:0xf bound_ctrl:1
	v_cndmask_b32_e32 v112, v112, v119, vcc
	v_cndmask_b32_e32 v119, v119, v113, vcc
	v_max_u32_dpp v16, v16, v16 row_half_mirror row_mask:0xf bank_mask:0xf bound_ctrl:1
	v_cndmask_b32_e32 v113, v113, v120, vcc
	v_cndmask_b32_e32 v120, v120, v114, vcc
	v_max_u32_dpp v29, v16, v16 row_mirror row_mask:0xf bank_mask:0xf bound_ctrl:1
	v_max_u32_dpp v16, v91, v91 quad_perm:[1,0,3,2] row_mask:0xf bank_mask:0xf bound_ctrl:1
	v_cndmask_b32_e64 v114, v114, 0, vcc
	v_cmp_eq_u32_e32 vcc, v66, v29
	v_max_u32_dpp v16, v16, v16 quad_perm:[2,3,0,1] row_mask:0xf bank_mask:0xf bound_ctrl:1
	s_nop 0
	v_cndmask_b32_e32 v66, v66, v121, vcc
	v_max_u32_dpp v16, v16, v16 row_half_mirror row_mask:0xf bank_mask:0xf bound_ctrl:1
	v_cndmask_b32_e32 v121, v121, v72, vcc
	v_cndmask_b32_e32 v72, v72, v64, vcc
	v_cndmask_b32_e32 v64, v64, v122, vcc
	v_cndmask_b32_e32 v122, v122, v20, vcc
	v_cndmask_b32_e32 v125, v20, v123, vcc
	v_max_u32_dpp v20, v16, v16 row_mirror row_mask:0xf bank_mask:0xf bound_ctrl:1
	v_max_u32_dpp v16, v86, v86 quad_perm:[1,0,3,2] row_mask:0xf bank_mask:0xf bound_ctrl:1
	v_cndmask_b32_e32 v123, v123, v19, vcc
	v_cndmask_b32_e64 v126, v19, 0, vcc
	v_max_u32_dpp v16, v16, v16 quad_perm:[2,3,0,1] row_mask:0xf bank_mask:0xf bound_ctrl:1
	v_max_u32_dpp v19, v104, v104 quad_perm:[1,0,3,2] row_mask:0xf bank_mask:0xf bound_ctrl:1
	v_cmp_eq_u32_e32 vcc, v91, v20
	v_max_u32_dpp v16, v16, v16 row_half_mirror row_mask:0xf bank_mask:0xf bound_ctrl:1
	v_max_u32_dpp v19, v19, v19 quad_perm:[2,3,0,1] row_mask:0xf bank_mask:0xf bound_ctrl:1
	v_cndmask_b32_e32 v91, v91, v77, vcc
	v_max_u32_dpp v16, v16, v16 row_mirror row_mask:0xf bank_mask:0xf bound_ctrl:1
	v_max_u32_dpp v19, v19, v19 row_half_mirror row_mask:0xf bank_mask:0xf bound_ctrl:1
	v_cndmask_b32_e32 v77, v77, v98, vcc
	v_cndmask_b32_e32 v98, v98, v87, vcc
	v_cndmask_b32_e32 v87, v87, v69, vcc
	v_cndmask_b32_e32 v69, v69, v68, vcc
	v_cndmask_b32_e32 v127, v68, v65, vcc
	v_cndmask_b32_e32 v128, v65, v27, vcc
	v_cndmask_b32_e64 v129, v27, 0, vcc
	v_cmp_eq_u32_e32 vcc, v86, v16
	v_max_u32_dpp v19, v19, v19 row_mirror row_mask:0xf bank_mask:0xf bound_ctrl:1
	v_cndmask_b32_e64 v115, v115, v19, s[44:45]
	v_cndmask_b32_e32 v86, v86, v78, vcc
	v_cndmask_b32_e32 v78, v78, v97, vcc
	v_cndmask_b32_e32 v97, v97, v92, vcc
	v_cndmask_b32_e32 v92, v92, v67, vcc
	v_cndmask_b32_e32 v67, v67, v82, vcc
	v_cndmask_b32_e32 v82, v82, v31, vcc
	v_cndmask_b32_e32 v31, v31, v25, vcc
	v_cndmask_b32_e64 v130, v25, 0, vcc
	v_cmp_eq_u32_e32 vcc, v104, v19
	v_max_u32_dpp v19, v103, v103 quad_perm:[1,0,3,2] row_mask:0xf bank_mask:0xf bound_ctrl:1
	v_max_u32_dpp v25, v124, v124 quad_perm:[1,0,3,2] row_mask:0xf bank_mask:0xf bound_ctrl:1
	v_cndmask_b32_e32 v104, v104, v101, vcc
	v_max_u32_dpp v19, v19, v19 quad_perm:[2,3,0,1] row_mask:0xf bank_mask:0xf bound_ctrl:1
	v_cndmask_b32_e32 v101, v101, v105, vcc
	v_cndmask_b32_e32 v105, v105, v100, vcc
	v_max_u32_dpp v19, v19, v19 row_half_mirror row_mask:0xf bank_mask:0xf bound_ctrl:1
	v_cndmask_b32_e32 v100, v100, v102, vcc
	v_cndmask_b32_e32 v102, v102, v96, vcc
	v_max_u32_dpp v65, v19, v19 row_mirror row_mask:0xf bank_mask:0xf bound_ctrl:1
	v_max_u32_dpp v19, v93, v93 quad_perm:[1,0,3,2] row_mask:0xf bank_mask:0xf bound_ctrl:1
	v_cndmask_b32_e32 v96, v96, v94, vcc
	v_cndmask_b32_e32 v94, v94, v89, vcc
	v_max_u32_dpp v19, v19, v19 quad_perm:[2,3,0,1] row_mask:0xf bank_mask:0xf bound_ctrl:1
	v_cndmask_b32_e64 v89, v89, 0, vcc
	v_cmp_eq_u32_e32 vcc, v103, v65
	v_max_u32_dpp v19, v19, v19 row_half_mirror row_mask:0xf bank_mask:0xf bound_ctrl:1
	v_max_u32_dpp v25, v25, v25 quad_perm:[2,3,0,1] row_mask:0xf bank_mask:0xf bound_ctrl:1
	v_cndmask_b32_e32 v103, v103, v95, vcc
	v_max_u32_dpp v27, v19, v19 row_mirror row_mask:0xf bank_mask:0xf bound_ctrl:1
	v_max_u32_dpp v19, v79, v79 quad_perm:[1,0,3,2] row_mask:0xf bank_mask:0xf bound_ctrl:1
	v_cndmask_b32_e32 v95, v95, v107, vcc
	v_cndmask_b32_e32 v107, v107, v90, vcc
	v_max_u32_dpp v19, v19, v19 quad_perm:[2,3,0,1] row_mask:0xf bank_mask:0xf bound_ctrl:1
	v_cndmask_b32_e32 v90, v90, v80, vcc
	v_cndmask_b32_e32 v80, v80, v84, vcc
	v_max_u32_dpp v19, v19, v19 row_half_mirror row_mask:0xf bank_mask:0xf bound_ctrl:1
	v_cndmask_b32_e32 v84, v84, v106, vcc
	v_cndmask_b32_e32 v106, v106, v116, vcc
	v_cndmask_b32_e64 v116, v116, 0, vcc
	v_cmp_eq_u32_e32 vcc, v93, v27
	v_max_u32_dpp v19, v19, v19 row_mirror row_mask:0xf bank_mask:0xf bound_ctrl:1
	v_max_u32_dpp v25, v25, v25 row_half_mirror row_mask:0xf bank_mask:0xf bound_ctrl:1
	v_cndmask_b32_e32 v93, v93, v85, vcc
	v_cndmask_b32_e32 v85, v85, v108, vcc
	v_cndmask_b32_e32 v108, v108, v81, vcc
	v_cndmask_b32_e32 v81, v81, v88, vcc
	v_cndmask_b32_e32 v88, v88, v75, vcc
	v_cndmask_b32_e32 v75, v75, v99, vcc
	v_cndmask_b32_e32 v99, v99, v73, vcc
	v_cndmask_b32_e64 v73, v73, 0, vcc
	v_cmp_eq_u32_e32 vcc, v79, v19
	v_max_u32_dpp v25, v25, v25 row_mirror row_mask:0xf bank_mask:0xf bound_ctrl:1
	v_cndmask_b32_e64 v111, v111, v25, s[46:47]
	v_cndmask_b32_e32 v79, v79, v74, vcc
	v_cndmask_b32_e32 v74, v74, v83, vcc
	v_cndmask_b32_e32 v83, v83, v71, vcc
	v_cndmask_b32_e32 v131, v71, v110, vcc
	v_cndmask_b32_e32 v110, v110, v70, vcc
	v_cndmask_b32_e32 v70, v70, v76, vcc
	v_cndmask_b32_e32 v76, v76, v109, vcc
	v_cndmask_b32_e64 v109, v109, 0, vcc
	v_cmp_eq_u32_e32 vcc, v124, v25
	v_max_u32_dpp v25, v66, v66 quad_perm:[1,0,3,2] row_mask:0xf bank_mask:0xf bound_ctrl:1
	s_nop 0
	v_cndmask_b32_e32 v124, v124, v117, vcc
	v_max_u32_dpp v25, v25, v25 quad_perm:[2,3,0,1] row_mask:0xf bank_mask:0xf bound_ctrl:1
	v_cndmask_b32_e32 v117, v117, v118, vcc
	v_cndmask_b32_e32 v118, v118, v112, vcc
	v_max_u32_dpp v25, v25, v25 row_half_mirror row_mask:0xf bank_mask:0xf bound_ctrl:1
	v_cndmask_b32_e32 v112, v112, v119, vcc
	v_cndmask_b32_e32 v119, v119, v113, vcc
	v_max_u32_dpp v68, v25, v25 row_mirror row_mask:0xf bank_mask:0xf bound_ctrl:1
	v_max_u32_dpp v25, v91, v91 quad_perm:[1,0,3,2] row_mask:0xf bank_mask:0xf bound_ctrl:1
	v_cndmask_b32_e32 v113, v113, v120, vcc
	v_cndmask_b32_e32 v120, v120, v114, vcc
	v_max_u32_dpp v25, v25, v25 quad_perm:[2,3,0,1] row_mask:0xf bank_mask:0xf bound_ctrl:1
	v_cndmask_b32_e64 v114, v114, 0, vcc
	v_cmp_eq_u32_e32 vcc, v66, v68
	v_max_u32_dpp v25, v25, v25 row_half_mirror row_mask:0xf bank_mask:0xf bound_ctrl:1
	s_nop 0
	v_cndmask_b32_e32 v66, v66, v121, vcc
	v_cndmask_b32_e32 v121, v121, v72, vcc
	v_cndmask_b32_e32 v72, v72, v64, vcc
	v_cndmask_b32_e32 v132, v64, v122, vcc
	v_max_u32_dpp v64, v25, v25 row_mirror row_mask:0xf bank_mask:0xf bound_ctrl:1
	v_max_u32_dpp v25, v86, v86 quad_perm:[1,0,3,2] row_mask:0xf bank_mask:0xf bound_ctrl:1
	v_cndmask_b32_e32 v122, v122, v125, vcc
	v_cndmask_b32_e32 v125, v125, v123, vcc
	v_max_u32_dpp v25, v25, v25 quad_perm:[2,3,0,1] row_mask:0xf bank_mask:0xf bound_ctrl:1
	v_cndmask_b32_e32 v123, v123, v126, vcc
	v_cndmask_b32_e64 v126, v126, 0, vcc
	v_max_u32_dpp v25, v25, v25 row_half_mirror row_mask:0xf bank_mask:0xf bound_ctrl:1
	v_cmp_eq_u32_e32 vcc, v91, v64
	s_nop 0
	v_max_u32_dpp v25, v25, v25 row_mirror row_mask:0xf bank_mask:0xf bound_ctrl:1
	v_cndmask_b32_e32 v91, v91, v77, vcc
	v_cndmask_b32_e32 v77, v77, v98, vcc
	v_cndmask_b32_e32 v98, v98, v87, vcc
	v_cndmask_b32_e32 v87, v87, v69, vcc
	v_cndmask_b32_e32 v69, v69, v127, vcc
	v_cndmask_b32_e32 v127, v127, v128, vcc
	v_cndmask_b32_e32 v128, v128, v129, vcc
	v_cndmask_b32_e64 v129, v129, 0, vcc
	v_cmp_eq_u32_e32 vcc, v86, v25
	s_nop 1
	v_cndmask_b32_e32 v133, v67, v82, vcc
	v_cndmask_b32_e32 v82, v82, v31, vcc
	v_cndmask_b32_e32 v134, v31, v130, vcc
	v_max_u32_dpp v31, v104, v104 quad_perm:[1,0,3,2] row_mask:0xf bank_mask:0xf bound_ctrl:1
	v_cndmask_b32_e32 v86, v86, v78, vcc
	v_cndmask_b32_e32 v78, v78, v97, vcc
	v_max_u32_dpp v31, v31, v31 quad_perm:[2,3,0,1] row_mask:0xf bank_mask:0xf bound_ctrl:1
	v_cndmask_b32_e32 v97, v97, v92, vcc
	v_cndmask_b32_e32 v92, v92, v67, vcc
	v_max_u32_dpp v31, v31, v31 row_half_mirror row_mask:0xf bank_mask:0xf bound_ctrl:1
	v_cndmask_b32_e64 v130, v130, 0, vcc
	s_nop 0
	v_max_u32_dpp v31, v31, v31 row_mirror row_mask:0xf bank_mask:0xf bound_ctrl:1
	v_cndmask_b32_e64 v115, v115, v31, s[46:47]
	v_cmp_eq_u32_e32 vcc, v104, v31
	v_max_u32_dpp v31, v103, v103 quad_perm:[1,0,3,2] row_mask:0xf bank_mask:0xf bound_ctrl:1
	s_nop 0
	v_cndmask_b32_e32 v104, v104, v101, vcc
	v_max_u32_dpp v31, v31, v31 quad_perm:[2,3,0,1] row_mask:0xf bank_mask:0xf bound_ctrl:1
	v_cndmask_b32_e32 v101, v101, v105, vcc
	v_cndmask_b32_e32 v105, v105, v100, vcc
	v_max_u32_dpp v31, v31, v31 row_half_mirror row_mask:0xf bank_mask:0xf bound_ctrl:1
	v_cndmask_b32_e32 v100, v100, v102, vcc
	v_cndmask_b32_e32 v102, v102, v96, vcc
	v_max_u32_dpp v71, v31, v31 row_mirror row_mask:0xf bank_mask:0xf bound_ctrl:1
	v_max_u32_dpp v31, v93, v93 quad_perm:[1,0,3,2] row_mask:0xf bank_mask:0xf bound_ctrl:1
	v_cndmask_b32_e32 v96, v96, v94, vcc
	v_cndmask_b32_e32 v94, v94, v89, vcc
	v_max_u32_dpp v31, v31, v31 quad_perm:[2,3,0,1] row_mask:0xf bank_mask:0xf bound_ctrl:1
	v_cndmask_b32_e64 v89, v89, 0, vcc
	v_cmp_eq_u32_e32 vcc, v103, v71
	v_max_u32_dpp v31, v31, v31 row_half_mirror row_mask:0xf bank_mask:0xf bound_ctrl:1
	s_nop 0
	v_cndmask_b32_e32 v103, v103, v95, vcc
	v_max_u32_dpp v67, v31, v31 row_mirror row_mask:0xf bank_mask:0xf bound_ctrl:1
	v_max_u32_dpp v31, v79, v79 quad_perm:[1,0,3,2] row_mask:0xf bank_mask:0xf bound_ctrl:1
	v_cndmask_b32_e32 v95, v95, v107, vcc
	v_cndmask_b32_e32 v107, v107, v90, vcc
	v_max_u32_dpp v31, v31, v31 quad_perm:[2,3,0,1] row_mask:0xf bank_mask:0xf bound_ctrl:1
	v_cndmask_b32_e32 v90, v90, v80, vcc
	v_cndmask_b32_e32 v80, v80, v84, vcc
	v_max_u32_dpp v31, v31, v31 row_half_mirror row_mask:0xf bank_mask:0xf bound_ctrl:1
	v_cndmask_b32_e32 v84, v84, v106, vcc
	v_cndmask_b32_e32 v106, v106, v116, vcc
	v_cndmask_b32_e64 v116, v116, 0, vcc
	v_cmp_eq_u32_e32 vcc, v93, v67
	v_max_u32_dpp v31, v31, v31 row_mirror row_mask:0xf bank_mask:0xf bound_ctrl:1
	s_nop 0
	v_cndmask_b32_e32 v93, v93, v85, vcc
	v_cndmask_b32_e32 v85, v85, v108, vcc
	v_cndmask_b32_e32 v108, v108, v81, vcc
	v_cndmask_b32_e32 v81, v81, v88, vcc
	v_cndmask_b32_e32 v88, v88, v75, vcc
	v_cndmask_b32_e32 v75, v75, v99, vcc
	v_cndmask_b32_e32 v99, v99, v73, vcc
	v_cndmask_b32_e64 v135, v73, 0, vcc
	v_cmp_eq_u32_e32 vcc, v79, v31
	s_nop 1
	v_cndmask_b32_e32 v136, v74, v83, vcc
	v_cndmask_b32_e32 v83, v83, v131, vcc
	v_cndmask_b32_e32 v131, v131, v110, vcc
	v_cndmask_b32_e32 v110, v110, v70, vcc
	v_cndmask_b32_e32 v137, v70, v76, vcc
	v_max_u32_dpp v70, v124, v124 quad_perm:[1,0,3,2] row_mask:0xf bank_mask:0xf bound_ctrl:1
	v_cndmask_b32_e32 v79, v79, v74, vcc
	v_cndmask_b32_e32 v76, v76, v109, vcc
	v_max_u32_dpp v70, v70, v70 quad_perm:[2,3,0,1] row_mask:0xf bank_mask:0xf bound_ctrl:1
	v_cndmask_b32_e64 v109, v109, 0, vcc
	s_nop 0
	v_max_u32_dpp v70, v70, v70 row_half_mirror row_mask:0xf bank_mask:0xf bound_ctrl:1
	s_nop 1
	v_max_u32_dpp v70, v70, v70 row_mirror row_mask:0xf bank_mask:0xf bound_ctrl:1
	v_cndmask_b32_e64 v111, v111, v70, s[48:49]
	v_cmp_eq_u32_e32 vcc, v124, v70
	v_max_u32_dpp v70, v66, v66 quad_perm:[1,0,3,2] row_mask:0xf bank_mask:0xf bound_ctrl:1
	s_nop 0
	v_cndmask_b32_e32 v124, v124, v117, vcc
	v_max_u32_dpp v70, v70, v70 quad_perm:[2,3,0,1] row_mask:0xf bank_mask:0xf bound_ctrl:1
	v_cndmask_b32_e32 v117, v117, v118, vcc
	v_cndmask_b32_e32 v118, v118, v112, vcc
	v_max_u32_dpp v70, v70, v70 row_half_mirror row_mask:0xf bank_mask:0xf bound_ctrl:1
	v_cndmask_b32_e32 v112, v112, v119, vcc
	v_cndmask_b32_e32 v119, v119, v113, vcc
	v_max_u32_dpp v74, v70, v70 row_mirror row_mask:0xf bank_mask:0xf bound_ctrl:1
	v_cndmask_b32_e32 v113, v113, v120, vcc
	v_cndmask_b32_e32 v120, v120, v114, vcc
	v_cndmask_b32_e64 v114, v114, 0, vcc
	v_cmp_eq_u32_e32 vcc, v66, v74
	s_nop 1
	v_cndmask_b32_e32 v138, v66, v121, vcc
	v_max_u32_dpp v66, v91, v91 quad_perm:[1,0,3,2] row_mask:0xf bank_mask:0xf bound_ctrl:1
	v_cndmask_b32_e32 v121, v121, v72, vcc
	v_cndmask_b32_e32 v72, v72, v132, vcc
	v_max_u32_dpp v66, v66, v66 quad_perm:[2,3,0,1] row_mask:0xf bank_mask:0xf bound_ctrl:1
	v_cndmask_b32_e32 v132, v132, v122, vcc
	v_cndmask_b32_e32 v122, v122, v125, vcc
	v_max_u32_dpp v66, v66, v66 row_half_mirror row_mask:0xf bank_mask:0xf bound_ctrl:1
	v_cndmask_b32_e32 v125, v125, v123, vcc
	v_cndmask_b32_e32 v123, v123, v126, vcc
	v_max_u32_dpp v70, v66, v66 row_mirror row_mask:0xf bank_mask:0xf bound_ctrl:1
	v_cndmask_b32_e64 v126, v126, 0, vcc
	v_cmp_eq_u32_e32 vcc, v91, v70
	v_max_u32_dpp v66, v86, v86 quad_perm:[1,0,3,2] row_mask:0xf bank_mask:0xf bound_ctrl:1
	s_nop 0
	v_cndmask_b32_e32 v139, v77, v98, vcc
	v_cndmask_b32_e32 v98, v98, v87, vcc
	v_cndmask_b32_e32 v87, v87, v69, vcc
	v_cndmask_b32_e32 v140, v69, v127, vcc
	v_max_u32_dpp v66, v66, v66 quad_perm:[2,3,0,1] row_mask:0xf bank_mask:0xf bound_ctrl:1
	v_max_u32_dpp v69, v104, v104 quad_perm:[1,0,3,2] row_mask:0xf bank_mask:0xf bound_ctrl:1
	v_cndmask_b32_e32 v91, v91, v77, vcc
	v_max_u32_dpp v66, v66, v66 row_half_mirror row_mask:0xf bank_mask:0xf bound_ctrl:1
	v_max_u32_dpp v69, v69, v69 quad_perm:[2,3,0,1] row_mask:0xf bank_mask:0xf bound_ctrl:1
	v_cndmask_b32_e32 v127, v127, v128, vcc
	v_max_u32_dpp v66, v66, v66 row_mirror row_mask:0xf bank_mask:0xf bound_ctrl:1
	v_max_u32_dpp v69, v69, v69 row_half_mirror row_mask:0xf bank_mask:0xf bound_ctrl:1
	v_cndmask_b32_e32 v128, v128, v129, vcc
	v_cndmask_b32_e64 v129, v129, 0, vcc
	v_cmp_eq_u32_e32 vcc, v86, v66
	v_max_u32_dpp v69, v69, v69 row_mirror row_mask:0xf bank_mask:0xf bound_ctrl:1
	v_cndmask_b32_e64 v115, v115, v69, s[48:49]
	v_cndmask_b32_e32 v86, v86, v78, vcc
	v_cndmask_b32_e32 v78, v78, v97, vcc
	v_cndmask_b32_e32 v97, v97, v92, vcc
	v_cndmask_b32_e32 v92, v92, v133, vcc
	v_cndmask_b32_e32 v133, v133, v82, vcc
	v_cndmask_b32_e32 v82, v82, v134, vcc
	v_cndmask_b32_e32 v134, v134, v130, vcc
	v_cndmask_b32_e64 v130, v130, 0, vcc
	v_cmp_eq_u32_e32 vcc, v104, v69
	v_max_u32_dpp v69, v103, v103 quad_perm:[1,0,3,2] row_mask:0xf bank_mask:0xf bound_ctrl:1
	s_nop 0
	v_cndmask_b32_e32 v104, v104, v101, vcc
	v_max_u32_dpp v69, v69, v69 quad_perm:[2,3,0,1] row_mask:0xf bank_mask:0xf bound_ctrl:1
	v_cndmask_b32_e32 v101, v101, v105, vcc
	v_cndmask_b32_e32 v105, v105, v100, vcc
	v_max_u32_dpp v69, v69, v69 row_half_mirror row_mask:0xf bank_mask:0xf bound_ctrl:1
	v_cndmask_b32_e32 v100, v100, v102, vcc
	v_cndmask_b32_e32 v102, v102, v96, vcc
	v_max_u32_dpp v77, v69, v69 row_mirror row_mask:0xf bank_mask:0xf bound_ctrl:1
	v_max_u32_dpp v69, v93, v93 quad_perm:[1,0,3,2] row_mask:0xf bank_mask:0xf bound_ctrl:1
	v_cndmask_b32_e32 v96, v96, v94, vcc
	v_cndmask_b32_e32 v94, v94, v89, vcc
	v_max_u32_dpp v69, v69, v69 quad_perm:[2,3,0,1] row_mask:0xf bank_mask:0xf bound_ctrl:1
	v_cndmask_b32_e64 v89, v89, 0, vcc
	v_cmp_eq_u32_e32 vcc, v103, v77
	v_max_u32_dpp v69, v69, v69 row_half_mirror row_mask:0xf bank_mask:0xf bound_ctrl:1
	s_nop 0
	v_cndmask_b32_e32 v103, v103, v95, vcc
	v_max_u32_dpp v73, v69, v69 row_mirror row_mask:0xf bank_mask:0xf bound_ctrl:1
	v_max_u32_dpp v69, v79, v79 quad_perm:[1,0,3,2] row_mask:0xf bank_mask:0xf bound_ctrl:1
	v_cndmask_b32_e32 v95, v95, v107, vcc
	v_cndmask_b32_e32 v107, v107, v90, vcc
	v_max_u32_dpp v69, v69, v69 quad_perm:[2,3,0,1] row_mask:0xf bank_mask:0xf bound_ctrl:1
	v_cndmask_b32_e32 v90, v90, v80, vcc
	v_cndmask_b32_e32 v141, v80, v84, vcc
	v_max_u32_dpp v69, v69, v69 row_half_mirror row_mask:0xf bank_mask:0xf bound_ctrl:1
	v_cndmask_b32_e32 v84, v84, v106, vcc
	v_cndmask_b32_e32 v106, v106, v116, vcc
	v_cndmask_b32_e64 v116, v116, 0, vcc
	v_cmp_eq_u32_e32 vcc, v93, v73
	v_max_u32_dpp v69, v69, v69 row_mirror row_mask:0xf bank_mask:0xf bound_ctrl:1
	s_nop 0
	v_cndmask_b32_e32 v93, v93, v85, vcc
	v_cndmask_b32_e32 v85, v85, v108, vcc
	v_cndmask_b32_e32 v108, v108, v81, vcc
	v_cndmask_b32_e32 v81, v81, v88, vcc
	v_cndmask_b32_e32 v88, v88, v75, vcc
	v_cndmask_b32_e32 v75, v75, v99, vcc
	v_cndmask_b32_e32 v99, v99, v135, vcc
	v_cndmask_b32_e64 v135, v135, 0, vcc
	v_cmp_eq_u32_e32 vcc, v79, v69
	s_nop 1
	v_cndmask_b32_e32 v143, v83, v131, vcc
	v_cndmask_b32_e32 v131, v131, v110, vcc
	v_cndmask_b32_e32 v110, v110, v137, vcc
	v_cndmask_b32_e32 v137, v137, v76, vcc
	v_cndmask_b32_e32 v144, v76, v109, vcc
	v_max_u32_dpp v76, v124, v124 quad_perm:[1,0,3,2] row_mask:0xf bank_mask:0xf bound_ctrl:1
	v_cndmask_b32_e32 v142, v79, v136, vcc
	v_cndmask_b32_e32 v136, v136, v83, vcc
	v_max_u32_dpp v76, v76, v76 quad_perm:[2,3,0,1] row_mask:0xf bank_mask:0xf bound_ctrl:1
	v_cndmask_b32_e64 v109, v109, 0, vcc
	s_nop 0
	v_max_u32_dpp v76, v76, v76 row_half_mirror row_mask:0xf bank_mask:0xf bound_ctrl:1
	s_nop 1
	v_max_u32_dpp v76, v76, v76 row_mirror row_mask:0xf bank_mask:0xf bound_ctrl:1
	v_cndmask_b32_e64 v111, v111, v76, s[50:51]
	v_cmp_eq_u32_e32 vcc, v124, v76
	v_max_u32_dpp v76, v138, v138 quad_perm:[1,0,3,2] row_mask:0xf bank_mask:0xf bound_ctrl:1
	s_nop 0
	v_cndmask_b32_e32 v124, v124, v117, vcc
	v_max_u32_dpp v76, v76, v76 quad_perm:[2,3,0,1] row_mask:0xf bank_mask:0xf bound_ctrl:1
	v_cndmask_b32_e32 v117, v117, v118, vcc
	v_cndmask_b32_e32 v118, v118, v112, vcc
	v_max_u32_dpp v76, v76, v76 row_half_mirror row_mask:0xf bank_mask:0xf bound_ctrl:1
	v_cndmask_b32_e32 v112, v112, v119, vcc
	v_cndmask_b32_e32 v119, v119, v113, vcc
	v_max_u32_dpp v80, v76, v76 row_mirror row_mask:0xf bank_mask:0xf bound_ctrl:1
	v_cndmask_b32_e32 v113, v113, v120, vcc
	v_cndmask_b32_e32 v120, v120, v114, vcc
	v_cndmask_b32_e64 v114, v114, 0, vcc
	v_cmp_eq_u32_e32 vcc, v138, v80
	s_nop 1
	v_cndmask_b32_e32 v138, v138, v121, vcc
	v_cndmask_b32_e32 v121, v121, v72, vcc
	v_cndmask_b32_e32 v145, v72, v132, vcc
	v_max_u32_dpp v72, v91, v91 quad_perm:[1,0,3,2] row_mask:0xf bank_mask:0xf bound_ctrl:1
	v_cndmask_b32_e32 v132, v132, v122, vcc
	v_cndmask_b32_e32 v122, v122, v125, vcc
	v_max_u32_dpp v72, v72, v72 quad_perm:[2,3,0,1] row_mask:0xf bank_mask:0xf bound_ctrl:1
	v_cndmask_b32_e32 v125, v125, v123, vcc
	v_cndmask_b32_e32 v123, v123, v126, vcc
	v_max_u32_dpp v72, v72, v72 row_half_mirror row_mask:0xf bank_mask:0xf bound_ctrl:1
	v_cndmask_b32_e64 v126, v126, 0, vcc
	s_nop 0
	v_max_u32_dpp v76, v72, v72 row_mirror row_mask:0xf bank_mask:0xf bound_ctrl:1
	v_max_u32_dpp v72, v86, v86 quad_perm:[1,0,3,2] row_mask:0xf bank_mask:0xf bound_ctrl:1
	v_cmp_eq_u32_e32 vcc, v91, v76
	s_nop 0
	v_max_u32_dpp v72, v72, v72 quad_perm:[2,3,0,1] row_mask:0xf bank_mask:0xf bound_ctrl:1
	v_cndmask_b32_e32 v91, v91, v139, vcc
	v_cndmask_b32_e32 v139, v139, v98, vcc
	v_max_u32_dpp v72, v72, v72 row_half_mirror row_mask:0xf bank_mask:0xf bound_ctrl:1
	v_cndmask_b32_e32 v98, v98, v87, vcc
	v_cndmask_b32_e32 v87, v87, v140, vcc
	v_max_u32_dpp v72, v72, v72 row_mirror row_mask:0xf bank_mask:0xf bound_ctrl:1
	v_cndmask_b32_e32 v140, v140, v127, vcc
	v_cndmask_b32_e32 v127, v127, v128, vcc
	v_cndmask_b32_e32 v128, v128, v129, vcc
	v_cndmask_b32_e64 v129, v129, 0, vcc
	v_cmp_eq_u32_e32 vcc, v86, v72
	s_nop 1
	v_cndmask_b32_e32 v146, v86, v78, vcc
	v_cndmask_b32_e32 v147, v78, v97, vcc
	v_max_u32_dpp v78, v104, v104 quad_perm:[1,0,3,2] row_mask:0xf bank_mask:0xf bound_ctrl:1
	v_cndmask_b32_e32 v97, v97, v92, vcc
	v_cndmask_b32_e32 v92, v92, v133, vcc
	v_max_u32_dpp v78, v78, v78 quad_perm:[2,3,0,1] row_mask:0xf bank_mask:0xf bound_ctrl:1
	v_cndmask_b32_e32 v133, v133, v82, vcc
	v_cndmask_b32_e32 v148, v82, v134, vcc
	v_max_u32_dpp v78, v78, v78 row_half_mirror row_mask:0xf bank_mask:0xf bound_ctrl:1
	v_cndmask_b32_e32 v134, v134, v130, vcc
	v_cndmask_b32_e64 v130, v130, 0, vcc
	v_max_u32_dpp v78, v78, v78 row_mirror row_mask:0xf bank_mask:0xf bound_ctrl:1
	v_cndmask_b32_e64 v115, v115, v78, s[50:51]
	v_cmp_eq_u32_e32 vcc, v104, v78
	v_max_u32_dpp v78, v103, v103 quad_perm:[1,0,3,2] row_mask:0xf bank_mask:0xf bound_ctrl:1
	s_nop 0
	v_cndmask_b32_e32 v104, v104, v101, vcc
	v_max_u32_dpp v78, v78, v78 quad_perm:[2,3,0,1] row_mask:0xf bank_mask:0xf bound_ctrl:1
	v_cndmask_b32_e32 v101, v101, v105, vcc
	v_cndmask_b32_e32 v105, v105, v100, vcc
	v_max_u32_dpp v78, v78, v78 row_half_mirror row_mask:0xf bank_mask:0xf bound_ctrl:1
	v_cndmask_b32_e32 v100, v100, v102, vcc
	v_cndmask_b32_e32 v102, v102, v96, vcc
	v_max_u32_dpp v83, v78, v78 row_mirror row_mask:0xf bank_mask:0xf bound_ctrl:1
	v_max_u32_dpp v78, v93, v93 quad_perm:[1,0,3,2] row_mask:0xf bank_mask:0xf bound_ctrl:1
	v_cndmask_b32_e32 v96, v96, v94, vcc
	v_cndmask_b32_e32 v94, v94, v89, vcc
	v_max_u32_dpp v78, v78, v78 quad_perm:[2,3,0,1] row_mask:0xf bank_mask:0xf bound_ctrl:1
	v_cndmask_b32_e64 v89, v89, 0, vcc
	v_cmp_eq_u32_e32 vcc, v103, v83
	v_max_u32_dpp v78, v78, v78 row_half_mirror row_mask:0xf bank_mask:0xf bound_ctrl:1
	s_nop 0
	v_cndmask_b32_e32 v103, v103, v95, vcc
	v_max_u32_dpp v79, v78, v78 row_mirror row_mask:0xf bank_mask:0xf bound_ctrl:1
	v_cndmask_b32_e32 v95, v95, v107, vcc
	v_cndmask_b32_e32 v107, v107, v90, vcc
	v_cndmask_b32_e32 v90, v90, v141, vcc
	v_cndmask_b32_e32 v141, v141, v84, vcc
	v_cndmask_b32_e32 v84, v84, v106, vcc
	v_cndmask_b32_e32 v106, v106, v116, vcc
	v_cndmask_b32_e64 v116, v116, 0, vcc
	v_cmp_eq_u32_e32 vcc, v93, v79
	v_max_u32_dpp v78, v124, v124 quad_perm:[1,0,3,2] row_mask:0xf bank_mask:0xf bound_ctrl:1
	s_nop 0
	v_cndmask_b32_e32 v149, v85, v108, vcc
	v_cndmask_b32_e32 v108, v108, v81, vcc
	v_cndmask_b32_e32 v81, v81, v88, vcc
	v_cndmask_b32_e32 v88, v88, v75, vcc
	v_cndmask_b32_e32 v150, v75, v99, vcc
	v_max_u32_dpp v75, v142, v142 quad_perm:[1,0,3,2] row_mask:0xf bank_mask:0xf bound_ctrl:1
	v_max_u32_dpp v78, v78, v78 quad_perm:[2,3,0,1] row_mask:0xf bank_mask:0xf bound_ctrl:1
	v_cndmask_b32_e32 v93, v93, v85, vcc
	v_max_u32_dpp v75, v75, v75 quad_perm:[2,3,0,1] row_mask:0xf bank_mask:0xf bound_ctrl:1
	v_max_u32_dpp v78, v78, v78 row_half_mirror row_mask:0xf bank_mask:0xf bound_ctrl:1
	v_cndmask_b32_e32 v99, v99, v135, vcc
	v_max_u32_dpp v75, v75, v75 row_half_mirror row_mask:0xf bank_mask:0xf bound_ctrl:1
	v_cndmask_b32_e64 v135, v135, 0, vcc
	v_max_u32_dpp v78, v78, v78 row_mirror row_mask:0xf bank_mask:0xf bound_ctrl:1
	v_max_u32_dpp v75, v75, v75 row_mirror row_mask:0xf bank_mask:0xf bound_ctrl:1
	v_cmp_eq_u32_e32 vcc, v142, v75
	v_cndmask_b32_e64 v111, v111, v78, s[52:53]
	v_max_u32_dpp v85, v104, v104 quad_perm:[1,0,3,2] row_mask:0xf bank_mask:0xf bound_ctrl:1
	v_cndmask_b32_e32 v142, v142, v136, vcc
	v_cndmask_b32_e32 v136, v136, v143, vcc
	v_cndmask_b32_e32 v143, v143, v131, vcc
	v_cndmask_b32_e32 v131, v131, v110, vcc
	v_cndmask_b32_e32 v110, v110, v137, vcc
	v_cndmask_b32_e32 v137, v137, v144, vcc
	v_cndmask_b32_e32 v144, v144, v109, vcc
	v_cndmask_b32_e64 v109, v109, 0, vcc
	v_cmp_eq_u32_e32 vcc, v124, v78
	v_max_u32_dpp v78, v138, v138 quad_perm:[1,0,3,2] row_mask:0xf bank_mask:0xf bound_ctrl:1
	v_max_u32_dpp v85, v85, v85 quad_perm:[2,3,0,1] row_mask:0xf bank_mask:0xf bound_ctrl:1
	v_cndmask_b32_e32 v124, v124, v117, vcc
	v_max_u32_dpp v78, v78, v78 quad_perm:[2,3,0,1] row_mask:0xf bank_mask:0xf bound_ctrl:1
	v_cndmask_b32_e32 v117, v117, v118, vcc
	v_cndmask_b32_e32 v118, v118, v112, vcc
	v_max_u32_dpp v78, v78, v78 row_half_mirror row_mask:0xf bank_mask:0xf bound_ctrl:1
	v_cndmask_b32_e32 v112, v112, v119, vcc
	v_cndmask_b32_e32 v119, v119, v113, vcc
	v_max_u32_dpp v86, v78, v78 row_mirror row_mask:0xf bank_mask:0xf bound_ctrl:1
	v_max_u32_dpp v78, v91, v91 quad_perm:[1,0,3,2] row_mask:0xf bank_mask:0xf bound_ctrl:1
	v_cndmask_b32_e32 v113, v113, v120, vcc
	v_cndmask_b32_e32 v120, v120, v114, vcc
	v_max_u32_dpp v78, v78, v78 quad_perm:[2,3,0,1] row_mask:0xf bank_mask:0xf bound_ctrl:1
	v_cndmask_b32_e64 v114, v114, 0, vcc
	v_cmp_eq_u32_e32 vcc, v138, v86
	v_max_u32_dpp v78, v78, v78 row_half_mirror row_mask:0xf bank_mask:0xf bound_ctrl:1
	v_max_u32_dpp v85, v85, v85 row_half_mirror row_mask:0xf bank_mask:0xf bound_ctrl:1
	v_cndmask_b32_e32 v138, v138, v121, vcc
	v_max_u32_dpp v82, v78, v78 row_mirror row_mask:0xf bank_mask:0xf bound_ctrl:1
	v_max_u32_dpp v78, v146, v146 quad_perm:[1,0,3,2] row_mask:0xf bank_mask:0xf bound_ctrl:1
	v_cndmask_b32_e32 v121, v121, v145, vcc
	v_cndmask_b32_e32 v145, v145, v132, vcc
	v_max_u32_dpp v78, v78, v78 quad_perm:[2,3,0,1] row_mask:0xf bank_mask:0xf bound_ctrl:1
	v_cndmask_b32_e32 v132, v132, v122, vcc
	v_cndmask_b32_e32 v122, v122, v125, vcc
	v_max_u32_dpp v78, v78, v78 row_half_mirror row_mask:0xf bank_mask:0xf bound_ctrl:1
	v_cndmask_b32_e32 v125, v125, v123, vcc
	v_cndmask_b32_e32 v123, v123, v126, vcc
	v_cndmask_b32_e64 v126, v126, 0, vcc
	v_cmp_eq_u32_e32 vcc, v91, v82
	v_max_u32_dpp v78, v78, v78 row_mirror row_mask:0xf bank_mask:0xf bound_ctrl:1
	v_max_u32_dpp v85, v85, v85 row_mirror row_mask:0xf bank_mask:0xf bound_ctrl:1
	v_cndmask_b32_e32 v91, v91, v139, vcc
	v_cndmask_b32_e32 v139, v139, v98, vcc
	v_cndmask_b32_e32 v98, v98, v87, vcc
	v_cndmask_b32_e32 v87, v87, v140, vcc
	v_cndmask_b32_e32 v140, v140, v127, vcc
	v_cndmask_b32_e32 v127, v127, v128, vcc
	v_cndmask_b32_e32 v128, v128, v129, vcc
	v_cndmask_b32_e64 v129, v129, 0, vcc
	v_cmp_eq_u32_e32 vcc, v146, v78
	v_cndmask_b32_e64 v115, v115, v85, s[52:53]
	s_nop 0
	v_cndmask_b32_e32 v146, v146, v147, vcc
	v_cndmask_b32_e32 v147, v147, v97, vcc
	v_cndmask_b32_e32 v97, v97, v92, vcc
	v_cndmask_b32_e32 v151, v92, v133, vcc
	v_cndmask_b32_e32 v133, v133, v148, vcc
	v_cndmask_b32_e32 v148, v148, v134, vcc
	v_cndmask_b32_e32 v134, v134, v130, vcc
	v_cndmask_b32_e64 v130, v130, 0, vcc
	v_cmp_eq_u32_e32 vcc, v104, v85
	v_max_u32_dpp v85, v103, v103 quad_perm:[1,0,3,2] row_mask:0xf bank_mask:0xf bound_ctrl:1
	s_nop 0
	v_cndmask_b32_e32 v104, v104, v101, vcc
	v_max_u32_dpp v85, v85, v85 quad_perm:[2,3,0,1] row_mask:0xf bank_mask:0xf bound_ctrl:1
	v_cndmask_b32_e32 v101, v101, v105, vcc
	v_cndmask_b32_e32 v105, v105, v100, vcc
	v_max_u32_dpp v85, v85, v85 row_half_mirror row_mask:0xf bank_mask:0xf bound_ctrl:1
	v_cndmask_b32_e32 v100, v100, v102, vcc
	v_cndmask_b32_e32 v102, v102, v96, vcc
	v_cndmask_b32_e32 v96, v96, v94, vcc
	v_cndmask_b32_e32 v94, v94, v89, vcc
	v_cndmask_b32_e64 v152, v89, 0, vcc
	v_max_u32_dpp v89, v85, v85 row_mirror row_mask:0xf bank_mask:0xf bound_ctrl:1
	v_cmp_eq_u32_e32 vcc, v103, v89
	s_nop 1
	v_cndmask_b32_e32 v153, v95, v107, vcc
	v_cndmask_b32_e32 v107, v107, v90, vcc
	v_cndmask_b32_e32 v90, v90, v141, vcc
	v_cndmask_b32_e32 v141, v141, v84, vcc
	v_cndmask_b32_e32 v154, v84, v106, vcc
	v_max_u32_dpp v84, v93, v93 quad_perm:[1,0,3,2] row_mask:0xf bank_mask:0xf bound_ctrl:1
	v_cndmask_b32_e32 v103, v103, v95, vcc
	v_cndmask_b32_e32 v106, v106, v116, vcc
	v_max_u32_dpp v84, v84, v84 quad_perm:[2,3,0,1] row_mask:0xf bank_mask:0xf bound_ctrl:1
	v_cndmask_b32_e64 v116, v116, 0, vcc
	s_nop 0
	v_max_u32_dpp v84, v84, v84 row_half_mirror row_mask:0xf bank_mask:0xf bound_ctrl:1
	s_nop 1
	v_max_u32_dpp v85, v84, v84 row_mirror row_mask:0xf bank_mask:0xf bound_ctrl:1
	v_cmp_eq_u32_e32 vcc, v93, v85
	v_max_u32_dpp v84, v124, v124 quad_perm:[1,0,3,2] row_mask:0xf bank_mask:0xf bound_ctrl:1
	s_nop 0
	v_cndmask_b32_e32 v93, v93, v149, vcc
	v_cndmask_b32_e32 v149, v149, v108, vcc
	v_cndmask_b32_e32 v108, v108, v81, vcc
	v_cndmask_b32_e32 v155, v81, v88, vcc
	v_max_u32_dpp v81, v142, v142 quad_perm:[1,0,3,2] row_mask:0xf bank_mask:0xf bound_ctrl:1
	v_max_u32_dpp v84, v84, v84 quad_perm:[2,3,0,1] row_mask:0xf bank_mask:0xf bound_ctrl:1
	v_cndmask_b32_e32 v156, v88, v150, vcc
	v_max_u32_dpp v81, v81, v81 quad_perm:[2,3,0,1] row_mask:0xf bank_mask:0xf bound_ctrl:1
	v_max_u32_dpp v84, v84, v84 row_half_mirror row_mask:0xf bank_mask:0xf bound_ctrl:1
	v_cndmask_b32_e32 v150, v150, v99, vcc
	v_max_u32_dpp v81, v81, v81 row_half_mirror row_mask:0xf bank_mask:0xf bound_ctrl:1
	v_cndmask_b32_e32 v99, v99, v135, vcc
	v_cndmask_b32_e64 v135, v135, 0, vcc
	v_max_u32_dpp v81, v81, v81 row_mirror row_mask:0xf bank_mask:0xf bound_ctrl:1
	v_cmp_eq_u32_e32 vcc, v142, v81
	v_max_u32_dpp v84, v84, v84 row_mirror row_mask:0xf bank_mask:0xf bound_ctrl:1
	v_cndmask_b32_e64 v111, v111, v84, s[54:55]
	v_cndmask_b32_e32 v142, v142, v136, vcc
	v_cndmask_b32_e32 v136, v136, v143, vcc
	v_cndmask_b32_e32 v143, v143, v131, vcc
	v_cndmask_b32_e32 v131, v131, v110, vcc
	v_cndmask_b32_e32 v110, v110, v137, vcc
	v_cndmask_b32_e32 v137, v137, v144, vcc
	v_cndmask_b32_e32 v144, v144, v109, vcc
	v_cndmask_b32_e64 v109, v109, 0, vcc
	v_cmp_eq_u32_e32 vcc, v124, v84
	v_max_u32_dpp v84, v138, v138 quad_perm:[1,0,3,2] row_mask:0xf bank_mask:0xf bound_ctrl:1
	s_nop 0
	v_cndmask_b32_e32 v124, v124, v117, vcc
	v_max_u32_dpp v84, v84, v84 quad_perm:[2,3,0,1] row_mask:0xf bank_mask:0xf bound_ctrl:1
	v_cndmask_b32_e32 v117, v117, v118, vcc
	v_cndmask_b32_e32 v118, v118, v112, vcc
	v_max_u32_dpp v84, v84, v84 row_half_mirror row_mask:0xf bank_mask:0xf bound_ctrl:1
	v_cndmask_b32_e32 v112, v112, v119, vcc
	v_cndmask_b32_e32 v119, v119, v113, vcc
	v_max_u32_dpp v92, v84, v84 row_mirror row_mask:0xf bank_mask:0xf bound_ctrl:1
	v_max_u32_dpp v84, v91, v91 quad_perm:[1,0,3,2] row_mask:0xf bank_mask:0xf bound_ctrl:1
	v_cndmask_b32_e32 v113, v113, v120, vcc
	v_cndmask_b32_e32 v120, v120, v114, vcc
	v_max_u32_dpp v84, v84, v84 quad_perm:[2,3,0,1] row_mask:0xf bank_mask:0xf bound_ctrl:1
	v_cndmask_b32_e64 v114, v114, 0, vcc
	v_cmp_eq_u32_e32 vcc, v138, v92
	v_max_u32_dpp v84, v84, v84 row_half_mirror row_mask:0xf bank_mask:0xf bound_ctrl:1
	s_nop 0
	v_cndmask_b32_e32 v138, v138, v121, vcc
	v_max_u32_dpp v88, v84, v84 row_mirror row_mask:0xf bank_mask:0xf bound_ctrl:1
	v_cndmask_b32_e32 v121, v121, v145, vcc
	v_cndmask_b32_e32 v145, v145, v132, vcc
	v_cndmask_b32_e32 v132, v132, v122, vcc
	v_cndmask_b32_e32 v122, v122, v125, vcc
	v_cndmask_b32_e32 v125, v125, v123, vcc
	v_cndmask_b32_e32 v123, v123, v126, vcc
	v_cndmask_b32_e64 v126, v126, 0, vcc
	v_cmp_eq_u32_e32 vcc, v91, v88
	v_max_u32_dpp v84, v146, v146 quad_perm:[1,0,3,2] row_mask:0xf bank_mask:0xf bound_ctrl:1
	s_nop 0
	v_cndmask_b32_e32 v158, v98, v87, vcc
	v_cndmask_b32_e32 v159, v87, v140, vcc
	v_max_u32_dpp v84, v84, v84 quad_perm:[2,3,0,1] row_mask:0xf bank_mask:0xf bound_ctrl:1
	v_max_u32_dpp v87, v104, v104 quad_perm:[1,0,3,2] row_mask:0xf bank_mask:0xf bound_ctrl:1
	v_cndmask_b32_e32 v157, v91, v139, vcc
	v_max_u32_dpp v84, v84, v84 row_half_mirror row_mask:0xf bank_mask:0xf bound_ctrl:1
	v_max_u32_dpp v87, v87, v87 quad_perm:[2,3,0,1] row_mask:0xf bank_mask:0xf bound_ctrl:1
	v_cndmask_b32_e32 v139, v139, v98, vcc
	v_max_u32_dpp v84, v84, v84 row_mirror row_mask:0xf bank_mask:0xf bound_ctrl:1
	v_max_u32_dpp v87, v87, v87 row_half_mirror row_mask:0xf bank_mask:0xf bound_ctrl:1
	v_cndmask_b32_e32 v140, v140, v127, vcc
	v_cndmask_b32_e32 v127, v127, v128, vcc
	v_cndmask_b32_e32 v128, v128, v129, vcc
	v_cndmask_b32_e64 v129, v129, 0, vcc
	v_cmp_eq_u32_e32 vcc, v146, v84
	v_max_u32_dpp v87, v87, v87 row_mirror row_mask:0xf bank_mask:0xf bound_ctrl:1
	v_cndmask_b32_e64 v115, v115, v87, s[54:55]
	v_cndmask_b32_e32 v146, v146, v147, vcc
	v_cndmask_b32_e32 v147, v147, v97, vcc
	v_cndmask_b32_e32 v97, v97, v151, vcc
	v_cndmask_b32_e32 v151, v151, v133, vcc
	v_cndmask_b32_e32 v133, v133, v148, vcc
	v_cndmask_b32_e32 v148, v148, v134, vcc
	v_cndmask_b32_e32 v134, v134, v130, vcc
	v_cndmask_b32_e64 v130, v130, 0, vcc
	v_cmp_eq_u32_e32 vcc, v104, v87
	v_max_u32_dpp v87, v103, v103 quad_perm:[1,0,3,2] row_mask:0xf bank_mask:0xf bound_ctrl:1
	s_nop 0
	v_cndmask_b32_e32 v104, v104, v101, vcc
	v_max_u32_dpp v87, v87, v87 quad_perm:[2,3,0,1] row_mask:0xf bank_mask:0xf bound_ctrl:1
	v_cndmask_b32_e32 v101, v101, v105, vcc
	v_cndmask_b32_e32 v105, v105, v100, vcc
	v_max_u32_dpp v87, v87, v87 row_half_mirror row_mask:0xf bank_mask:0xf bound_ctrl:1
	v_cndmask_b32_e32 v100, v100, v102, vcc
	v_cndmask_b32_e32 v102, v102, v96, vcc
	v_max_u32_dpp v95, v87, v87 row_mirror row_mask:0xf bank_mask:0xf bound_ctrl:1
	v_max_u32_dpp v87, v93, v93 quad_perm:[1,0,3,2] row_mask:0xf bank_mask:0xf bound_ctrl:1
	v_cndmask_b32_e32 v96, v96, v94, vcc
	v_cndmask_b32_e32 v160, v94, v152, vcc
	v_max_u32_dpp v87, v87, v87 quad_perm:[2,3,0,1] row_mask:0xf bank_mask:0xf bound_ctrl:1
	v_cndmask_b32_e64 v152, v152, 0, vcc
	v_cmp_eq_u32_e32 vcc, v103, v95
	v_max_u32_dpp v87, v87, v87 row_half_mirror row_mask:0xf bank_mask:0xf bound_ctrl:1
	s_nop 0
	v_cndmask_b32_e32 v103, v103, v153, vcc
	v_max_u32_dpp v91, v87, v87 row_mirror row_mask:0xf bank_mask:0xf bound_ctrl:1
	v_max_u32_dpp v87, v142, v142 quad_perm:[1,0,3,2] row_mask:0xf bank_mask:0xf bound_ctrl:1
	v_cndmask_b32_e32 v153, v153, v107, vcc
	v_cndmask_b32_e32 v107, v107, v90, vcc
	v_cndmask_b32_e32 v161, v90, v141, vcc
	v_max_u32_dpp v87, v87, v87 quad_perm:[2,3,0,1] row_mask:0xf bank_mask:0xf bound_ctrl:1
	v_max_u32_dpp v90, v124, v124 quad_perm:[1,0,3,2] row_mask:0xf bank_mask:0xf bound_ctrl:1
	v_cndmask_b32_e32 v141, v141, v154, vcc
	v_max_u32_dpp v87, v87, v87 row_half_mirror row_mask:0xf bank_mask:0xf bound_ctrl:1
	v_max_u32_dpp v90, v90, v90 quad_perm:[2,3,0,1] row_mask:0xf bank_mask:0xf bound_ctrl:1
	v_cndmask_b32_e32 v154, v154, v106, vcc
	v_cndmask_b32_e32 v106, v106, v116, vcc
	v_cndmask_b32_e64 v116, v116, 0, vcc
	v_cmp_eq_u32_e32 vcc, v93, v91
	v_max_u32_dpp v87, v87, v87 row_mirror row_mask:0xf bank_mask:0xf bound_ctrl:1
	v_max_u32_dpp v90, v90, v90 row_half_mirror row_mask:0xf bank_mask:0xf bound_ctrl:1
	v_cndmask_b32_e32 v93, v93, v149, vcc
	v_cndmask_b32_e32 v149, v149, v108, vcc
	v_cndmask_b32_e32 v108, v108, v155, vcc
	v_cndmask_b32_e32 v155, v155, v156, vcc
	v_cndmask_b32_e32 v156, v156, v150, vcc
	v_cndmask_b32_e32 v150, v150, v99, vcc
	v_cndmask_b32_e32 v99, v99, v135, vcc
	v_cndmask_b32_e64 v135, v135, 0, vcc
	v_cmp_eq_u32_e32 vcc, v142, v87
	v_max_u32_dpp v90, v90, v90 row_mirror row_mask:0xf bank_mask:0xf bound_ctrl:1
	v_cndmask_b32_e64 v111, v111, v90, s[56:57]
	v_cndmask_b32_e32 v142, v142, v136, vcc
	v_cndmask_b32_e32 v136, v136, v143, vcc
	v_cndmask_b32_e32 v143, v143, v131, vcc
	v_cndmask_b32_e32 v131, v131, v110, vcc
	v_cndmask_b32_e32 v110, v110, v137, vcc
	v_cndmask_b32_e32 v137, v137, v144, vcc
	v_cndmask_b32_e32 v144, v144, v109, vcc
	v_cndmask_b32_e64 v109, v109, 0, vcc
	v_cmp_eq_u32_e32 vcc, v124, v90
	v_max_u32_dpp v90, v138, v138 quad_perm:[1,0,3,2] row_mask:0xf bank_mask:0xf bound_ctrl:1
	s_nop 0
	v_cndmask_b32_e32 v124, v124, v117, vcc
	v_max_u32_dpp v90, v90, v90 quad_perm:[2,3,0,1] row_mask:0xf bank_mask:0xf bound_ctrl:1
	v_cndmask_b32_e32 v117, v117, v118, vcc
	v_cndmask_b32_e32 v118, v118, v112, vcc
	v_max_u32_dpp v90, v90, v90 row_half_mirror row_mask:0xf bank_mask:0xf bound_ctrl:1
	v_cndmask_b32_e32 v112, v112, v119, vcc
	v_cndmask_b32_e32 v119, v119, v113, vcc
	v_max_u32_dpp v98, v90, v90 row_mirror row_mask:0xf bank_mask:0xf bound_ctrl:1
	v_max_u32_dpp v90, v157, v157 quad_perm:[1,0,3,2] row_mask:0xf bank_mask:0xf bound_ctrl:1
	v_cndmask_b32_e32 v113, v113, v120, vcc
	v_cndmask_b32_e32 v114, v120, v114, vcc
	v_max_u32_dpp v90, v90, v90 quad_perm:[2,3,0,1] row_mask:0xf bank_mask:0xf bound_ctrl:1
	v_cmp_eq_u32_e32 vcc, v138, v98
	s_nop 0
	v_max_u32_dpp v90, v90, v90 row_half_mirror row_mask:0xf bank_mask:0xf bound_ctrl:1
	v_cndmask_b32_e32 v120, v138, v121, vcc
	v_cndmask_b32_e32 v121, v121, v145, vcc
	v_max_u32_dpp v94, v90, v90 row_mirror row_mask:0xf bank_mask:0xf bound_ctrl:1
	v_max_u32_dpp v90, v146, v146 quad_perm:[1,0,3,2] row_mask:0xf bank_mask:0xf bound_ctrl:1
	v_cndmask_b32_e32 v138, v145, v132, vcc
	v_cndmask_b32_e32 v132, v132, v122, vcc
	v_max_u32_dpp v90, v90, v90 quad_perm:[2,3,0,1] row_mask:0xf bank_mask:0xf bound_ctrl:1
	v_cndmask_b32_e32 v122, v122, v125, vcc
	v_cndmask_b32_e32 v125, v125, v123, vcc
	v_max_u32_dpp v90, v90, v90 row_half_mirror row_mask:0xf bank_mask:0xf bound_ctrl:1
	v_cndmask_b32_e32 v123, v123, v126, vcc
	v_cmp_eq_u32_e32 vcc, v157, v94
	v_max_u32_dpp v90, v90, v90 row_mirror row_mask:0xf bank_mask:0xf bound_ctrl:1
	s_nop 0
	v_cndmask_b32_e32 v126, v157, v139, vcc
	v_cndmask_b32_e32 v139, v139, v158, vcc
	v_cndmask_b32_e32 v145, v158, v159, vcc
	v_cndmask_b32_e32 v157, v159, v140, vcc
	v_cndmask_b32_e32 v140, v140, v127, vcc
	v_cndmask_b32_e32 v127, v127, v128, vcc
	v_cndmask_b32_e32 v128, v128, v129, vcc
	v_cmp_eq_u32_e32 vcc, v146, v90
	s_nop 1
	v_cndmask_b32_e32 v129, v146, v147, vcc
	v_cndmask_b32_e32 v146, v147, v97, vcc
	v_cndmask_b32_e32 v147, v97, v151, vcc
	v_max_u32_dpp v97, v104, v104 quad_perm:[1,0,3,2] row_mask:0xf bank_mask:0xf bound_ctrl:1
	v_cndmask_b32_e32 v151, v151, v133, vcc
	v_cndmask_b32_e32 v133, v133, v148, vcc
	v_max_u32_dpp v97, v97, v97 quad_perm:[2,3,0,1] row_mask:0xf bank_mask:0xf bound_ctrl:1
	v_cndmask_b32_e32 v148, v148, v134, vcc
	v_cndmask_b32_e32 v130, v134, v130, vcc
	v_max_u32_dpp v97, v97, v97 row_half_mirror row_mask:0xf bank_mask:0xf bound_ctrl:1
	s_nop 1
	v_max_u32_dpp v97, v97, v97 row_mirror row_mask:0xf bank_mask:0xf bound_ctrl:1
	v_cmp_eq_u32_e32 vcc, v104, v97
	v_cndmask_b32_e64 v115, v115, v97, s[56:57]
	s_nop 0
	v_cndmask_b32_e32 v159, v100, v102, vcc
	v_cndmask_b32_e32 v102, v102, v96, vcc
	v_cndmask_b32_e32 v162, v96, v160, vcc
	v_max_u32_dpp v96, v103, v103 quad_perm:[1,0,3,2] row_mask:0xf bank_mask:0xf bound_ctrl:1
	v_cndmask_b32_e32 v134, v104, v101, vcc
	v_cndmask_b32_e32 v158, v101, v105, vcc
	v_max_u32_dpp v96, v96, v96 quad_perm:[2,3,0,1] row_mask:0xf bank_mask:0xf bound_ctrl:1
	v_cndmask_b32_e32 v105, v105, v100, vcc
	v_cndmask_b32_e32 v152, v160, v152, vcc
	v_max_u32_dpp v96, v96, v96 row_half_mirror row_mask:0xf bank_mask:0xf bound_ctrl:1
	s_nop 1
	v_max_u32_dpp v101, v96, v96 row_mirror row_mask:0xf bank_mask:0xf bound_ctrl:1
	v_max_u32_dpp v96, v93, v93 quad_perm:[1,0,3,2] row_mask:0xf bank_mask:0xf bound_ctrl:1
	v_cmp_eq_u32_e32 vcc, v103, v101
	s_nop 0
	v_max_u32_dpp v96, v96, v96 quad_perm:[2,3,0,1] row_mask:0xf bank_mask:0xf bound_ctrl:1
	v_cndmask_b32_e32 v103, v103, v153, vcc
	v_cndmask_b32_e32 v153, v153, v107, vcc
	v_max_u32_dpp v96, v96, v96 row_half_mirror row_mask:0xf bank_mask:0xf bound_ctrl:1
	v_cndmask_b32_e32 v107, v107, v161, vcc
	v_cndmask_b32_e32 v160, v161, v141, vcc
	v_max_u32_dpp v97, v96, v96 row_mirror row_mask:0xf bank_mask:0xf bound_ctrl:1
	v_cndmask_b32_e32 v141, v141, v154, vcc
	v_cndmask_b32_e32 v154, v154, v106, vcc
	v_cndmask_b32_e32 v106, v106, v116, vcc
	v_cmp_eq_u32_e32 vcc, v93, v97
	v_max_u32_dpp v96, v124, v124 quad_perm:[1,0,3,2] row_mask:0xf bank_mask:0xf bound_ctrl:1
	s_nop 0
	v_cndmask_b32_e32 v116, v93, v149, vcc
	v_max_u32_dpp v93, v142, v142 quad_perm:[1,0,3,2] row_mask:0xf bank_mask:0xf bound_ctrl:1
	v_max_u32_dpp v96, v96, v96 quad_perm:[2,3,0,1] row_mask:0xf bank_mask:0xf bound_ctrl:1
	v_cndmask_b32_e32 v149, v149, v108, vcc
	v_max_u32_dpp v93, v93, v93 quad_perm:[2,3,0,1] row_mask:0xf bank_mask:0xf bound_ctrl:1
	v_max_u32_dpp v96, v96, v96 row_half_mirror row_mask:0xf bank_mask:0xf bound_ctrl:1
	v_cndmask_b32_e32 v161, v108, v155, vcc
	v_max_u32_dpp v93, v93, v93 row_half_mirror row_mask:0xf bank_mask:0xf bound_ctrl:1
	v_cndmask_b32_e32 v155, v155, v156, vcc
	v_cndmask_b32_e32 v156, v156, v150, vcc
	v_max_u32_dpp v93, v93, v93 row_mirror row_mask:0xf bank_mask:0xf bound_ctrl:1
	v_cndmask_b32_e32 v150, v150, v99, vcc
	v_cndmask_b32_e32 v99, v99, v135, vcc
	v_cmp_eq_u32_e32 vcc, v142, v93
	v_max_u32_dpp v96, v96, v96 row_mirror row_mask:0xf bank_mask:0xf bound_ctrl:1
	v_cndmask_b32_e64 v111, v111, v96, s[58:59]
	v_cndmask_b32_e32 v135, v142, v136, vcc
	v_cndmask_b32_e32 v136, v136, v143, vcc
	v_cndmask_b32_e32 v142, v143, v131, vcc
	v_cndmask_b32_e32 v131, v131, v110, vcc
	v_cndmask_b32_e32 v110, v110, v137, vcc
	v_cndmask_b32_e32 v137, v137, v144, vcc
	v_cndmask_b32_e32 v109, v144, v109, vcc
	v_cmp_eq_u32_e32 vcc, v124, v96
	v_max_u32_dpp v96, v120, v120 quad_perm:[1,0,3,2] row_mask:0xf bank_mask:0xf bound_ctrl:1
	v_max_u32_dpp v108, v134, v134 quad_perm:[1,0,3,2] row_mask:0xf bank_mask:0xf bound_ctrl:1
	v_cndmask_b32_e32 v124, v124, v117, vcc
	v_max_u32_dpp v96, v96, v96 quad_perm:[2,3,0,1] row_mask:0xf bank_mask:0xf bound_ctrl:1
	v_cndmask_b32_e32 v117, v117, v118, vcc
	v_cndmask_b32_e32 v118, v118, v112, vcc
	v_max_u32_dpp v96, v96, v96 row_half_mirror row_mask:0xf bank_mask:0xf bound_ctrl:1
	v_cndmask_b32_e32 v112, v112, v119, vcc
	v_cndmask_b32_e32 v119, v119, v113, vcc
	v_max_u32_dpp v104, v96, v96 row_mirror row_mask:0xf bank_mask:0xf bound_ctrl:1
	v_max_u32_dpp v96, v126, v126 quad_perm:[1,0,3,2] row_mask:0xf bank_mask:0xf bound_ctrl:1
	v_cndmask_b32_e32 v113, v113, v114, vcc
	v_cmp_eq_u32_e32 vcc, v120, v104
	v_max_u32_dpp v96, v96, v96 quad_perm:[2,3,0,1] row_mask:0xf bank_mask:0xf bound_ctrl:1
	v_max_u32_dpp v108, v108, v108 quad_perm:[2,3,0,1] row_mask:0xf bank_mask:0xf bound_ctrl:1
	v_cndmask_b32_e32 v114, v120, v121, vcc
	v_max_u32_dpp v96, v96, v96 row_half_mirror row_mask:0xf bank_mask:0xf bound_ctrl:1
	v_cndmask_b32_e32 v120, v121, v138, vcc
	v_cndmask_b32_e32 v121, v138, v132, vcc
	v_max_u32_dpp v100, v96, v96 row_mirror row_mask:0xf bank_mask:0xf bound_ctrl:1
	v_max_u32_dpp v96, v129, v129 quad_perm:[1,0,3,2] row_mask:0xf bank_mask:0xf bound_ctrl:1
	v_cndmask_b32_e32 v132, v132, v122, vcc
	v_cndmask_b32_e32 v122, v122, v125, vcc
	v_max_u32_dpp v96, v96, v96 quad_perm:[2,3,0,1] row_mask:0xf bank_mask:0xf bound_ctrl:1
	v_cndmask_b32_e32 v123, v125, v123, vcc
	v_cmp_eq_u32_e32 vcc, v126, v100
	v_max_u32_dpp v96, v96, v96 row_half_mirror row_mask:0xf bank_mask:0xf bound_ctrl:1
	v_max_u32_dpp v108, v108, v108 row_half_mirror row_mask:0xf bank_mask:0xf bound_ctrl:1
	v_cndmask_b32_e32 v125, v126, v139, vcc
	v_max_u32_dpp v96, v96, v96 row_mirror row_mask:0xf bank_mask:0xf bound_ctrl:1
	v_cndmask_b32_e32 v126, v139, v145, vcc
	v_cndmask_b32_e32 v138, v145, v157, vcc
	v_cndmask_b32_e32 v139, v157, v140, vcc
	v_cndmask_b32_e32 v140, v140, v127, vcc
	v_cndmask_b32_e32 v127, v127, v128, vcc
	v_cmp_eq_u32_e32 vcc, v129, v96
	v_max_u32_dpp v108, v108, v108 row_mirror row_mask:0xf bank_mask:0xf bound_ctrl:1
	v_cndmask_b32_e64 v115, v115, v108, s[58:59]
	v_cndmask_b32_e32 v128, v129, v146, vcc
	v_cndmask_b32_e32 v129, v146, v147, vcc
	v_cndmask_b32_e32 v143, v147, v151, vcc
	v_cndmask_b32_e32 v144, v151, v133, vcc
	v_cndmask_b32_e32 v133, v133, v148, vcc
	v_cndmask_b32_e32 v130, v148, v130, vcc
	v_cmp_eq_u32_e32 vcc, v134, v108
	s_nop 1
	v_cndmask_b32_e32 v146, v159, v102, vcc
	v_cndmask_b32_e32 v147, v102, v162, vcc
	v_max_u32_dpp v102, v103, v103 quad_perm:[1,0,3,2] row_mask:0xf bank_mask:0xf bound_ctrl:1
	v_cndmask_b32_e32 v134, v134, v158, vcc
	v_cndmask_b32_e32 v145, v158, v105, vcc
	v_max_u32_dpp v102, v102, v102 quad_perm:[2,3,0,1] row_mask:0xf bank_mask:0xf bound_ctrl:1
	v_cndmask_b32_e32 v105, v105, v159, vcc
	v_cndmask_b32_e32 v148, v162, v152, vcc
	v_max_u32_dpp v102, v102, v102 row_half_mirror row_mask:0xf bank_mask:0xf bound_ctrl:1
	s_nop 1
	v_max_u32_dpp v108, v102, v102 row_mirror row_mask:0xf bank_mask:0xf bound_ctrl:1
	v_max_u32_dpp v102, v116, v116 quad_perm:[1,0,3,2] row_mask:0xf bank_mask:0xf bound_ctrl:1
	v_cmp_eq_u32_e32 vcc, v103, v108
	s_nop 0
	v_max_u32_dpp v102, v102, v102 quad_perm:[2,3,0,1] row_mask:0xf bank_mask:0xf bound_ctrl:1
	v_cndmask_b32_e32 v151, v103, v153, vcc
	v_cndmask_b32_e32 v152, v153, v107, vcc
	v_max_u32_dpp v102, v102, v102 row_half_mirror row_mask:0xf bank_mask:0xf bound_ctrl:1
	v_cndmask_b32_e32 v107, v107, v160, vcc
	v_cndmask_b32_e32 v153, v160, v141, vcc
	v_max_u32_dpp v103, v102, v102 row_mirror row_mask:0xf bank_mask:0xf bound_ctrl:1
	v_cndmask_b32_e32 v141, v141, v154, vcc
	v_cndmask_b32_e32 v154, v154, v106, vcc
	v_cmp_eq_u32_e32 vcc, v116, v103
	v_max_u32_dpp v102, v124, v124 quad_perm:[1,0,3,2] row_mask:0xf bank_mask:0xf bound_ctrl:1
	s_nop 0
	v_cndmask_b32_e32 v157, v161, v155, vcc
	v_cndmask_b32_e32 v155, v155, v156, vcc
	v_cndmask_b32_e32 v156, v156, v150, vcc
	v_cndmask_b32_e32 v150, v150, v99, vcc
	v_max_u32_dpp v99, v135, v135 quad_perm:[1,0,3,2] row_mask:0xf bank_mask:0xf bound_ctrl:1
	v_max_u32_dpp v102, v102, v102 quad_perm:[2,3,0,1] row_mask:0xf bank_mask:0xf bound_ctrl:1
	v_cndmask_b32_e32 v116, v116, v149, vcc
	v_max_u32_dpp v99, v99, v99 quad_perm:[2,3,0,1] row_mask:0xf bank_mask:0xf bound_ctrl:1
	v_max_u32_dpp v102, v102, v102 row_half_mirror row_mask:0xf bank_mask:0xf bound_ctrl:1
	v_cndmask_b32_e32 v149, v149, v161, vcc
	v_max_u32_dpp v99, v99, v99 row_half_mirror row_mask:0xf bank_mask:0xf bound_ctrl:1
	v_max_u32_dpp v102, v102, v102 row_mirror row_mask:0xf bank_mask:0xf bound_ctrl:1
	v_cndmask_b32_e64 v158, v111, v102, s[60:61]
	v_max_u32_dpp v99, v99, v99 row_mirror row_mask:0xf bank_mask:0xf bound_ctrl:1
	v_cmp_eq_u32_e32 vcc, v135, v99
	s_nop 1
	v_cndmask_b32_e32 v135, v135, v136, vcc
	v_cndmask_b32_e32 v136, v136, v142, vcc
	v_cndmask_b32_e32 v142, v142, v131, vcc
	v_cndmask_b32_e32 v131, v131, v110, vcc
	v_cndmask_b32_e32 v110, v110, v137, vcc
	v_cndmask_b32_e32 v137, v137, v109, vcc
	v_cmp_eq_u32_e32 vcc, v124, v102
	v_max_u32_dpp v102, v114, v114 quad_perm:[1,0,3,2] row_mask:0xf bank_mask:0xf bound_ctrl:1
	v_max_u32_dpp v109, v134, v134 quad_perm:[1,0,3,2] row_mask:0xf bank_mask:0xf bound_ctrl:1
	v_cndmask_b32_e32 v124, v124, v117, vcc
	v_max_u32_dpp v102, v102, v102 quad_perm:[2,3,0,1] row_mask:0xf bank_mask:0xf bound_ctrl:1
	v_cndmask_b32_e32 v117, v117, v118, vcc
	v_cndmask_b32_e32 v118, v118, v112, vcc
	v_max_u32_dpp v102, v102, v102 row_half_mirror row_mask:0xf bank_mask:0xf bound_ctrl:1
	v_cndmask_b32_e32 v112, v112, v119, vcc
	v_cndmask_b32_e32 v113, v119, v113, vcc
	v_max_u32_dpp v111, v102, v102 row_mirror row_mask:0xf bank_mask:0xf bound_ctrl:1
	v_max_u32_dpp v102, v125, v125 quad_perm:[1,0,3,2] row_mask:0xf bank_mask:0xf bound_ctrl:1
	v_cmp_eq_u32_e32 vcc, v114, v111
	v_max_u32_dpp v109, v109, v109 quad_perm:[2,3,0,1] row_mask:0xf bank_mask:0xf bound_ctrl:1
	v_max_u32_dpp v102, v102, v102 quad_perm:[2,3,0,1] row_mask:0xf bank_mask:0xf bound_ctrl:1
	v_cndmask_b32_e32 v119, v114, v120, vcc
	v_cndmask_b32_e32 v120, v120, v121, vcc
	v_max_u32_dpp v102, v102, v102 row_half_mirror row_mask:0xf bank_mask:0xf bound_ctrl:1
	v_cndmask_b32_e32 v121, v121, v132, vcc
	v_cndmask_b32_e32 v132, v132, v122, vcc
	v_max_u32_dpp v106, v102, v102 row_mirror row_mask:0xf bank_mask:0xf bound_ctrl:1
	v_max_u32_dpp v102, v128, v128 quad_perm:[1,0,3,2] row_mask:0xf bank_mask:0xf bound_ctrl:1
	v_cndmask_b32_e32 v122, v122, v123, vcc
	v_cmp_eq_u32_e32 vcc, v125, v106
	v_max_u32_dpp v102, v102, v102 quad_perm:[2,3,0,1] row_mask:0xf bank_mask:0xf bound_ctrl:1
	v_max_u32_dpp v109, v109, v109 row_half_mirror row_mask:0xf bank_mask:0xf bound_ctrl:1
	v_cndmask_b32_e32 v123, v125, v126, vcc
	v_max_u32_dpp v102, v102, v102 row_half_mirror row_mask:0xf bank_mask:0xf bound_ctrl:1
	v_cndmask_b32_e32 v125, v126, v138, vcc
	v_cndmask_b32_e32 v126, v138, v139, vcc
	v_max_u32_dpp v102, v102, v102 row_mirror row_mask:0xf bank_mask:0xf bound_ctrl:1
	v_cndmask_b32_e32 v138, v139, v140, vcc
	v_cndmask_b32_e32 v127, v140, v127, vcc
	v_cmp_eq_u32_e32 vcc, v128, v102
	v_max_u32_dpp v109, v109, v109 row_mirror row_mask:0xf bank_mask:0xf bound_ctrl:1
	v_cndmask_b32_e64 v115, v115, v109, s[60:61]
	v_cndmask_b32_e32 v128, v128, v129, vcc
	v_cndmask_b32_e32 v129, v129, v143, vcc
	v_cndmask_b32_e32 v139, v143, v144, vcc
	v_cndmask_b32_e32 v140, v144, v133, vcc
	v_cndmask_b32_e32 v130, v133, v130, vcc
	v_cmp_eq_u32_e32 vcc, v134, v109
	s_nop 1
	v_cndmask_b32_e32 v133, v134, v145, vcc
	v_cndmask_b32_e32 v134, v145, v105, vcc
	v_cndmask_b32_e32 v143, v105, v146, vcc
	v_max_u32_dpp v105, v151, v151 quad_perm:[1,0,3,2] row_mask:0xf bank_mask:0xf bound_ctrl:1
	v_cndmask_b32_e32 v144, v146, v147, vcc
	v_cndmask_b32_e32 v145, v147, v148, vcc
	v_max_u32_dpp v105, v105, v105 quad_perm:[2,3,0,1] row_mask:0xf bank_mask:0xf bound_ctrl:1
	s_nop 1
	v_max_u32_dpp v105, v105, v105 row_half_mirror row_mask:0xf bank_mask:0xf bound_ctrl:1
	s_nop 1
	v_max_u32_dpp v114, v105, v105 row_mirror row_mask:0xf bank_mask:0xf bound_ctrl:1
	v_max_u32_dpp v105, v116, v116 quad_perm:[1,0,3,2] row_mask:0xf bank_mask:0xf bound_ctrl:1
	v_cmp_eq_u32_e32 vcc, v151, v114
	s_nop 0
	v_max_u32_dpp v105, v105, v105 quad_perm:[2,3,0,1] row_mask:0xf bank_mask:0xf bound_ctrl:1
	v_cndmask_b32_e32 v147, v152, v107, vcc
	v_cndmask_b32_e32 v148, v107, v153, vcc
	v_max_u32_dpp v105, v105, v105 row_half_mirror row_mask:0xf bank_mask:0xf bound_ctrl:1
	v_max_u32_dpp v107, v124, v124 quad_perm:[1,0,3,2] row_mask:0xf bank_mask:0xf bound_ctrl:1
	v_cndmask_b32_e32 v146, v151, v152, vcc
	v_max_u32_dpp v109, v105, v105 row_mirror row_mask:0xf bank_mask:0xf bound_ctrl:1
	v_max_u32_dpp v105, v135, v135 quad_perm:[1,0,3,2] row_mask:0xf bank_mask:0xf bound_ctrl:1
	v_max_u32_dpp v107, v107, v107 quad_perm:[2,3,0,1] row_mask:0xf bank_mask:0xf bound_ctrl:1
	v_cndmask_b32_e32 v151, v153, v141, vcc
	v_max_u32_dpp v105, v105, v105 quad_perm:[2,3,0,1] row_mask:0xf bank_mask:0xf bound_ctrl:1
	v_cndmask_b32_e32 v141, v141, v154, vcc
	v_cmp_eq_u32_e32 vcc, v116, v109
	v_max_u32_dpp v105, v105, v105 row_half_mirror row_mask:0xf bank_mask:0xf bound_ctrl:1
	v_max_u32_dpp v107, v107, v107 row_half_mirror row_mask:0xf bank_mask:0xf bound_ctrl:1
	v_cndmask_b32_e32 v116, v116, v149, vcc
	v_max_u32_dpp v105, v105, v105 row_mirror row_mask:0xf bank_mask:0xf bound_ctrl:1
	v_cndmask_b32_e32 v149, v149, v157, vcc
	v_cndmask_b32_e32 v152, v157, v155, vcc
	v_cndmask_b32_e32 v153, v155, v156, vcc
	v_cndmask_b32_e32 v150, v156, v150, vcc
	v_cmp_eq_u32_e32 vcc, v135, v105
	v_max_u32_dpp v107, v107, v107 row_mirror row_mask:0xf bank_mask:0xf bound_ctrl:1
	v_cndmask_b32_e64 v154, v158, v107, s[62:63]
	v_cndmask_b32_e32 v135, v135, v136, vcc
	v_cndmask_b32_e32 v136, v136, v142, vcc
	v_cndmask_b32_e32 v142, v142, v131, vcc
	v_cndmask_b32_e32 v131, v131, v110, vcc
	v_cndmask_b32_e32 v137, v110, v137, vcc
	v_cmp_eq_u32_e32 vcc, v124, v107
	v_max_u32_dpp v107, v119, v119 quad_perm:[1,0,3,2] row_mask:0xf bank_mask:0xf bound_ctrl:1
	v_max_u32_dpp v110, v133, v133 quad_perm:[1,0,3,2] row_mask:0xf bank_mask:0xf bound_ctrl:1
	v_cndmask_b32_e32 v124, v124, v117, vcc
	v_max_u32_dpp v107, v107, v107 quad_perm:[2,3,0,1] row_mask:0xf bank_mask:0xf bound_ctrl:1
	v_cndmask_b32_e32 v155, v117, v118, vcc
	v_cndmask_b32_e32 v118, v118, v112, vcc
	v_max_u32_dpp v107, v107, v107 row_half_mirror row_mask:0xf bank_mask:0xf bound_ctrl:1
	v_cndmask_b32_e32 v113, v112, v113, vcc
	v_max_u32_dpp v110, v110, v110 quad_perm:[2,3,0,1] row_mask:0xf bank_mask:0xf bound_ctrl:1
	v_max_u32_dpp v117, v107, v107 row_mirror row_mask:0xf bank_mask:0xf bound_ctrl:1
	v_max_u32_dpp v107, v123, v123 quad_perm:[1,0,3,2] row_mask:0xf bank_mask:0xf bound_ctrl:1
	v_cmp_eq_u32_e32 vcc, v119, v117
	v_max_u32_dpp v110, v110, v110 row_half_mirror row_mask:0xf bank_mask:0xf bound_ctrl:1
	v_max_u32_dpp v107, v107, v107 quad_perm:[2,3,0,1] row_mask:0xf bank_mask:0xf bound_ctrl:1
	v_cndmask_b32_e32 v119, v119, v120, vcc
	v_cndmask_b32_e32 v120, v120, v121, vcc
	v_max_u32_dpp v107, v107, v107 row_half_mirror row_mask:0xf bank_mask:0xf bound_ctrl:1
	v_cndmask_b32_e32 v121, v121, v132, vcc
	v_cndmask_b32_e32 v122, v132, v122, vcc
	v_max_u32_dpp v112, v107, v107 row_mirror row_mask:0xf bank_mask:0xf bound_ctrl:1
	v_max_u32_dpp v107, v128, v128 quad_perm:[1,0,3,2] row_mask:0xf bank_mask:0xf bound_ctrl:1
	v_cmp_eq_u32_e32 vcc, v123, v112
	v_max_u32_dpp v110, v110, v110 row_mirror row_mask:0xf bank_mask:0xf bound_ctrl:1
	v_max_u32_dpp v107, v107, v107 quad_perm:[2,3,0,1] row_mask:0xf bank_mask:0xf bound_ctrl:1
	v_cndmask_b32_e32 v132, v123, v125, vcc
	v_cndmask_b32_e32 v125, v125, v126, vcc
	v_max_u32_dpp v107, v107, v107 row_half_mirror row_mask:0xf bank_mask:0xf bound_ctrl:1
	v_cndmask_b32_e32 v126, v126, v138, vcc
	v_cndmask_b32_e32 v127, v138, v127, vcc
	v_max_u32_dpp v107, v107, v107 row_mirror row_mask:0xf bank_mask:0xf bound_ctrl:1
	v_cmp_eq_u32_e32 vcc, v128, v107
	s_nop 1
	v_cndmask_b32_e32 v128, v128, v129, vcc
	v_cndmask_b32_e32 v129, v129, v139, vcc
	v_cndmask_b32_e32 v138, v139, v140, vcc
	v_cndmask_b32_e32 v130, v140, v130, vcc
	v_cndmask_b32_e64 v139, v115, v110, s[62:63]
	v_cmp_eq_u32_e32 vcc, v133, v110
	v_max_u32_dpp v110, v146, v146 quad_perm:[1,0,3,2] row_mask:0xf bank_mask:0xf bound_ctrl:1
	s_nop 0
	v_cndmask_b32_e32 v140, v133, v134, vcc
	v_max_u32_dpp v110, v110, v110 quad_perm:[2,3,0,1] row_mask:0xf bank_mask:0xf bound_ctrl:1
	v_max_u32_dpp v133, v124, v124 quad_perm:[1,0,3,2] row_mask:0xf bank_mask:0xf bound_ctrl:1
	v_cndmask_b32_e32 v134, v134, v143, vcc
	v_max_u32_dpp v110, v110, v110 row_half_mirror row_mask:0xf bank_mask:0xf bound_ctrl:1
	v_cndmask_b32_e32 v143, v143, v144, vcc
	v_cndmask_b32_e32 v144, v144, v145, vcc
	v_max_u32_dpp v123, v110, v110 row_mirror row_mask:0xf bank_mask:0xf bound_ctrl:1
	v_max_u32_dpp v110, v116, v116 quad_perm:[1,0,3,2] row_mask:0xf bank_mask:0xf bound_ctrl:1
	v_cmp_eq_u32_e32 vcc, v146, v123
	v_max_u32_dpp v133, v133, v133 quad_perm:[2,3,0,1] row_mask:0xf bank_mask:0xf bound_ctrl:1
	v_max_u32_dpp v110, v110, v110 quad_perm:[2,3,0,1] row_mask:0xf bank_mask:0xf bound_ctrl:1
	v_cndmask_b32_e32 v145, v146, v147, vcc
	v_cndmask_b32_e32 v146, v147, v148, vcc
	v_max_u32_dpp v110, v110, v110 row_half_mirror row_mask:0xf bank_mask:0xf bound_ctrl:1
	v_cndmask_b32_e32 v147, v148, v151, vcc
	v_cndmask_b32_e32 v141, v151, v141, vcc
	v_max_u32_dpp v115, v110, v110 row_mirror row_mask:0xf bank_mask:0xf bound_ctrl:1
	v_max_u32_dpp v110, v135, v135 quad_perm:[1,0,3,2] row_mask:0xf bank_mask:0xf bound_ctrl:1
	v_cmp_eq_u32_e32 vcc, v116, v115
	v_max_u32_dpp v133, v133, v133 row_half_mirror row_mask:0xf bank_mask:0xf bound_ctrl:1
	v_max_u32_dpp v110, v110, v110 quad_perm:[2,3,0,1] row_mask:0xf bank_mask:0xf bound_ctrl:1
	v_cndmask_b32_e32 v116, v116, v149, vcc
	v_cndmask_b32_e32 v148, v149, v152, vcc
	v_max_u32_dpp v110, v110, v110 row_half_mirror row_mask:0xf bank_mask:0xf bound_ctrl:1
	v_cndmask_b32_e32 v149, v152, v153, vcc
	v_cndmask_b32_e32 v150, v153, v150, vcc
	v_max_u32_dpp v110, v110, v110 row_mirror row_mask:0xf bank_mask:0xf bound_ctrl:1
	v_cmp_eq_u32_e32 vcc, v135, v110
	v_max_u32_dpp v133, v133, v133 row_mirror row_mask:0xf bank_mask:0xf bound_ctrl:1
	s_nop 0
	v_cndmask_b32_e32 v135, v135, v136, vcc
	v_cndmask_b32_e32 v136, v136, v142, vcc
	v_cndmask_b32_e32 v142, v142, v131, vcc
	v_cndmask_b32_e32 v131, v131, v137, vcc
	v_cmp_eq_u32_e32 vcc, v124, v133
	v_cndmask_b32_e64 v137, v154, v133, s[64:65]
	s_nop 0
	v_cndmask_b32_e32 v152, v155, v118, vcc
	v_cndmask_b32_e32 v118, v118, v113, vcc
	v_max_u32_dpp v113, v119, v119 quad_perm:[1,0,3,2] row_mask:0xf bank_mask:0xf bound_ctrl:1
	v_cndmask_b32_e32 v151, v124, v155, vcc
	v_max_u32_dpp v124, v140, v140 quad_perm:[1,0,3,2] row_mask:0xf bank_mask:0xf bound_ctrl:1
	v_max_u32_dpp v113, v113, v113 quad_perm:[2,3,0,1] row_mask:0xf bank_mask:0xf bound_ctrl:1
	v_mov_b32_e32 v155, 0
	v_max_u32_dpp v124, v124, v124 quad_perm:[2,3,0,1] row_mask:0xf bank_mask:0xf bound_ctrl:1
	v_max_u32_dpp v113, v113, v113 row_half_mirror row_mask:0xf bank_mask:0xf bound_ctrl:1
	s_nop 0
	v_max_u32_dpp v124, v124, v124 row_half_mirror row_mask:0xf bank_mask:0xf bound_ctrl:1
	v_max_u32_dpp v133, v113, v113 row_mirror row_mask:0xf bank_mask:0xf bound_ctrl:1
	v_max_u32_dpp v113, v132, v132 quad_perm:[1,0,3,2] row_mask:0xf bank_mask:0xf bound_ctrl:1
	v_cmp_eq_u32_e32 vcc, v119, v133
	v_max_u32_dpp v124, v124, v124 row_mirror row_mask:0xf bank_mask:0xf bound_ctrl:1
	v_max_u32_dpp v113, v113, v113 quad_perm:[2,3,0,1] row_mask:0xf bank_mask:0xf bound_ctrl:1
	v_cndmask_b32_e32 v119, v119, v120, vcc
	v_cndmask_b32_e32 v153, v120, v121, vcc
	v_max_u32_dpp v113, v113, v113 row_half_mirror row_mask:0xf bank_mask:0xf bound_ctrl:1
	v_cndmask_b32_e32 v121, v121, v122, vcc
	s_nop 0
	v_max_u32_dpp v120, v113, v113 row_mirror row_mask:0xf bank_mask:0xf bound_ctrl:1
	v_max_u32_dpp v113, v128, v128 quad_perm:[1,0,3,2] row_mask:0xf bank_mask:0xf bound_ctrl:1
	v_cmp_eq_u32_e32 vcc, v132, v120
	s_nop 0
	v_max_u32_dpp v113, v113, v113 quad_perm:[2,3,0,1] row_mask:0xf bank_mask:0xf bound_ctrl:1
	v_cndmask_b32_e32 v122, v132, v125, vcc
	v_cndmask_b32_e32 v125, v125, v126, vcc
	v_max_u32_dpp v113, v113, v113 row_half_mirror row_mask:0xf bank_mask:0xf bound_ctrl:1
	v_cndmask_b32_e32 v126, v126, v127, vcc
	v_max_u32_dpp v132, v151, v151 quad_perm:[1,0,3,2] row_mask:0xf bank_mask:0xf bound_ctrl:1
	v_max_u32_dpp v113, v113, v113 row_mirror row_mask:0xf bank_mask:0xf bound_ctrl:1
	v_cmp_eq_u32_e32 vcc, v128, v113
	v_max_u32_dpp v132, v132, v132 quad_perm:[2,3,0,1] row_mask:0xf bank_mask:0xf bound_ctrl:1
	s_nop 0
	v_cndmask_b32_e32 v127, v128, v129, vcc
	v_cndmask_b32_e32 v128, v129, v138, vcc
	v_cndmask_b32_e32 v129, v138, v130, vcc
	v_cndmask_b32_e64 v130, v139, v124, s[64:65]
	v_cmp_eq_u32_e32 vcc, v140, v124
	v_max_u32_dpp v124, v145, v145 quad_perm:[1,0,3,2] row_mask:0xf bank_mask:0xf bound_ctrl:1
	v_max_u32_dpp v132, v132, v132 row_half_mirror row_mask:0xf bank_mask:0xf bound_ctrl:1
	v_cndmask_b32_e32 v139, v140, v134, vcc
	v_max_u32_dpp v124, v124, v124 quad_perm:[2,3,0,1] row_mask:0xf bank_mask:0xf bound_ctrl:1
	v_cndmask_b32_e32 v134, v134, v143, vcc
	v_cndmask_b32_e32 v140, v143, v144, vcc
	v_max_u32_dpp v124, v124, v124 row_half_mirror row_mask:0xf bank_mask:0xf bound_ctrl:1
	v_max_u32_dpp v132, v132, v132 row_mirror row_mask:0xf bank_mask:0xf bound_ctrl:1
	v_cndmask_b32_e64 v137, v137, v132, s[66:67]
	v_max_u32_dpp v138, v124, v124 row_mirror row_mask:0xf bank_mask:0xf bound_ctrl:1
	v_max_u32_dpp v124, v116, v116 quad_perm:[1,0,3,2] row_mask:0xf bank_mask:0xf bound_ctrl:1
	v_cmp_eq_u32_e32 vcc, v145, v138
	s_nop 0
	v_max_u32_dpp v124, v124, v124 quad_perm:[2,3,0,1] row_mask:0xf bank_mask:0xf bound_ctrl:1
	v_cndmask_b32_e32 v144, v145, v146, vcc
	v_cndmask_b32_e32 v146, v146, v147, vcc
	v_max_u32_dpp v124, v124, v124 row_half_mirror row_mask:0xf bank_mask:0xf bound_ctrl:1
	v_cndmask_b32_e32 v141, v147, v141, vcc
	s_nop 0
	v_max_u32_dpp v124, v124, v124 row_mirror row_mask:0xf bank_mask:0xf bound_ctrl:1
	v_cmp_eq_u32_e32 vcc, v116, v124
	s_nop 1
	v_cndmask_b32_e32 v147, v116, v148, vcc
	v_max_u32_dpp v116, v135, v135 quad_perm:[1,0,3,2] row_mask:0xf bank_mask:0xf bound_ctrl:1
	v_cndmask_b32_e32 v148, v148, v149, vcc
	v_cndmask_b32_e32 v149, v149, v150, vcc
	v_max_u32_dpp v116, v116, v116 quad_perm:[2,3,0,1] row_mask:0xf bank_mask:0xf bound_ctrl:1
	s_nop 1
	v_max_u32_dpp v116, v116, v116 row_half_mirror row_mask:0xf bank_mask:0xf bound_ctrl:1
	s_nop 1
	v_max_u32_dpp v116, v116, v116 row_mirror row_mask:0xf bank_mask:0xf bound_ctrl:1
	v_cmp_eq_u32_e32 vcc, v135, v116
	s_nop 1
	v_cndmask_b32_e32 v135, v135, v136, vcc
	v_cndmask_b32_e32 v150, v136, v142, vcc
	v_cndmask_b32_e32 v131, v142, v131, vcc
	v_cmp_eq_u32_e32 vcc, v151, v132
	v_max_u32_dpp v132, v119, v119 quad_perm:[1,0,3,2] row_mask:0xf bank_mask:0xf bound_ctrl:1
	s_nop 0
	v_cndmask_b32_e32 v142, v151, v152, vcc
	v_max_u32_dpp v132, v132, v132 quad_perm:[2,3,0,1] row_mask:0xf bank_mask:0xf bound_ctrl:1
	v_cndmask_b32_e32 v118, v152, v118, vcc
	s_nop 0
	v_max_u32_dpp v132, v132, v132 row_half_mirror row_mask:0xf bank_mask:0xf bound_ctrl:1
	s_nop 1
	v_max_u32_dpp v143, v132, v132 row_mirror row_mask:0xf bank_mask:0xf bound_ctrl:1
	v_cmp_eq_u32_e32 vcc, v119, v143
	s_nop 1
	v_cndmask_b32_e32 v151, v119, v153, vcc
	v_max_u32_dpp v119, v122, v122 quad_perm:[1,0,3,2] row_mask:0xf bank_mask:0xf bound_ctrl:1
	v_cndmask_b32_e32 v121, v153, v121, vcc
	v_mov_b32_e32 v153, 0
	v_max_u32_dpp v119, v119, v119 quad_perm:[2,3,0,1] row_mask:0xf bank_mask:0xf bound_ctrl:1
	s_nop 1
	v_max_u32_dpp v119, v119, v119 row_half_mirror row_mask:0xf bank_mask:0xf bound_ctrl:1
	s_nop 1
	v_max_u32_dpp v132, v119, v119 row_mirror row_mask:0xf bank_mask:0xf bound_ctrl:1
	v_cmp_eq_u32_e32 vcc, v122, v132
	v_max_u32_dpp v119, v127, v127 quad_perm:[1,0,3,2] row_mask:0xf bank_mask:0xf bound_ctrl:1
	s_nop 0
	v_cndmask_b32_e32 v152, v122, v125, vcc
	v_max_u32_dpp v119, v119, v119 quad_perm:[2,3,0,1] row_mask:0xf bank_mask:0xf bound_ctrl:1
	v_max_u32_dpp v122, v139, v139 quad_perm:[1,0,3,2] row_mask:0xf bank_mask:0xf bound_ctrl:1
	v_cndmask_b32_e32 v125, v125, v126, vcc
	v_max_u32_dpp v119, v119, v119 row_half_mirror row_mask:0xf bank_mask:0xf bound_ctrl:1
	v_max_u32_dpp v122, v122, v122 quad_perm:[2,3,0,1] row_mask:0xf bank_mask:0xf bound_ctrl:1
	s_nop 0
	v_max_u32_dpp v119, v119, v119 row_mirror row_mask:0xf bank_mask:0xf bound_ctrl:1
	v_max_u32_dpp v122, v122, v122 row_half_mirror row_mask:0xf bank_mask:0xf bound_ctrl:1
	v_cmp_eq_u32_e32 vcc, v127, v119
	s_nop 0
	v_max_u32_dpp v122, v122, v122 row_mirror row_mask:0xf bank_mask:0xf bound_ctrl:1
	v_cndmask_b32_e32 v126, v127, v128, vcc
	v_cndmask_b32_e32 v127, v128, v129, vcc
	v_cndmask_b32_e64 v128, v130, v122, s[66:67]
	v_cmp_eq_u32_e32 vcc, v139, v122
	v_max_u32_dpp v122, v144, v144 quad_perm:[1,0,3,2] row_mask:0xf bank_mask:0xf bound_ctrl:1
	s_nop 0
	v_cndmask_b32_e32 v129, v139, v134, vcc
	v_max_u32_dpp v122, v122, v122 quad_perm:[2,3,0,1] row_mask:0xf bank_mask:0xf bound_ctrl:1
	v_cndmask_b32_e32 v130, v134, v140, vcc
	s_nop 0
	v_max_u32_dpp v122, v122, v122 row_half_mirror row_mask:0xf bank_mask:0xf bound_ctrl:1
	s_nop 1
	v_max_u32_dpp v145, v122, v122 row_mirror row_mask:0xf bank_mask:0xf bound_ctrl:1
	v_max_u32_dpp v122, v147, v147 quad_perm:[1,0,3,2] row_mask:0xf bank_mask:0xf bound_ctrl:1
	v_cmp_eq_u32_e32 vcc, v144, v145
	s_nop 0
	v_max_u32_dpp v122, v122, v122 quad_perm:[2,3,0,1] row_mask:0xf bank_mask:0xf bound_ctrl:1
	v_cndmask_b32_e32 v134, v144, v146, vcc
	v_cndmask_b32_e32 v139, v146, v141, vcc
	v_max_u32_dpp v122, v122, v122 row_half_mirror row_mask:0xf bank_mask:0xf bound_ctrl:1
	s_nop 1
	v_max_u32_dpp v136, v122, v122 row_mirror row_mask:0xf bank_mask:0xf bound_ctrl:1
	v_max_u32_dpp v122, v135, v135 quad_perm:[1,0,3,2] row_mask:0xf bank_mask:0xf bound_ctrl:1
	v_cmp_eq_u32_e32 vcc, v147, v136
	s_nop 0
	v_max_u32_dpp v122, v122, v122 quad_perm:[2,3,0,1] row_mask:0xf bank_mask:0xf bound_ctrl:1
	v_cndmask_b32_e32 v140, v147, v148, vcc
	v_cndmask_b32_e32 v141, v148, v149, vcc
	v_max_u32_dpp v122, v122, v122 row_half_mirror row_mask:0xf bank_mask:0xf bound_ctrl:1
	v_mov_b32_e32 v149, 0
	s_nop 0
	v_max_u32_dpp v122, v122, v122 row_mirror row_mask:0xf bank_mask:0xf bound_ctrl:1
	v_cmp_eq_u32_e32 vcc, v135, v122
	s_nop 1
	v_cndmask_b32_e32 v146, v135, v150, vcc
	v_max_u32_dpp v135, v142, v142 quad_perm:[1,0,3,2] row_mask:0xf bank_mask:0xf bound_ctrl:1
	v_cndmask_b32_e32 v131, v150, v131, vcc
	s_nop 0
	v_max_u32_dpp v135, v135, v135 quad_perm:[2,3,0,1] row_mask:0xf bank_mask:0xf bound_ctrl:1
	s_nop 1
	v_max_u32_dpp v135, v135, v135 row_half_mirror row_mask:0xf bank_mask:0xf bound_ctrl:1
	s_nop 1
	v_max_u32_dpp v135, v135, v135 row_mirror row_mask:0xf bank_mask:0xf bound_ctrl:1
	v_cndmask_b32_e64 v137, v137, v135, s[68:69]
	v_cmp_eq_u32_e32 vcc, v142, v135
	v_max_u32_dpp v135, v151, v151 quad_perm:[1,0,3,2] row_mask:0xf bank_mask:0xf bound_ctrl:1
	s_nop 0
	v_cndmask_b32_e32 v118, v142, v118, vcc
	v_max_u32_dpp v135, v135, v135 quad_perm:[2,3,0,1] row_mask:0xf bank_mask:0xf bound_ctrl:1
	s_nop 0
	v_max_u32_dpp v118, v118, v118 quad_perm:[1,0,3,2] row_mask:0xf bank_mask:0xf bound_ctrl:1
	v_max_u32_dpp v135, v135, v135 row_half_mirror row_mask:0xf bank_mask:0xf bound_ctrl:1
	s_nop 0
	v_max_u32_dpp v118, v118, v118 quad_perm:[2,3,0,1] row_mask:0xf bank_mask:0xf bound_ctrl:1
	v_max_u32_dpp v150, v135, v135 row_mirror row_mask:0xf bank_mask:0xf bound_ctrl:1
	v_max_u32_dpp v135, v152, v152 quad_perm:[1,0,3,2] row_mask:0xf bank_mask:0xf bound_ctrl:1
	v_cmp_eq_u32_e32 vcc, v151, v150
	v_max_u32_dpp v118, v118, v118 row_half_mirror row_mask:0xf bank_mask:0xf bound_ctrl:1
	v_max_u32_dpp v135, v135, v135 quad_perm:[2,3,0,1] row_mask:0xf bank_mask:0xf bound_ctrl:1
	v_cndmask_b32_e32 v121, v151, v121, vcc
	v_max_u32_dpp v118, v118, v118 row_mirror row_mask:0xf bank_mask:0xf bound_ctrl:1
	v_max_u32_dpp v135, v135, v135 row_half_mirror row_mask:0xf bank_mask:0xf bound_ctrl:1
	v_max_u32_dpp v121, v121, v121 quad_perm:[1,0,3,2] row_mask:0xf bank_mask:0xf bound_ctrl:1
	v_cndmask_b32_e64 v118, v137, v118, s[70:71]
	v_max_u32_dpp v142, v135, v135 row_mirror row_mask:0xf bank_mask:0xf bound_ctrl:1
	v_cmp_eq_u32_e32 vcc, v152, v142
	v_max_u32_dpp v121, v121, v121 quad_perm:[2,3,0,1] row_mask:0xf bank_mask:0xf bound_ctrl:1
	s_nop 0
	v_cndmask_b32_e32 v147, v152, v125, vcc
	v_max_u32_dpp v125, v126, v126 quad_perm:[1,0,3,2] row_mask:0xf bank_mask:0xf bound_ctrl:1
	v_max_u32_dpp v152, v121, v121 row_half_mirror row_mask:0xf bank_mask:0xf bound_ctrl:1
	v_max_u32_dpp v121, v147, v147 quad_perm:[1,0,3,2] row_mask:0xf bank_mask:0xf bound_ctrl:1
	v_max_u32_dpp v125, v125, v125 quad_perm:[2,3,0,1] row_mask:0xf bank_mask:0xf bound_ctrl:1
	v_mov_b32_e32 v147, 0
	v_max_u32_dpp v121, v121, v121 quad_perm:[2,3,0,1] row_mask:0xf bank_mask:0xf bound_ctrl:1
	v_max_u32_dpp v125, v125, v125 row_half_mirror row_mask:0xf bank_mask:0xf bound_ctrl:1
	v_mov_b32_dpp v153, v152 row_mirror row_mask:0xf bank_mask:0xf
	s_nop 0
	v_max_u32_dpp v125, v125, v125 row_mirror row_mask:0xf bank_mask:0xf bound_ctrl:1
	v_cmp_eq_u32_e32 vcc, v126, v125
	s_nop 1
	v_cndmask_b32_e32 v126, v126, v127, vcc
	v_max_u32_dpp v127, v129, v129 quad_perm:[1,0,3,2] row_mask:0xf bank_mask:0xf bound_ctrl:1
	s_nop 1
	v_max_u32_dpp v127, v127, v127 quad_perm:[2,3,0,1] row_mask:0xf bank_mask:0xf bound_ctrl:1
	s_nop 1
	v_max_u32_dpp v127, v127, v127 row_half_mirror row_mask:0xf bank_mask:0xf bound_ctrl:1
	s_nop 1
	v_max_u32_dpp v127, v127, v127 row_mirror row_mask:0xf bank_mask:0xf bound_ctrl:1
	v_cmp_eq_u32_e32 vcc, v129, v127
	v_cndmask_b32_e64 v128, v128, v127, s[68:69]
	s_nop 0
	v_cndmask_b32_e32 v127, v129, v130, vcc
	v_max_u32_dpp v129, v134, v134 quad_perm:[1,0,3,2] row_mask:0xf bank_mask:0xf bound_ctrl:1
	v_max_u32_dpp v130, v140, v140 quad_perm:[1,0,3,2] row_mask:0xf bank_mask:0xf bound_ctrl:1
	s_nop 0
	v_max_u32_dpp v129, v129, v129 quad_perm:[2,3,0,1] row_mask:0xf bank_mask:0xf bound_ctrl:1
	v_max_u32_dpp v130, v130, v130 quad_perm:[2,3,0,1] row_mask:0xf bank_mask:0xf bound_ctrl:1
	s_nop 0
	v_max_u32_dpp v129, v129, v129 row_half_mirror row_mask:0xf bank_mask:0xf bound_ctrl:1
	v_max_u32_dpp v130, v130, v130 row_half_mirror row_mask:0xf bank_mask:0xf bound_ctrl:1
	s_nop 0
	v_max_u32_dpp v151, v129, v129 row_mirror row_mask:0xf bank_mask:0xf bound_ctrl:1
	v_cmp_eq_u32_e32 vcc, v134, v151
	v_max_u32_dpp v144, v130, v130 row_mirror row_mask:0xf bank_mask:0xf bound_ctrl:1
	s_nop 0
	v_cndmask_b32_e32 v129, v134, v139, vcc
	v_max_u32_dpp v134, v146, v146 quad_perm:[1,0,3,2] row_mask:0xf bank_mask:0xf bound_ctrl:1
	v_cmp_eq_u32_e32 vcc, v140, v144
	v_mov_b32_e32 v139, 0
	v_max_u32_dpp v134, v134, v134 quad_perm:[2,3,0,1] row_mask:0xf bank_mask:0xf bound_ctrl:1
	v_cndmask_b32_e32 v130, v140, v141, vcc
	v_mov_b32_e32 v141, 0
	v_max_u32_dpp v134, v134, v134 row_half_mirror row_mask:0xf bank_mask:0xf bound_ctrl:1
	s_nop 1
	v_max_u32_dpp v135, v134, v134 row_mirror row_mask:0xf bank_mask:0xf bound_ctrl:1
	v_cmp_eq_u32_e32 vcc, v146, v135
	s_nop 1
	v_cndmask_b32_e32 v131, v146, v131, vcc
	v_max_u32_dpp v146, v121, v121 row_half_mirror row_mask:0xf bank_mask:0xf bound_ctrl:1
	v_max_u32_dpp v121, v126, v126 quad_perm:[1,0,3,2] row_mask:0xf bank_mask:0xf bound_ctrl:1
	v_max_u32_dpp v126, v129, v129 quad_perm:[1,0,3,2] row_mask:0xf bank_mask:0xf bound_ctrl:1
	v_cmp_gt_i32_e32 vcc, 0, v118
	v_max_u32_dpp v121, v121, v121 quad_perm:[2,3,0,1] row_mask:0xf bank_mask:0xf bound_ctrl:1
	v_max_u32_dpp v126, v126, v126 quad_perm:[2,3,0,1] row_mask:0xf bank_mask:0xf bound_ctrl:1
	v_mov_b32_dpp v147, v146 row_mirror row_mask:0xf bank_mask:0xf
	v_max_u32_dpp v137, v121, v121 row_half_mirror row_mask:0xf bank_mask:0xf bound_ctrl:1
	v_max_u32_dpp v121, v127, v127 quad_perm:[1,0,3,2] row_mask:0xf bank_mask:0xf bound_ctrl:1
	v_max_u32_dpp v154, v126, v126 row_half_mirror row_mask:0xf bank_mask:0xf bound_ctrl:1
	v_max_u32_dpp v126, v130, v130 quad_perm:[1,0,3,2] row_mask:0xf bank_mask:0xf bound_ctrl:1
	v_max_u32_dpp v121, v121, v121 quad_perm:[2,3,0,1] row_mask:0xf bank_mask:0xf bound_ctrl:1
	v_bitop3_b32 v127, v118, s17, v118 bitop3:0xcf
	v_max_u32_dpp v126, v126, v126 quad_perm:[2,3,0,1] row_mask:0xf bank_mask:0xf bound_ctrl:1
	v_max_u32_dpp v121, v121, v121 row_half_mirror row_mask:0xf bank_mask:0xf bound_ctrl:1
	v_mov_b32_dpp v139, v137 row_mirror row_mask:0xf bank_mask:0xf
	v_max_u32_dpp v148, v126, v126 row_half_mirror row_mask:0xf bank_mask:0xf bound_ctrl:1
	v_max_u32_dpp v126, v131, v131 quad_perm:[1,0,3,2] row_mask:0xf bank_mask:0xf bound_ctrl:1
	v_max_u32_dpp v121, v121, v121 row_mirror row_mask:0xf bank_mask:0xf bound_ctrl:1
	v_cndmask_b32_e64 v121, v128, v121, s[70:71]
	v_max_u32_dpp v126, v126, v126 quad_perm:[2,3,0,1] row_mask:0xf bank_mask:0xf bound_ctrl:1
	v_mov_b32_dpp v155, v154 row_mirror row_mask:0xf bank_mask:0xf
	v_mov_b32_dpp v149, v148 row_mirror row_mask:0xf bank_mask:0xf
	v_max_u32_dpp v140, v126, v126 row_half_mirror row_mask:0xf bank_mask:0xf bound_ctrl:1
	v_and_b32_e32 v126, 0x7fffff80, v118
	v_cndmask_b32_e32 v134, v127, v126, vcc
	v_cmp_gt_i32_e32 vcc, 0, v121
	v_and_b32_e32 v126, 0x7fffff80, v121
	v_bitop3_b32 v127, v121, s17, v121 bitop3:0xcf
	v_cndmask_b32_e32 v157, v127, v126, vcc
	ds_bpermute_b32 v130, v54, v134
	ds_bpermute_b32 v131, v55, v157
	ds_bpermute_b32 v128, v56, v134
	ds_bpermute_b32 v129, v57, v157
	ds_bpermute_b32 v126, v61, v134
	ds_bpermute_b32 v127, v62, v157
	ds_bpermute_b32 v156, v59, v134
	ds_bpermute_b32 v157, v54, v157
	v_mov_b32_dpp v141, v140 row_mirror row_mask:0xf bank_mask:0xf
	v_mov_b32_e32 v134, 0
	s_and_saveexec_b64 s[6:7], s[40:41]
	s_cbranch_execz .LBB0_3017
	s_waitcnt lgkmcnt(0)
	v_add_f32_e32 v134, v156, v157
	v_ashrrev_i32_e32 v156, 31, v134
	v_bitop3_b32 v134, v156, v134, s95 bitop3:0x36
	s_movk_i32 s10, 0xff00
	v_and_or_b32 v134, v134, s10, v60
